# speedup vs baseline: 1.0112x; 1.0013x over previous
.Lrs_b_4:
	v_med3_f32 v166, v18, v160, 0
	v_med3_f32 v165, v19, v160, 0
	v_med3_f32 v167, v20, v160, 0
	v_med3_f32 v168, v21, v160, 0
	v_cvt_scalef32_pk_fp4_f32 v166, v166, v165, v159
	v_med3_f32 v169, v22, v160, 0
	v_med3_f32 v170, v23, v160, 0
	v_cvt_scalef32_pk_fp4_f32 v166, v167, v168, v159 op_sel:[0,0,1,0]
	v_med3_f32 v167, v50, v160, 0
	v_med3_f32 v165, v51, v160, 0
	v_med3_f32 v171, v24, v160, 0
	v_med3_f32 v172, v25, v160, 0
	v_cvt_scalef32_pk_fp4_f32 v166, v169, v170, v159 op_sel:[0,0,0,1]
	v_med3_f32 v168, v52, v160, 0
	v_med3_f32 v169, v53, v160, 0
	v_cvt_scalef32_pk_fp4_f32 v167, v167, v165, v159
	v_cvt_scalef32_pk_fp4_f32 v166, v171, v172, v159 op_sel:[0,0,1,1]
	v_med3_f32 v170, v54, v160, 0
	v_med3_f32 v171, v55, v160, 0
	v_cvt_scalef32_pk_fp4_f32 v167, v168, v169, v159 op_sel:[0,0,1,0]
	v_med3_f32 v168, v26, v160, 0
	v_med3_f32 v165, v27, v160, 0
	v_med3_f32 v172, v56, v160, 0
	v_med3_f32 v173, v57, v160, 0
	v_cvt_scalef32_pk_fp4_f32 v167, v170, v171, v159 op_sel:[0,0,0,1]
	v_med3_f32 v169, v28, v160, 0
	v_med3_f32 v170, v29, v160, 0
	v_cvt_scalef32_pk_fp4_f32 v168, v168, v165, v159
	v_cvt_scalef32_pk_fp4_f32 v167, v172, v173, v159 op_sel:[0,0,1,1]
	v_med3_f32 v171, v30, v160, 0
	v_med3_f32 v172, v31, v160, 0
	v_cvt_scalef32_pk_fp4_f32 v168, v169, v170, v159 op_sel:[0,0,1,0]
	v_med3_f32 v169, v58, v160, 0
	v_med3_f32 v165, v59, v160, 0
	v_med3_f32 v173, v32, v160, 0
	v_med3_f32 v174, v33, v160, 0
	v_cvt_scalef32_pk_fp4_f32 v168, v171, v172, v159 op_sel:[0,0,0,1]
	v_med3_f32 v170, v60, v160, 0
	v_med3_f32 v171, v61, v160, 0
	v_cvt_scalef32_pk_fp4_f32 v169, v169, v165, v159
	v_lshl_add_u32 v1, s77, 8, v149
	v_lshl_or_b32 v156, s76, 8, v151
	v_cvt_scalef32_pk_fp4_f32 v168, v173, v174, v159 op_sel:[0,0,1,1]
	v_med3_f32 v172, v62, v160, 0
	v_med3_f32 v173, v63, v160, 0
	v_cvt_scalef32_pk_fp4_f32 v169, v170, v171, v159 op_sel:[0,0,1,0]
	v_ashrrev_i32_e32 v156, 1, v156
	v_med3_f32 v174, v64, v160, 0
	v_med3_f32 v175, v65, v160, 0
	v_cvt_scalef32_pk_fp4_f32 v169, v172, v173, v159 op_sel:[0,0,0,1]
	v_or_b32_e32 v165, v1, v153
	v_mov_b64_e32 v[170:171], s[8:9]
	v_ashrrev_i32_e32 v157, 31, v156
	v_cvt_scalef32_pk_fp4_f32 v169, v174, v175, v159 op_sel:[0,0,1,1]
	v_mad_i64_i32 v[172:173], s[38:39], v165, s12, v[170:171]
	v_permlane16_swap_b32_e32 v166, v168
	v_permlane16_swap_b32_e32 v167, v169
	v_lshl_add_u64 v[172:173], v[172:173], 0, v[156:157]
	global_store_dwordx4 v[172:173], v[166:169], off
	v_med3_f32 v165, v35, v160, 0
	v_med3_f32 v172, v39, v160, 0
	v_med3_f32 v166, v34, v160, 0
	v_med3_f32 v167, v36, v160, 0
	v_med3_f32 v168, v37, v160, 0
	v_cvt_scalef32_pk_fp4_f32 v166, v166, v165, v159
	v_med3_f32 v169, v38, v160, 0
	v_cvt_scalef32_pk_fp4_f32 v166, v167, v168, v159 op_sel:[0,0,1,0]
	v_med3_f32 v167, v66, v160, 0
	v_med3_f32 v165, v67, v160, 0
	v_med3_f32 v173, v40, v160, 0
	v_med3_f32 v174, v41, v160, 0
	v_cvt_scalef32_pk_fp4_f32 v166, v169, v172, v159 op_sel:[0,0,0,1]
	v_med3_f32 v168, v68, v160, 0
	v_med3_f32 v169, v69, v160, 0
	v_cvt_scalef32_pk_fp4_f32 v167, v167, v165, v159
	v_cvt_scalef32_pk_fp4_f32 v166, v173, v174, v159 op_sel:[0,0,1,1]
	v_med3_f32 v172, v70, v160, 0
	v_med3_f32 v173, v71, v160, 0
	v_cvt_scalef32_pk_fp4_f32 v167, v168, v169, v159 op_sel:[0,0,1,0]
	v_med3_f32 v168, v42, v160, 0
	v_med3_f32 v165, v43, v160, 0
	v_med3_f32 v174, v72, v160, 0
	v_med3_f32 v175, v73, v160, 0
	v_cvt_scalef32_pk_fp4_f32 v167, v172, v173, v159 op_sel:[0,0,0,1]
	v_med3_f32 v169, v44, v160, 0
	v_med3_f32 v172, v45, v160, 0
	v_cvt_scalef32_pk_fp4_f32 v168, v168, v165, v159
	v_cvt_scalef32_pk_fp4_f32 v167, v174, v175, v159 op_sel:[0,0,1,1]
	v_med3_f32 v173, v46, v160, 0
	v_med3_f32 v174, v47, v160, 0
	v_cvt_scalef32_pk_fp4_f32 v168, v169, v172, v159 op_sel:[0,0,1,0]
	v_med3_f32 v169, v74, v160, 0
	v_med3_f32 v165, v75, v160, 0
	v_med3_f32 v175, v48, v160, 0
	v_med3_f32 v176, v49, v160, 0
	v_cvt_scalef32_pk_fp4_f32 v168, v173, v174, v159 op_sel:[0,0,0,1]
	v_med3_f32 v172, v76, v160, 0
	v_med3_f32 v173, v77, v160, 0
	v_cvt_scalef32_pk_fp4_f32 v169, v169, v165, v159
	v_cvt_scalef32_pk_fp4_f32 v168, v175, v176, v159 op_sel:[0,0,1,1]
	v_med3_f32 v174, v78, v160, 0
	v_med3_f32 v175, v79, v160, 0
	v_cvt_scalef32_pk_fp4_f32 v169, v172, v173, v159 op_sel:[0,0,1,0]
	v_med3_f32 v176, v80, v160, 0
	v_med3_f32 v177, v81, v160, 0
	v_cvt_scalef32_pk_fp4_f32 v169, v174, v175, v159 op_sel:[0,0,0,1]
	v_or_b32_e32 v165, v1, v158
	v_cvt_scalef32_pk_fp4_f32 v169, v176, v177, v159 op_sel:[0,0,1,1]
	v_mad_i64_i32 v[172:173], s[38:39], v165, s12, v[170:171]
	v_permlane16_swap_b32_e32 v166, v168
	v_permlane16_swap_b32_e32 v167, v169
	v_lshl_add_u64 v[172:173], v[172:173], 0, v[156:157]
	global_store_dwordx4 v[172:173], v[166:169], off
	s_branch .Lep_g3_4

.Lep_rs_4:
	v_mov_b32_e32 v1, v244
	v_mov_b32_e32 v156, v246
	v_mov_b32_e32 v157, v247
	v_mov_b64_e32 v[170:171], s[8:9]
.Lep_g3_4:
	v_med3_f32 v165, v87, v160, 0
	v_med3_f32 v172, v91, v160, 0
	v_med3_f32 v166, v86, v160, 0
	v_med3_f32 v167, v88, v160, 0
	v_med3_f32 v168, v89, v160, 0
	v_cvt_scalef32_pk_fp4_f32 v166, v166, v165, v159
	v_med3_f32 v169, v90, v160, 0
	v_cvt_scalef32_pk_fp4_f32 v166, v167, v168, v159 op_sel:[0,0,1,0]
	v_med3_f32 v167, v94, v160, 0
	v_med3_f32 v165, v95, v160, 0
	v_med3_f32 v173, v92, v160, 0
	v_med3_f32 v174, v93, v160, 0
	v_cvt_scalef32_pk_fp4_f32 v166, v169, v172, v159 op_sel:[0,0,0,1]
	v_med3_f32 v168, v96, v160, 0
	v_med3_f32 v169, v97, v160, 0
	v_cvt_scalef32_pk_fp4_f32 v167, v167, v165, v159
	v_cvt_scalef32_pk_fp4_f32 v166, v173, v174, v159 op_sel:[0,0,1,1]
	v_med3_f32 v172, v102, v160, 0
	v_med3_f32 v173, v103, v160, 0
	v_cvt_scalef32_pk_fp4_f32 v167, v168, v169, v159 op_sel:[0,0,1,0]
	v_med3_f32 v168, v98, v160, 0
	v_med3_f32 v165, v99, v160, 0
	v_med3_f32 v174, v104, v160, 0
	v_med3_f32 v175, v105, v160, 0
	v_cvt_scalef32_pk_fp4_f32 v167, v172, v173, v159 op_sel:[0,0,0,1]
	v_med3_f32 v169, v100, v160, 0
	v_med3_f32 v172, v101, v160, 0
	v_cvt_scalef32_pk_fp4_f32 v168, v168, v165, v159
	v_cvt_scalef32_pk_fp4_f32 v167, v174, v175, v159 op_sel:[0,0,1,1]
	v_med3_f32 v173, v106, v160, 0
	v_med3_f32 v174, v107, v160, 0
	v_cvt_scalef32_pk_fp4_f32 v168, v169, v172, v159 op_sel:[0,0,1,0]
	v_med3_f32 v169, v110, v160, 0
	v_med3_f32 v165, v111, v160, 0
	v_med3_f32 v175, v108, v160, 0
	v_med3_f32 v176, v109, v160, 0
	v_cvt_scalef32_pk_fp4_f32 v168, v173, v174, v159 op_sel:[0,0,0,1]
	v_med3_f32 v172, v112, v160, 0
	v_med3_f32 v173, v113, v160, 0
	v_cvt_scalef32_pk_fp4_f32 v169, v169, v165, v159
	v_add_u32_e32 v1, 0x80, v1
	v_cvt_scalef32_pk_fp4_f32 v168, v175, v176, v159 op_sel:[0,0,1,1]
	v_med3_f32 v174, v114, v160, 0
	v_med3_f32 v175, v115, v160, 0
	v_cvt_scalef32_pk_fp4_f32 v169, v172, v173, v159 op_sel:[0,0,1,0]
	v_med3_f32 v176, v116, v160, 0
	v_med3_f32 v177, v117, v160, 0
	v_cvt_scalef32_pk_fp4_f32 v169, v174, v175, v159 op_sel:[0,0,0,1]
	v_or_b32_e32 v165, v1, v153
	v_cvt_scalef32_pk_fp4_f32 v169, v176, v177, v159 op_sel:[0,0,1,1]
	v_mad_i64_i32 v[172:173], s[38:39], v165, s12, v[170:171]
	v_permlane16_swap_b32_e32 v166, v168
	v_permlane16_swap_b32_e32 v167, v169
	v_lshl_add_u64 v[172:173], v[172:173], 0, v[156:157]
	global_store_dwordx4 v[172:173], v[166:169], off
	v_med3_f32 v165, v119, v160, 0
	v_med3_f32 v172, v127, v160, 0
	v_med3_f32 v166, v118, v160, 0
	v_med3_f32 v167, v120, v160, 0
	v_med3_f32 v168, v121, v160, 0
	v_cvt_scalef32_pk_fp4_f32 v166, v166, v165, v159
	v_med3_f32 v169, v126, v160, 0
	v_cvt_scalef32_pk_fp4_f32 v166, v167, v168, v159 op_sel:[0,0,1,0]
	v_med3_f32 v167, v122, v160, 0
	v_med3_f32 v165, v123, v160, 0
	v_med3_f32 v173, v128, v160, 0
	v_med3_f32 v174, v129, v160, 0
	v_cvt_scalef32_pk_fp4_f32 v166, v169, v172, v159 op_sel:[0,0,0,1]
	v_med3_f32 v168, v124, v160, 0
	v_med3_f32 v169, v125, v160, 0
	v_cvt_scalef32_pk_fp4_f32 v167, v167, v165, v159
	v_cvt_scalef32_pk_fp4_f32 v166, v173, v174, v159 op_sel:[0,0,1,1]
	v_med3_f32 v172, v130, v160, 0
	v_med3_f32 v173, v131, v160, 0
	v_cvt_scalef32_pk_fp4_f32 v167, v168, v169, v159 op_sel:[0,0,1,0]
	v_med3_f32 v168, v138, v160, 0
	v_med3_f32 v165, v139, v160, 0
	v_med3_f32 v174, v132, v160, 0
	v_med3_f32 v175, v133, v160, 0
	v_cvt_scalef32_pk_fp4_f32 v167, v172, v173, v159 op_sel:[0,0,0,1]
	v_med3_f32 v169, v140, v160, 0
	v_med3_f32 v172, v141, v160, 0
	v_cvt_scalef32_pk_fp4_f32 v168, v168, v165, v159
	v_cvt_scalef32_pk_fp4_f32 v167, v174, v175, v159 op_sel:[0,0,1,1]
	v_med3_f32 v173, v82, v160, 0
	v_med3_f32 v174, v83, v160, 0
	v_cvt_scalef32_pk_fp4_f32 v168, v169, v172, v159 op_sel:[0,0,1,0]
	v_med3_f32 v169, v134, v160, 0
	v_med3_f32 v165, v135, v160, 0
	v_med3_f32 v175, v84, v160, 0
	v_med3_f32 v176, v85, v160, 0
	v_cvt_scalef32_pk_fp4_f32 v168, v173, v174, v159 op_sel:[0,0,0,1]
	v_med3_f32 v172, v136, v160, 0
	v_med3_f32 v173, v137, v160, 0
	v_cvt_scalef32_pk_fp4_f32 v169, v169, v165, v159
	v_cvt_scalef32_pk_fp4_f32 v168, v175, v176, v159 op_sel:[0,0,1,1]
	v_med3_f32 v174, v142, v160, 0
	v_med3_f32 v175, v143, v160, 0
	v_cvt_scalef32_pk_fp4_f32 v169, v172, v173, v159 op_sel:[0,0,1,0]
	v_med3_f32 v176, v144, v160, 0
	v_med3_f32 v177, v145, v160, 0
	v_cvt_scalef32_pk_fp4_f32 v169, v174, v175, v159 op_sel:[0,0,0,1]
	v_or_b32_e32 v1, v1, v158
	v_cvt_scalef32_pk_fp4_f32 v169, v176, v177, v159 op_sel:[0,0,1,1]
	v_mad_i64_i32 v[170:171], s[38:39], v1, s12, v[170:171]
	v_permlane16_swap_b32_e32 v166, v168
	v_permlane16_swap_b32_e32 v167, v169
	v_lshl_add_u64 v[156:157], v[170:171], 0, v[156:157]
	s_mov_b32 s76, s13
	s_mov_b32 s77, s74
	s_mov_b64 s[38:39], s[4:5]
	s_mov_b64 s[40:41], s[36:37]
	s_mov_b64 vcc, s[0:1]
	global_store_dwordx4 v[156:157], v[166:169], off
	s_cbranch_vccnz .LBB4_17

.Lrs_a_4:
	s_add_u32 s81, s40, s22
	s_addc_u32 s82, s41, s23
	s_add_u32 s29, s40, 0x100
	s_addc_u32 s44, s41, 0
	s_and_b64 s[42:43], s[14:15], exec
	ds_read_b128 v[82:85], v161
	ds_read_b128 v[94:97], v161 offset:2048
	ds_read_b128 v[102:105], v162
	ds_read_b128 v[110:113], v162 offset:2048
	s_cselect_b32 s47, s37, s44
	s_cselect_b32 s46, s36, s29
	s_add_u32 s29, s38, 0x100
	s_addc_u32 s44, s39, 0
	s_and_b64 s[42:43], s[14:15], exec
	s_cselect_b32 s49, s5, s44
	s_cselect_b32 s48, s4, s29
	s_add_u32 s44, s46, 0x80
	s_addc_u32 s45, s47, 0
	s_add_u32 s42, s48, 0x80
	s_addc_u32 s43, s49, 0
	ds_read_b128 v[58:61], v163
	ds_read_b128 v[66:69], v163 offset:2048
	ds_read_b128 v[62:65], v164
	ds_read_b128 v[70:73], v164 offset:2048
	ds_read_b128 v[74:77], v163 offset:4096
	ds_read_b128 v[86:89], v163 offset:6144
	ds_read_b128 v[78:81], v164 offset:4096
	ds_read_b128 v[90:93], v164 offset:6144
	s_add_u32 s78, s81, 0x80
	s_addc_u32 s79, s82, 0
	s_mov_b32 m0, s70
	s_nop 0
	global_load_lds_dwordx4 v146, s[78:79]
	s_mov_b32 m0, s71
	s_nop 0
	global_load_lds_dwordx4 v150, s[78:79]
	s_waitcnt lgkmcnt(8)
	ds_read_b128 v[142:145], v161 offset:16384
	ds_read_b128 v[166:169], v161 offset:18432
	ds_read_b128 v[170:173], v162 offset:16384
	ds_read_b128 v[174:177], v162 offset:18432
	s_waitcnt vmcnt(8)
	s_waitcnt lgkmcnt(0)
	s_barrier
	s_waitcnt lgkmcnt(0)
	s_waitcnt vmcnt(16)
	v_mov_b32_e32 v1, v0
	v_pk_mul_f32 v[16:17], v[0:1], v[16:17]
	v_pk_mul_f32 v[14:15], v[154:155], v[14:15]
	v_pk_mul_f32 v[12:13], v[0:1], v[12:13]
	v_pk_mul_f32 v[10:11], v[154:155], v[10:11]
	v_pk_mul_f32 v[8:9], v[0:1], v[8:9]
	v_pk_mul_f32 v[6:7], v[154:155], v[6:7]
	v_pk_mul_f32 v[4:5], v[0:1], v[4:5]
	v_pk_mul_f32 v[2:3], v[154:155], v[2:3]
	s_setprio 1
	v_mfma_f32_16x16x128_f8f6f4 v[18:21], v[82:85], v[58:61], v[14:17] cbsz:4 blgp:4
	v_mfma_f32_16x16x128_f8f6f4 v[18:21], v[102:105], v[62:65], v[18:21] cbsz:4 blgp:4
	v_mfma_f32_16x16x128_f8f6f4 v[22:25], v[94:97], v[58:61], v[10:13] cbsz:4 blgp:4
	v_mfma_f32_16x16x128_f8f6f4 v[22:25], v[110:113], v[62:65], v[22:25] cbsz:4 blgp:4
	v_mfma_f32_16x16x128_f8f6f4 v[50:53], v[142:145], v[58:61], v[6:9] cbsz:4 blgp:4
	v_mfma_f32_16x16x128_f8f6f4 v[50:53], v[170:173], v[62:65], v[50:53] cbsz:4 blgp:4
	v_mfma_f32_16x16x128_f8f6f4 v[54:57], v[166:169], v[58:61], v[2:5] cbsz:4 blgp:4
	v_mfma_f32_16x16x128_f8f6f4 v[54:57], v[174:177], v[62:65], v[54:57] cbsz:4 blgp:4
	v_mfma_f32_16x16x128_f8f6f4 v[26:29], v[82:85], v[66:69], v[14:17] cbsz:4 blgp:4
	v_mfma_f32_16x16x128_f8f6f4 v[26:29], v[102:105], v[70:73], v[26:29] cbsz:4 blgp:4
	v_mfma_f32_16x16x128_f8f6f4 v[30:33], v[94:97], v[66:69], v[10:13] cbsz:4 blgp:4
	v_mfma_f32_16x16x128_f8f6f4 v[30:33], v[110:113], v[70:73], v[30:33] cbsz:4 blgp:4
	v_mfma_f32_16x16x128_f8f6f4 v[58:61], v[142:145], v[66:69], v[6:9] cbsz:4 blgp:4
	v_mfma_f32_16x16x128_f8f6f4 v[58:61], v[170:173], v[70:73], v[58:61] cbsz:4 blgp:4
	v_mfma_f32_16x16x128_f8f6f4 v[62:65], v[166:169], v[66:69], v[2:5] cbsz:4 blgp:4
	v_mfma_f32_16x16x128_f8f6f4 v[62:65], v[174:177], v[70:73], v[62:65] cbsz:4 blgp:4
	v_mfma_f32_16x16x128_f8f6f4 v[34:37], v[82:85], v[74:77], v[14:17] cbsz:4 blgp:4
	v_mfma_f32_16x16x128_f8f6f4 v[34:37], v[102:105], v[78:81], v[34:37] cbsz:4 blgp:4
	v_mfma_f32_16x16x128_f8f6f4 v[38:41], v[94:97], v[74:77], v[10:13] cbsz:4 blgp:4
	v_mfma_f32_16x16x128_f8f6f4 v[38:41], v[110:113], v[78:81], v[38:41] cbsz:4 blgp:4
	v_mfma_f32_16x16x128_f8f6f4 v[66:69], v[142:145], v[74:77], v[6:9] cbsz:4 blgp:4
	v_mfma_f32_16x16x128_f8f6f4 v[66:69], v[170:173], v[78:81], v[66:69] cbsz:4 blgp:4
	v_mfma_f32_16x16x128_f8f6f4 v[70:73], v[166:169], v[74:77], v[2:5] cbsz:4 blgp:4
	v_mfma_f32_16x16x128_f8f6f4 v[70:73], v[174:177], v[78:81], v[70:73] cbsz:4 blgp:4
	v_mfma_f32_16x16x128_f8f6f4 v[42:45], v[82:85], v[86:89], v[14:17] cbsz:4 blgp:4
	v_mfma_f32_16x16x128_f8f6f4 v[42:45], v[102:105], v[90:93], v[42:45] cbsz:4 blgp:4
	v_mfma_f32_16x16x128_f8f6f4 v[46:49], v[94:97], v[86:89], v[10:13] cbsz:4 blgp:4
	v_mfma_f32_16x16x128_f8f6f4 v[46:49], v[110:113], v[90:93], v[46:49] cbsz:4 blgp:4
	v_mfma_f32_16x16x128_f8f6f4 v[74:77], v[142:145], v[86:89], v[6:9] cbsz:4 blgp:4
	v_mfma_f32_16x16x128_f8f6f4 v[74:77], v[170:173], v[90:93], v[74:77] cbsz:4 blgp:4
	v_mfma_f32_16x16x128_f8f6f4 v[78:81], v[166:169], v[86:89], v[2:5] cbsz:4 blgp:4
	v_mfma_f32_16x16x128_f8f6f4 v[78:81], v[174:177], v[90:93], v[78:81] cbsz:4 blgp:4
	s_setprio 0
	s_barrier
	s_mov_b32 m0, s55
	s_nop 0
	global_load_lds_dwordx4 v148, s[48:49]
	s_mov_b32 m0, s56
	s_nop 0
	global_load_lds_dwordx4 v152, s[48:49]
	ds_read_b128 v[114:117], v163 offset:16384
	ds_read_b128 v[122:125], v163 offset:18432
	ds_read_b128 v[130:133], v164 offset:16384
	ds_read_b128 v[134:137], v164 offset:18432
	ds_read_b128 v[178:181], v163 offset:20480
	ds_read_b128 v[182:185], v163 offset:22528
	ds_read_b128 v[186:189], v164 offset:20480
	ds_read_b128 v[190:193], v164 offset:22528
	s_mov_b32 m0, s54
	s_nop 0
	global_load_lds_dwordx4 v146, s[46:47]
	s_mov_b32 m0, s57
	s_nop 0
	global_load_lds_dwordx4 v150, s[46:47]
	s_add_u32 s48, s48, s24
	s_addc_u32 s49, s49, s25
	s_mov_b32 m0, s58
	s_nop 0
	global_load_lds_dwordx4 v148, s[48:49]
	s_mov_b32 m0, s59
	s_nop 0
	global_load_lds_dwordx4 v152, s[48:49]
	s_waitcnt vmcnt(8)
	s_waitcnt lgkmcnt(0)
	s_barrier
	s_setprio 1
	v_mfma_f32_16x16x128_f8f6f4 v[86:89], v[82:85], v[114:117], v[14:17] cbsz:4 blgp:4
	v_mfma_f32_16x16x128_f8f6f4 v[86:89], v[102:105], v[130:133], v[86:89] cbsz:4 blgp:4
	v_mfma_f32_16x16x128_f8f6f4 v[90:93], v[94:97], v[114:117], v[10:13] cbsz:4 blgp:4
	v_mfma_f32_16x16x128_f8f6f4 v[90:93], v[110:113], v[130:133], v[90:93] cbsz:4 blgp:4
	v_mfma_f32_16x16x128_f8f6f4 v[98:101], v[82:85], v[122:125], v[14:17] cbsz:4 blgp:4
	v_mfma_f32_16x16x128_f8f6f4 v[98:101], v[102:105], v[134:137], v[98:101] cbsz:4 blgp:4
	v_mfma_f32_16x16x128_f8f6f4 v[106:109], v[94:97], v[122:125], v[10:13] cbsz:4 blgp:4
	v_mfma_f32_16x16x128_f8f6f4 v[106:109], v[110:113], v[134:137], v[106:109] cbsz:4 blgp:4
	v_mfma_f32_16x16x128_f8f6f4 v[118:121], v[82:85], v[178:181], v[14:17] cbsz:4 blgp:4
	v_mfma_f32_16x16x128_f8f6f4 v[118:121], v[102:105], v[186:189], v[118:121] cbsz:4 blgp:4
	v_mfma_f32_16x16x128_f8f6f4 v[126:129], v[94:97], v[178:181], v[10:13] cbsz:4 blgp:4
	v_mfma_f32_16x16x128_f8f6f4 v[126:129], v[110:113], v[186:189], v[126:129] cbsz:4 blgp:4
	v_mfma_f32_16x16x128_f8f6f4 v[138:141], v[82:85], v[182:185], v[14:17] cbsz:4 blgp:4
	v_mfma_f32_16x16x128_f8f6f4 v[138:141], v[102:105], v[190:193], v[138:141] cbsz:4 blgp:4
	v_mfma_f32_16x16x128_f8f6f4 v[82:85], v[94:97], v[182:185], v[10:13] cbsz:4 blgp:4
	v_mfma_f32_16x16x128_f8f6f4 v[82:85], v[110:113], v[190:193], v[82:85] cbsz:4 blgp:4
	v_mfma_f32_16x16x128_f8f6f4 v[94:97], v[142:145], v[114:117], v[6:9] cbsz:4 blgp:4
	v_mfma_f32_16x16x128_f8f6f4 v[94:97], v[170:173], v[130:133], v[94:97] cbsz:4 blgp:4
	v_mfma_f32_16x16x128_f8f6f4 v[102:105], v[166:169], v[114:117], v[2:5] cbsz:4 blgp:4
	v_mfma_f32_16x16x128_f8f6f4 v[102:105], v[174:177], v[130:133], v[102:105] cbsz:4 blgp:4
	v_mfma_f32_16x16x128_f8f6f4 v[110:113], v[142:145], v[122:125], v[6:9] cbsz:4 blgp:4
	v_mfma_f32_16x16x128_f8f6f4 v[110:113], v[170:173], v[134:137], v[110:113] cbsz:4 blgp:4
	v_mfma_f32_16x16x128_f8f6f4 v[114:117], v[166:169], v[122:125], v[2:5] cbsz:4 blgp:4
	v_mfma_f32_16x16x128_f8f6f4 v[114:117], v[174:177], v[134:137], v[114:117] cbsz:4 blgp:4
	v_mfma_f32_16x16x128_f8f6f4 v[122:125], v[142:145], v[178:181], v[6:9] cbsz:4 blgp:4
	v_mfma_f32_16x16x128_f8f6f4 v[122:125], v[170:173], v[186:189], v[122:125] cbsz:4 blgp:4
	v_mfma_f32_16x16x128_f8f6f4 v[130:133], v[166:169], v[178:181], v[2:5] cbsz:4 blgp:4
	v_mfma_f32_16x16x128_f8f6f4 v[130:133], v[174:177], v[186:189], v[130:133] cbsz:4 blgp:4
	v_mfma_f32_16x16x128_f8f6f4 v[134:137], v[142:145], v[182:185], v[6:9] cbsz:4 blgp:4
	v_mfma_f32_16x16x128_f8f6f4 v[134:137], v[170:173], v[190:193], v[134:137] cbsz:4 blgp:4
	v_mfma_f32_16x16x128_f8f6f4 v[142:145], v[166:169], v[182:185], v[2:5] cbsz:4 blgp:4
	v_mfma_f32_16x16x128_f8f6f4 v[142:145], v[174:177], v[190:193], v[142:145] cbsz:4 blgp:4
	s_setprio 0
	s_barrier
	ds_read_b128 v[166:169], v161 offset:32768
	ds_read_b128 v[170:173], v161 offset:34816
	ds_read_b128 v[174:177], v162 offset:32768
	ds_read_b128 v[178:181], v162 offset:34816
	ds_read_b128 v[182:185], v163 offset:32768
	ds_read_b128 v[186:189], v163 offset:34816
	ds_read_b128 v[190:193], v164 offset:32768
	ds_read_b128 v[194:197], v164 offset:34816
	ds_read_b128 v[198:201], v163 offset:36864
	ds_read_b128 v[202:205], v163 offset:38912
	ds_read_b128 v[206:209], v164 offset:36864
	ds_read_b128 v[210:213], v164 offset:38912
	s_add_u32 s46, s46, s22
	s_addc_u32 s47, s47, s23
	s_mov_b32 m0, s60
	s_nop 0
	global_load_lds_dwordx4 v146, s[46:47]
	s_mov_b32 m0, s61
	s_nop 0
	global_load_lds_dwordx4 v150, s[46:47]
	s_waitcnt lgkmcnt(8)
	ds_read_b128 v[214:217], v161 offset:49152
	ds_read_b128 v[218:221], v161 offset:51200
	ds_read_b128 v[222:225], v162 offset:49152
	ds_read_b128 v[226:229], v162 offset:51200
	s_waitcnt vmcnt(8)
	s_waitcnt lgkmcnt(0)
	s_barrier
	s_waitcnt lgkmcnt(0)
	s_setprio 1
	v_mfma_f32_16x16x128_f8f6f4 v[18:21], v[166:169], v[182:185], v[18:21] cbsz:4 blgp:4
	v_mfma_f32_16x16x128_f8f6f4 v[18:21], v[174:177], v[190:193], v[18:21] cbsz:4 blgp:4
	v_mfma_f32_16x16x128_f8f6f4 v[22:25], v[170:173], v[182:185], v[22:25] cbsz:4 blgp:4
	v_mfma_f32_16x16x128_f8f6f4 v[22:25], v[178:181], v[190:193], v[22:25] cbsz:4 blgp:4
	v_mfma_f32_16x16x128_f8f6f4 v[50:53], v[214:217], v[182:185], v[50:53] cbsz:4 blgp:4
	v_mfma_f32_16x16x128_f8f6f4 v[50:53], v[222:225], v[190:193], v[50:53] cbsz:4 blgp:4
	v_mfma_f32_16x16x128_f8f6f4 v[54:57], v[218:221], v[182:185], v[54:57] cbsz:4 blgp:4
	v_mfma_f32_16x16x128_f8f6f4 v[54:57], v[226:229], v[190:193], v[54:57] cbsz:4 blgp:4
	v_mfma_f32_16x16x128_f8f6f4 v[26:29], v[166:169], v[186:189], v[26:29] cbsz:4 blgp:4
	v_mfma_f32_16x16x128_f8f6f4 v[26:29], v[174:177], v[194:197], v[26:29] cbsz:4 blgp:4
	v_mfma_f32_16x16x128_f8f6f4 v[30:33], v[170:173], v[186:189], v[30:33] cbsz:4 blgp:4
	v_mfma_f32_16x16x128_f8f6f4 v[30:33], v[178:181], v[194:197], v[30:33] cbsz:4 blgp:4
	v_mfma_f32_16x16x128_f8f6f4 v[58:61], v[214:217], v[186:189], v[58:61] cbsz:4 blgp:4
	v_mfma_f32_16x16x128_f8f6f4 v[58:61], v[222:225], v[194:197], v[58:61] cbsz:4 blgp:4
	v_mfma_f32_16x16x128_f8f6f4 v[62:65], v[218:221], v[186:189], v[62:65] cbsz:4 blgp:4
	v_mfma_f32_16x16x128_f8f6f4 v[62:65], v[226:229], v[194:197], v[62:65] cbsz:4 blgp:4
	v_mfma_f32_16x16x128_f8f6f4 v[34:37], v[166:169], v[198:201], v[34:37] cbsz:4 blgp:4
	v_mfma_f32_16x16x128_f8f6f4 v[34:37], v[174:177], v[206:209], v[34:37] cbsz:4 blgp:4
	v_mfma_f32_16x16x128_f8f6f4 v[38:41], v[170:173], v[198:201], v[38:41] cbsz:4 blgp:4
	v_mfma_f32_16x16x128_f8f6f4 v[38:41], v[178:181], v[206:209], v[38:41] cbsz:4 blgp:4
	v_mfma_f32_16x16x128_f8f6f4 v[66:69], v[214:217], v[198:201], v[66:69] cbsz:4 blgp:4
	v_mfma_f32_16x16x128_f8f6f4 v[66:69], v[222:225], v[206:209], v[66:69] cbsz:4 blgp:4
	v_mfma_f32_16x16x128_f8f6f4 v[70:73], v[218:221], v[198:201], v[70:73] cbsz:4 blgp:4
	v_mfma_f32_16x16x128_f8f6f4 v[70:73], v[226:229], v[206:209], v[70:73] cbsz:4 blgp:4
	v_mfma_f32_16x16x128_f8f6f4 v[42:45], v[166:169], v[202:205], v[42:45] cbsz:4 blgp:4
	v_mfma_f32_16x16x128_f8f6f4 v[42:45], v[174:177], v[210:213], v[42:45] cbsz:4 blgp:4
	v_mfma_f32_16x16x128_f8f6f4 v[46:49], v[170:173], v[202:205], v[46:49] cbsz:4 blgp:4
	v_mfma_f32_16x16x128_f8f6f4 v[46:49], v[178:181], v[210:213], v[46:49] cbsz:4 blgp:4
	v_mfma_f32_16x16x128_f8f6f4 v[74:77], v[214:217], v[202:205], v[74:77] cbsz:4 blgp:4
	v_mfma_f32_16x16x128_f8f6f4 v[74:77], v[222:225], v[210:213], v[74:77] cbsz:4 blgp:4
	v_mfma_f32_16x16x128_f8f6f4 v[78:81], v[218:221], v[202:205], v[78:81] cbsz:4 blgp:4
	v_mfma_f32_16x16x128_f8f6f4 v[78:81], v[226:229], v[210:213], v[78:81] cbsz:4 blgp:4
	s_setprio 0
	s_barrier
	s_mov_b32 m0, s64
	s_nop 0
	global_load_lds_dwordx4 v148, s[42:43]
	s_mov_b32 m0, s65
	s_nop 0
	global_load_lds_dwordx4 v152, s[42:43]
	ds_read_b128 v[182:185], v163 offset:49152
	ds_read_b128 v[186:189], v163 offset:51200
	ds_read_b128 v[190:193], v164 offset:49152
	ds_read_b128 v[194:197], v164 offset:51200
	ds_read_b128 v[198:201], v163 offset:53248
	ds_read_b128 v[202:205], v163 offset:55296
	ds_read_b128 v[206:209], v164 offset:53248
	ds_read_b128 v[210:213], v164 offset:55296
	s_mov_b32 m0, s66
	s_nop 0
	global_load_lds_dwordx4 v146, s[44:45]
	s_mov_b32 m0, s67
	s_nop 0
	global_load_lds_dwordx4 v150, s[44:45]
	s_add_u32 s42, s42, s24
	s_addc_u32 s43, s43, s25
	s_mov_b32 m0, s68
	s_nop 0
	global_load_lds_dwordx4 v148, s[42:43]
	s_mov_b32 m0, s69
	s_nop 0
	global_load_lds_dwordx4 v152, s[42:43]
	s_waitcnt vmcnt(8)
	s_waitcnt lgkmcnt(0)
	s_barrier
	s_setprio 1
	v_mfma_f32_16x16x128_f8f6f4 v[86:89], v[166:169], v[182:185], v[86:89] cbsz:4 blgp:4
	v_mfma_f32_16x16x128_f8f6f4 v[86:89], v[174:177], v[190:193], v[86:89] cbsz:4 blgp:4
	v_mfma_f32_16x16x128_f8f6f4 v[90:93], v[170:173], v[182:185], v[90:93] cbsz:4 blgp:4
	v_mfma_f32_16x16x128_f8f6f4 v[90:93], v[178:181], v[190:193], v[90:93] cbsz:4 blgp:4
	v_mfma_f32_16x16x128_f8f6f4 v[94:97], v[214:217], v[182:185], v[94:97] cbsz:4 blgp:4
	v_mfma_f32_16x16x128_f8f6f4 v[94:97], v[222:225], v[190:193], v[94:97] cbsz:4 blgp:4
	v_mfma_f32_16x16x128_f8f6f4 v[102:105], v[218:221], v[182:185], v[102:105] cbsz:4 blgp:4
	v_mfma_f32_16x16x128_f8f6f4 v[102:105], v[226:229], v[190:193], v[102:105] cbsz:4 blgp:4
	v_mfma_f32_16x16x128_f8f6f4 v[98:101], v[166:169], v[186:189], v[98:101] cbsz:4 blgp:4
	v_mfma_f32_16x16x128_f8f6f4 v[98:101], v[174:177], v[194:197], v[98:101] cbsz:4 blgp:4
	v_mfma_f32_16x16x128_f8f6f4 v[106:109], v[170:173], v[186:189], v[106:109] cbsz:4 blgp:4
	v_mfma_f32_16x16x128_f8f6f4 v[106:109], v[178:181], v[194:197], v[106:109] cbsz:4 blgp:4
	v_mfma_f32_16x16x128_f8f6f4 v[110:113], v[214:217], v[186:189], v[110:113] cbsz:4 blgp:4
	v_mfma_f32_16x16x128_f8f6f4 v[110:113], v[222:225], v[194:197], v[110:113] cbsz:4 blgp:4
	v_mfma_f32_16x16x128_f8f6f4 v[114:117], v[218:221], v[186:189], v[114:117] cbsz:4 blgp:4
	v_mfma_f32_16x16x128_f8f6f4 v[114:117], v[226:229], v[194:197], v[114:117] cbsz:4 blgp:4
	v_mfma_f32_16x16x128_f8f6f4 v[118:121], v[166:169], v[198:201], v[118:121] cbsz:4 blgp:4
	v_mfma_f32_16x16x128_f8f6f4 v[118:121], v[174:177], v[206:209], v[118:121] cbsz:4 blgp:4
	v_mfma_f32_16x16x128_f8f6f4 v[126:129], v[170:173], v[198:201], v[126:129] cbsz:4 blgp:4
	v_mfma_f32_16x16x128_f8f6f4 v[126:129], v[178:181], v[206:209], v[126:129] cbsz:4 blgp:4
	v_mfma_f32_16x16x128_f8f6f4 v[122:125], v[214:217], v[198:201], v[122:125] cbsz:4 blgp:4
	v_mfma_f32_16x16x128_f8f6f4 v[122:125], v[222:225], v[206:209], v[122:125] cbsz:4 blgp:4
	v_mfma_f32_16x16x128_f8f6f4 v[130:133], v[218:221], v[198:201], v[130:133] cbsz:4 blgp:4
	v_mfma_f32_16x16x128_f8f6f4 v[130:133], v[226:229], v[206:209], v[130:133] cbsz:4 blgp:4
	v_mfma_f32_16x16x128_f8f6f4 v[138:141], v[166:169], v[202:205], v[138:141] cbsz:4 blgp:4
	v_mfma_f32_16x16x128_f8f6f4 v[138:141], v[174:177], v[210:213], v[138:141] cbsz:4 blgp:4
	v_mfma_f32_16x16x128_f8f6f4 v[82:85], v[170:173], v[202:205], v[82:85] cbsz:4 blgp:4
	v_mfma_f32_16x16x128_f8f6f4 v[82:85], v[178:181], v[210:213], v[82:85] cbsz:4 blgp:4
	v_mfma_f32_16x16x128_f8f6f4 v[134:137], v[214:217], v[202:205], v[134:137] cbsz:4 blgp:4
	v_mfma_f32_16x16x128_f8f6f4 v[134:137], v[222:225], v[210:213], v[134:137] cbsz:4 blgp:4
	v_mfma_f32_16x16x128_f8f6f4 v[142:145], v[218:221], v[202:205], v[142:145] cbsz:4 blgp:4
	v_mfma_f32_16x16x128_f8f6f4 v[142:145], v[226:229], v[210:213], v[142:145] cbsz:4 blgp:4
	s_setprio 0
	s_andn2_b64 vcc, exec, s[34:35]
	s_barrier
	s_cbranch_vccnz .LBB4_4
	s_ashr_i32 s29, s28, 31
	s_lshl_b64 s[42:43], s[28:29], 10
	s_add_u32 s42, s10, s42
	s_addc_u32 s43, s11, s43
	s_add_u32 s29, s40, 0x200
	s_addc_u32 s78, s41, 0
	s_add_u32 s79, s38, 0x200
	s_addc_u32 s80, s39, 0
	s_add_u32 s38, s81, 0x180
	s_addc_u32 s39, s82, 0
	s_mov_b32 s81, 4
	s_cmp_eq_u32 s63, s81
	s_cselect_b64 s[40:41], -1, 0
	s_cmp_lg_u32 s63, s81
	s_cbranch_scc1 .LBB4_15
.LBB4_14:
	global_load_dwordx4 v[14:17], v147, s[42:43]
	global_load_dwordx4 v[10:13], v147, s[42:43] offset:16
	global_load_dwordx4 v[6:9], v147, s[42:43] offset:32
	global_load_dwordx4 v[2:5], v147, s[42:43] offset:48
	s_branch .Llast_4
.LBB4_15:
	ds_read_b128 v[166:169], v161
	ds_read_b128 v[170:173], v161 offset:2048
	ds_read_b128 v[174:177], v162
	ds_read_b128 v[178:181], v162 offset:2048
	s_and_b64 s[40:41], s[40:41], exec
	s_cselect_b32 s46, s36, s29
	s_cselect_b32 s47, s37, s78
	s_cselect_b32 s49, s5, s80
	s_cselect_b32 s48, s4, s79
	s_add_u32 s44, s46, 0x80
	s_addc_u32 s45, s47, 0
	s_add_u32 s40, s48, 0x80
	s_addc_u32 s41, s49, 0
	ds_read_b128 v[182:185], v163
	ds_read_b128 v[186:189], v163 offset:2048
	ds_read_b128 v[190:193], v164
	ds_read_b128 v[194:197], v164 offset:2048
	ds_read_b128 v[198:201], v163 offset:4096
	ds_read_b128 v[202:205], v163 offset:6144
	ds_read_b128 v[206:209], v164 offset:4096
	ds_read_b128 v[210:213], v164 offset:6144
	s_mov_b32 m0, s70
	s_nop 0
	global_load_lds_dwordx4 v146, s[38:39]
	s_mov_b32 m0, s71
	s_nop 0
	global_load_lds_dwordx4 v150, s[38:39]
	s_waitcnt lgkmcnt(8)
	ds_read_b128 v[214:217], v161 offset:16384
	ds_read_b128 v[218:221], v161 offset:18432
	ds_read_b128 v[222:225], v162 offset:16384
	ds_read_b128 v[226:229], v162 offset:18432
	s_waitcnt vmcnt(8)
	s_waitcnt lgkmcnt(0)
	s_barrier
	s_waitcnt lgkmcnt(0)
	s_setprio 1
	v_mfma_f32_16x16x128_f8f6f4 v[18:21], v[166:169], v[182:185], v[18:21] cbsz:4 blgp:4
	v_mfma_f32_16x16x128_f8f6f4 v[18:21], v[174:177], v[190:193], v[18:21] cbsz:4 blgp:4
	v_mfma_f32_16x16x128_f8f6f4 v[22:25], v[170:173], v[182:185], v[22:25] cbsz:4 blgp:4
	v_mfma_f32_16x16x128_f8f6f4 v[22:25], v[178:181], v[190:193], v[22:25] cbsz:4 blgp:4
	v_mfma_f32_16x16x128_f8f6f4 v[50:53], v[214:217], v[182:185], v[50:53] cbsz:4 blgp:4
	v_mfma_f32_16x16x128_f8f6f4 v[50:53], v[222:225], v[190:193], v[50:53] cbsz:4 blgp:4
	v_mfma_f32_16x16x128_f8f6f4 v[54:57], v[218:221], v[182:185], v[54:57] cbsz:4 blgp:4
	v_mfma_f32_16x16x128_f8f6f4 v[54:57], v[226:229], v[190:193], v[54:57] cbsz:4 blgp:4
	v_mfma_f32_16x16x128_f8f6f4 v[26:29], v[166:169], v[186:189], v[26:29] cbsz:4 blgp:4
	v_mfma_f32_16x16x128_f8f6f4 v[26:29], v[174:177], v[194:197], v[26:29] cbsz:4 blgp:4
	v_mfma_f32_16x16x128_f8f6f4 v[30:33], v[170:173], v[186:189], v[30:33] cbsz:4 blgp:4
	v_mfma_f32_16x16x128_f8f6f4 v[30:33], v[178:181], v[194:197], v[30:33] cbsz:4 blgp:4
	v_mfma_f32_16x16x128_f8f6f4 v[58:61], v[214:217], v[186:189], v[58:61] cbsz:4 blgp:4
	v_mfma_f32_16x16x128_f8f6f4 v[58:61], v[222:225], v[194:197], v[58:61] cbsz:4 blgp:4
	v_mfma_f32_16x16x128_f8f6f4 v[62:65], v[218:221], v[186:189], v[62:65] cbsz:4 blgp:4
	v_mfma_f32_16x16x128_f8f6f4 v[62:65], v[226:229], v[194:197], v[62:65] cbsz:4 blgp:4
	v_mfma_f32_16x16x128_f8f6f4 v[34:37], v[166:169], v[198:201], v[34:37] cbsz:4 blgp:4
	v_mfma_f32_16x16x128_f8f6f4 v[34:37], v[174:177], v[206:209], v[34:37] cbsz:4 blgp:4
	v_mfma_f32_16x16x128_f8f6f4 v[38:41], v[170:173], v[198:201], v[38:41] cbsz:4 blgp:4
	v_mfma_f32_16x16x128_f8f6f4 v[38:41], v[178:181], v[206:209], v[38:41] cbsz:4 blgp:4
	v_mfma_f32_16x16x128_f8f6f4 v[66:69], v[214:217], v[198:201], v[66:69] cbsz:4 blgp:4
	v_mfma_f32_16x16x128_f8f6f4 v[66:69], v[222:225], v[206:209], v[66:69] cbsz:4 blgp:4
	v_mfma_f32_16x16x128_f8f6f4 v[70:73], v[218:221], v[198:201], v[70:73] cbsz:4 blgp:4
	v_mfma_f32_16x16x128_f8f6f4 v[70:73], v[226:229], v[206:209], v[70:73] cbsz:4 blgp:4
	v_mfma_f32_16x16x128_f8f6f4 v[42:45], v[166:169], v[202:205], v[42:45] cbsz:4 blgp:4
	v_mfma_f32_16x16x128_f8f6f4 v[42:45], v[174:177], v[210:213], v[42:45] cbsz:4 blgp:4
	v_mfma_f32_16x16x128_f8f6f4 v[46:49], v[170:173], v[202:205], v[46:49] cbsz:4 blgp:4
	v_mfma_f32_16x16x128_f8f6f4 v[46:49], v[178:181], v[210:213], v[46:49] cbsz:4 blgp:4
	v_mfma_f32_16x16x128_f8f6f4 v[74:77], v[214:217], v[202:205], v[74:77] cbsz:4 blgp:4
	v_mfma_f32_16x16x128_f8f6f4 v[74:77], v[222:225], v[210:213], v[74:77] cbsz:4 blgp:4
	v_mfma_f32_16x16x128_f8f6f4 v[78:81], v[218:221], v[202:205], v[78:81] cbsz:4 blgp:4
	v_mfma_f32_16x16x128_f8f6f4 v[78:81], v[226:229], v[210:213], v[78:81] cbsz:4 blgp:4
	s_setprio 0
	s_barrier
	s_mov_b32 m0, s55
	s_nop 0
	global_load_lds_dwordx4 v148, s[48:49]
	s_mov_b32 m0, s56
	s_nop 0
	global_load_lds_dwordx4 v152, s[48:49]
	ds_read_b128 v[182:185], v163 offset:16384
	ds_read_b128 v[186:189], v163 offset:18432
	ds_read_b128 v[190:193], v164 offset:16384
	ds_read_b128 v[194:197], v164 offset:18432
	ds_read_b128 v[198:201], v163 offset:20480
	ds_read_b128 v[202:205], v163 offset:22528
	ds_read_b128 v[206:209], v164 offset:20480
	ds_read_b128 v[210:213], v164 offset:22528
	s_mov_b32 m0, s54
	s_nop 0
	global_load_lds_dwordx4 v146, s[46:47]
	s_mov_b32 m0, s57
	s_nop 0
	global_load_lds_dwordx4 v150, s[46:47]
	s_add_u32 s48, s48, s24
	s_addc_u32 s49, s49, s25
	s_mov_b32 m0, s58
	s_nop 0
	global_load_lds_dwordx4 v148, s[48:49]
	s_mov_b32 m0, s59
	s_nop 0
	global_load_lds_dwordx4 v152, s[48:49]
	s_waitcnt vmcnt(8)
	s_waitcnt lgkmcnt(0)
	s_barrier
	s_setprio 1
	v_mfma_f32_16x16x128_f8f6f4 v[86:89], v[166:169], v[182:185], v[86:89] cbsz:4 blgp:4
	v_mfma_f32_16x16x128_f8f6f4 v[86:89], v[174:177], v[190:193], v[86:89] cbsz:4 blgp:4
	v_mfma_f32_16x16x128_f8f6f4 v[90:93], v[170:173], v[182:185], v[90:93] cbsz:4 blgp:4
	v_mfma_f32_16x16x128_f8f6f4 v[90:93], v[178:181], v[190:193], v[90:93] cbsz:4 blgp:4
	v_mfma_f32_16x16x128_f8f6f4 v[94:97], v[214:217], v[182:185], v[94:97] cbsz:4 blgp:4
	v_mfma_f32_16x16x128_f8f6f4 v[94:97], v[222:225], v[190:193], v[94:97] cbsz:4 blgp:4
	v_mfma_f32_16x16x128_f8f6f4 v[102:105], v[218:221], v[182:185], v[102:105] cbsz:4 blgp:4
	v_mfma_f32_16x16x128_f8f6f4 v[102:105], v[226:229], v[190:193], v[102:105] cbsz:4 blgp:4
	v_mfma_f32_16x16x128_f8f6f4 v[98:101], v[166:169], v[186:189], v[98:101] cbsz:4 blgp:4
	v_mfma_f32_16x16x128_f8f6f4 v[98:101], v[174:177], v[194:197], v[98:101] cbsz:4 blgp:4
	v_mfma_f32_16x16x128_f8f6f4 v[106:109], v[170:173], v[186:189], v[106:109] cbsz:4 blgp:4
	v_mfma_f32_16x16x128_f8f6f4 v[106:109], v[178:181], v[194:197], v[106:109] cbsz:4 blgp:4
	v_mfma_f32_16x16x128_f8f6f4 v[110:113], v[214:217], v[186:189], v[110:113] cbsz:4 blgp:4
	v_mfma_f32_16x16x128_f8f6f4 v[110:113], v[222:225], v[194:197], v[110:113] cbsz:4 blgp:4
	v_mfma_f32_16x16x128_f8f6f4 v[114:117], v[218:221], v[186:189], v[114:117] cbsz:4 blgp:4
	v_mfma_f32_16x16x128_f8f6f4 v[114:117], v[226:229], v[194:197], v[114:117] cbsz:4 blgp:4
	v_mfma_f32_16x16x128_f8f6f4 v[118:121], v[166:169], v[198:201], v[118:121] cbsz:4 blgp:4
	v_mfma_f32_16x16x128_f8f6f4 v[118:121], v[174:177], v[206:209], v[118:121] cbsz:4 blgp:4
	v_mfma_f32_16x16x128_f8f6f4 v[126:129], v[170:173], v[198:201], v[126:129] cbsz:4 blgp:4
	v_mfma_f32_16x16x128_f8f6f4 v[126:129], v[178:181], v[206:209], v[126:129] cbsz:4 blgp:4
	v_mfma_f32_16x16x128_f8f6f4 v[122:125], v[214:217], v[198:201], v[122:125] cbsz:4 blgp:4
	v_mfma_f32_16x16x128_f8f6f4 v[122:125], v[222:225], v[206:209], v[122:125] cbsz:4 blgp:4
	v_mfma_f32_16x16x128_f8f6f4 v[130:133], v[218:221], v[198:201], v[130:133] cbsz:4 blgp:4
	v_mfma_f32_16x16x128_f8f6f4 v[130:133], v[226:229], v[206:209], v[130:133] cbsz:4 blgp:4
	v_mfma_f32_16x16x128_f8f6f4 v[138:141], v[166:169], v[202:205], v[138:141] cbsz:4 blgp:4
	v_mfma_f32_16x16x128_f8f6f4 v[138:141], v[174:177], v[210:213], v[138:141] cbsz:4 blgp:4
	v_mfma_f32_16x16x128_f8f6f4 v[82:85], v[170:173], v[202:205], v[82:85] cbsz:4 blgp:4
	v_mfma_f32_16x16x128_f8f6f4 v[82:85], v[178:181], v[210:213], v[82:85] cbsz:4 blgp:4
	v_mfma_f32_16x16x128_f8f6f4 v[134:137], v[214:217], v[202:205], v[134:137] cbsz:4 blgp:4
	v_mfma_f32_16x16x128_f8f6f4 v[134:137], v[222:225], v[210:213], v[134:137] cbsz:4 blgp:4
	v_mfma_f32_16x16x128_f8f6f4 v[142:145], v[218:221], v[202:205], v[142:145] cbsz:4 blgp:4
	v_mfma_f32_16x16x128_f8f6f4 v[142:145], v[226:229], v[210:213], v[142:145] cbsz:4 blgp:4
	s_setprio 0
	s_barrier
	ds_read_b128 v[166:169], v161 offset:32768
	ds_read_b128 v[170:173], v161 offset:34816
	ds_read_b128 v[174:177], v162 offset:32768
	ds_read_b128 v[178:181], v162 offset:34816
	ds_read_b128 v[182:185], v163 offset:32768
	ds_read_b128 v[186:189], v163 offset:34816
	ds_read_b128 v[190:193], v164 offset:32768
	ds_read_b128 v[194:197], v164 offset:34816
	ds_read_b128 v[198:201], v163 offset:36864
	ds_read_b128 v[202:205], v163 offset:38912
	ds_read_b128 v[206:209], v164 offset:36864
	ds_read_b128 v[210:213], v164 offset:38912
	s_add_u32 s46, s46, s22
	s_addc_u32 s47, s47, s23
	s_mov_b32 m0, s60
	s_nop 0
	global_load_lds_dwordx4 v146, s[46:47]
	s_mov_b32 m0, s61
	s_nop 0
	global_load_lds_dwordx4 v150, s[46:47]
	s_waitcnt lgkmcnt(8)
	ds_read_b128 v[214:217], v161 offset:49152
	ds_read_b128 v[218:221], v161 offset:51200
	ds_read_b128 v[222:225], v162 offset:49152
	ds_read_b128 v[226:229], v162 offset:51200
	s_waitcnt vmcnt(8)
	s_waitcnt lgkmcnt(0)
	s_barrier
	s_waitcnt lgkmcnt(0)
	s_setprio 1
	v_mfma_f32_16x16x128_f8f6f4 v[18:21], v[166:169], v[182:185], v[18:21] cbsz:4 blgp:4
	v_mfma_f32_16x16x128_f8f6f4 v[18:21], v[174:177], v[190:193], v[18:21] cbsz:4 blgp:4
	v_mfma_f32_16x16x128_f8f6f4 v[22:25], v[170:173], v[182:185], v[22:25] cbsz:4 blgp:4
	v_mfma_f32_16x16x128_f8f6f4 v[22:25], v[178:181], v[190:193], v[22:25] cbsz:4 blgp:4
	v_mfma_f32_16x16x128_f8f6f4 v[50:53], v[214:217], v[182:185], v[50:53] cbsz:4 blgp:4
	v_mfma_f32_16x16x128_f8f6f4 v[50:53], v[222:225], v[190:193], v[50:53] cbsz:4 blgp:4
	v_mfma_f32_16x16x128_f8f6f4 v[54:57], v[218:221], v[182:185], v[54:57] cbsz:4 blgp:4
	v_mfma_f32_16x16x128_f8f6f4 v[54:57], v[226:229], v[190:193], v[54:57] cbsz:4 blgp:4
	v_mfma_f32_16x16x128_f8f6f4 v[26:29], v[166:169], v[186:189], v[26:29] cbsz:4 blgp:4
	v_mfma_f32_16x16x128_f8f6f4 v[26:29], v[174:177], v[194:197], v[26:29] cbsz:4 blgp:4
	v_mfma_f32_16x16x128_f8f6f4 v[30:33], v[170:173], v[186:189], v[30:33] cbsz:4 blgp:4
	v_mfma_f32_16x16x128_f8f6f4 v[30:33], v[178:181], v[194:197], v[30:33] cbsz:4 blgp:4
	v_mfma_f32_16x16x128_f8f6f4 v[58:61], v[214:217], v[186:189], v[58:61] cbsz:4 blgp:4
	v_mfma_f32_16x16x128_f8f6f4 v[58:61], v[222:225], v[194:197], v[58:61] cbsz:4 blgp:4
	v_mfma_f32_16x16x128_f8f6f4 v[62:65], v[218:221], v[186:189], v[62:65] cbsz:4 blgp:4
	v_mfma_f32_16x16x128_f8f6f4 v[62:65], v[226:229], v[194:197], v[62:65] cbsz:4 blgp:4
	v_mfma_f32_16x16x128_f8f6f4 v[34:37], v[166:169], v[198:201], v[34:37] cbsz:4 blgp:4
	v_mfma_f32_16x16x128_f8f6f4 v[34:37], v[174:177], v[206:209], v[34:37] cbsz:4 blgp:4
	v_mfma_f32_16x16x128_f8f6f4 v[38:41], v[170:173], v[198:201], v[38:41] cbsz:4 blgp:4
	v_mfma_f32_16x16x128_f8f6f4 v[38:41], v[178:181], v[206:209], v[38:41] cbsz:4 blgp:4
	v_mfma_f32_16x16x128_f8f6f4 v[66:69], v[214:217], v[198:201], v[66:69] cbsz:4 blgp:4
	v_mfma_f32_16x16x128_f8f6f4 v[66:69], v[222:225], v[206:209], v[66:69] cbsz:4 blgp:4
	v_mfma_f32_16x16x128_f8f6f4 v[70:73], v[218:221], v[198:201], v[70:73] cbsz:4 blgp:4
	v_mfma_f32_16x16x128_f8f6f4 v[70:73], v[226:229], v[206:209], v[70:73] cbsz:4 blgp:4
	v_mfma_f32_16x16x128_f8f6f4 v[42:45], v[166:169], v[202:205], v[42:45] cbsz:4 blgp:4
	v_mfma_f32_16x16x128_f8f6f4 v[42:45], v[174:177], v[210:213], v[42:45] cbsz:4 blgp:4
	v_mfma_f32_16x16x128_f8f6f4 v[46:49], v[170:173], v[202:205], v[46:49] cbsz:4 blgp:4
	v_mfma_f32_16x16x128_f8f6f4 v[46:49], v[178:181], v[210:213], v[46:49] cbsz:4 blgp:4
	v_mfma_f32_16x16x128_f8f6f4 v[74:77], v[214:217], v[202:205], v[74:77] cbsz:4 blgp:4
	v_mfma_f32_16x16x128_f8f6f4 v[74:77], v[222:225], v[210:213], v[74:77] cbsz:4 blgp:4
	v_mfma_f32_16x16x128_f8f6f4 v[78:81], v[218:221], v[202:205], v[78:81] cbsz:4 blgp:4
	v_mfma_f32_16x16x128_f8f6f4 v[78:81], v[226:229], v[210:213], v[78:81] cbsz:4 blgp:4
	s_setprio 0
	s_barrier
	s_mov_b32 m0, s64
	s_nop 0
	global_load_lds_dwordx4 v148, s[40:41]
	s_mov_b32 m0, s65
	s_nop 0
	global_load_lds_dwordx4 v152, s[40:41]
	ds_read_b128 v[182:185], v163 offset:49152
	ds_read_b128 v[186:189], v163 offset:51200
	ds_read_b128 v[190:193], v164 offset:49152
	ds_read_b128 v[194:197], v164 offset:51200
	ds_read_b128 v[198:201], v163 offset:53248
	ds_read_b128 v[202:205], v163 offset:55296
	ds_read_b128 v[206:209], v164 offset:53248
	ds_read_b128 v[210:213], v164 offset:55296
	s_mov_b32 m0, s66
	s_nop 0
	global_load_lds_dwordx4 v146, s[44:45]
	s_mov_b32 m0, s67
	s_nop 0
	global_load_lds_dwordx4 v150, s[44:45]
	s_add_u32 s40, s40, s24
	s_addc_u32 s41, s41, s25
	s_mov_b32 m0, s68
	s_nop 0
	global_load_lds_dwordx4 v148, s[40:41]
	s_mov_b32 m0, s69
	s_nop 0
	global_load_lds_dwordx4 v152, s[40:41]
	s_waitcnt vmcnt(8)
	s_waitcnt lgkmcnt(0)
	s_barrier
	s_setprio 1
	v_mfma_f32_16x16x128_f8f6f4 v[86:89], v[166:169], v[182:185], v[86:89] cbsz:4 blgp:4
	v_mfma_f32_16x16x128_f8f6f4 v[86:89], v[174:177], v[190:193], v[86:89] cbsz:4 blgp:4
	v_mfma_f32_16x16x128_f8f6f4 v[90:93], v[170:173], v[182:185], v[90:93] cbsz:4 blgp:4
	v_mfma_f32_16x16x128_f8f6f4 v[90:93], v[178:181], v[190:193], v[90:93] cbsz:4 blgp:4
	v_mfma_f32_16x16x128_f8f6f4 v[94:97], v[214:217], v[182:185], v[94:97] cbsz:4 blgp:4
	v_mfma_f32_16x16x128_f8f6f4 v[94:97], v[222:225], v[190:193], v[94:97] cbsz:4 blgp:4
	v_mfma_f32_16x16x128_f8f6f4 v[102:105], v[218:221], v[182:185], v[102:105] cbsz:4 blgp:4
	v_mfma_f32_16x16x128_f8f6f4 v[102:105], v[226:229], v[190:193], v[102:105] cbsz:4 blgp:4
	v_mfma_f32_16x16x128_f8f6f4 v[98:101], v[166:169], v[186:189], v[98:101] cbsz:4 blgp:4
	v_mfma_f32_16x16x128_f8f6f4 v[98:101], v[174:177], v[194:197], v[98:101] cbsz:4 blgp:4
	v_mfma_f32_16x16x128_f8f6f4 v[106:109], v[170:173], v[186:189], v[106:109] cbsz:4 blgp:4
	v_mfma_f32_16x16x128_f8f6f4 v[106:109], v[178:181], v[194:197], v[106:109] cbsz:4 blgp:4
	v_mfma_f32_16x16x128_f8f6f4 v[110:113], v[214:217], v[186:189], v[110:113] cbsz:4 blgp:4
	v_mfma_f32_16x16x128_f8f6f4 v[110:113], v[222:225], v[194:197], v[110:113] cbsz:4 blgp:4
	v_mfma_f32_16x16x128_f8f6f4 v[114:117], v[218:221], v[186:189], v[114:117] cbsz:4 blgp:4
	v_mfma_f32_16x16x128_f8f6f4 v[114:117], v[226:229], v[194:197], v[114:117] cbsz:4 blgp:4
	v_mfma_f32_16x16x128_f8f6f4 v[118:121], v[166:169], v[198:201], v[118:121] cbsz:4 blgp:4
	v_mfma_f32_16x16x128_f8f6f4 v[118:121], v[174:177], v[206:209], v[118:121] cbsz:4 blgp:4
	v_mfma_f32_16x16x128_f8f6f4 v[126:129], v[170:173], v[198:201], v[126:129] cbsz:4 blgp:4
	v_mfma_f32_16x16x128_f8f6f4 v[126:129], v[178:181], v[206:209], v[126:129] cbsz:4 blgp:4
	v_mfma_f32_16x16x128_f8f6f4 v[122:125], v[214:217], v[198:201], v[122:125] cbsz:4 blgp:4
	v_mfma_f32_16x16x128_f8f6f4 v[122:125], v[222:225], v[206:209], v[122:125] cbsz:4 blgp:4
	v_mfma_f32_16x16x128_f8f6f4 v[130:133], v[218:221], v[198:201], v[130:133] cbsz:4 blgp:4
	v_mfma_f32_16x16x128_f8f6f4 v[130:133], v[226:229], v[206:209], v[130:133] cbsz:4 blgp:4
	v_mfma_f32_16x16x128_f8f6f4 v[138:141], v[166:169], v[202:205], v[138:141] cbsz:4 blgp:4
	v_mfma_f32_16x16x128_f8f6f4 v[138:141], v[174:177], v[210:213], v[138:141] cbsz:4 blgp:4
	v_mfma_f32_16x16x128_f8f6f4 v[82:85], v[170:173], v[202:205], v[82:85] cbsz:4 blgp:4
	v_mfma_f32_16x16x128_f8f6f4 v[82:85], v[178:181], v[210:213], v[82:85] cbsz:4 blgp:4
	v_mfma_f32_16x16x128_f8f6f4 v[134:137], v[214:217], v[202:205], v[134:137] cbsz:4 blgp:4
	v_mfma_f32_16x16x128_f8f6f4 v[134:137], v[222:225], v[210:213], v[134:137] cbsz:4 blgp:4
	v_mfma_f32_16x16x128_f8f6f4 v[142:145], v[218:221], v[202:205], v[142:145] cbsz:4 blgp:4
	v_mfma_f32_16x16x128_f8f6f4 v[142:145], v[226:229], v[210:213], v[142:145] cbsz:4 blgp:4
	s_setprio 0
	s_add_i32 s40, s81, 2
	s_add_u32 s29, s29, 0x100
	s_addc_u32 s78, s78, 0
	s_add_u32 s79, s79, 0x100
	s_addc_u32 s80, s80, 0
	s_add_u32 s38, s38, 0x100
	s_addc_u32 s39, s39, 0
	s_cmp_ge_i32 s81, s63
	s_barrier
	s_cbranch_scc1 .LBB4_4
	s_mov_b32 s81, s40
	s_cmp_eq_u32 s63, s81
	s_cselect_b64 s[40:41], -1, 0
	s_cmp_lg_u32 s63, s81
	s_cbranch_scc0 .LBB4_14
	s_branch .LBB4_15
.Llast_4:
	ds_read_b128 v[166:169], v161
	ds_read_b128 v[170:173], v161 offset:2048
	ds_read_b128 v[174:177], v162
	ds_read_b128 v[178:181], v162 offset:2048
	s_and_b64 s[40:41], s[40:41], exec
	s_cselect_b32 s46, s36, s29
	s_cselect_b32 s47, s37, s78
	s_cselect_b32 s49, s5, s80
	s_cselect_b32 s48, s4, s79
	s_add_u32 s44, s46, 0x80
	s_addc_u32 s45, s47, 0
	s_add_u32 s40, s48, 0x80
	s_addc_u32 s41, s49, 0
	ds_read_b128 v[182:185], v163
	ds_read_b128 v[186:189], v163 offset:2048
	ds_read_b128 v[190:193], v164
	ds_read_b128 v[194:197], v164 offset:2048
	ds_read_b128 v[198:201], v163 offset:4096
	ds_read_b128 v[202:205], v163 offset:6144
	ds_read_b128 v[206:209], v164 offset:4096
	ds_read_b128 v[210:213], v164 offset:6144
	s_mov_b32 m0, s70
	s_nop 0
	global_load_lds_dwordx4 v146, s[38:39]
	s_mov_b32 m0, s71
	s_nop 0
	global_load_lds_dwordx4 v150, s[38:39]
	s_waitcnt lgkmcnt(8)
	ds_read_b128 v[214:217], v161 offset:16384
	ds_read_b128 v[218:221], v161 offset:18432
	ds_read_b128 v[222:225], v162 offset:16384
	ds_read_b128 v[226:229], v162 offset:18432
	s_waitcnt vmcnt(8)
	s_waitcnt lgkmcnt(0)
	s_barrier
	s_waitcnt lgkmcnt(0)
	s_setprio 1
	v_mfma_f32_16x16x128_f8f6f4 v[18:21], v[166:169], v[182:185], v[18:21] cbsz:4 blgp:4
	v_mfma_f32_16x16x128_f8f6f4 v[18:21], v[174:177], v[190:193], v[18:21] cbsz:4 blgp:4
	v_mfma_f32_16x16x128_f8f6f4 v[22:25], v[170:173], v[182:185], v[22:25] cbsz:4 blgp:4
	v_mfma_f32_16x16x128_f8f6f4 v[22:25], v[178:181], v[190:193], v[22:25] cbsz:4 blgp:4
	v_mfma_f32_16x16x128_f8f6f4 v[50:53], v[214:217], v[182:185], v[50:53] cbsz:4 blgp:4
	v_mfma_f32_16x16x128_f8f6f4 v[50:53], v[222:225], v[190:193], v[50:53] cbsz:4 blgp:4
	v_mfma_f32_16x16x128_f8f6f4 v[54:57], v[218:221], v[182:185], v[54:57] cbsz:4 blgp:4
	v_mfma_f32_16x16x128_f8f6f4 v[54:57], v[226:229], v[190:193], v[54:57] cbsz:4 blgp:4
	v_mfma_f32_16x16x128_f8f6f4 v[26:29], v[166:169], v[186:189], v[26:29] cbsz:4 blgp:4
	v_mfma_f32_16x16x128_f8f6f4 v[26:29], v[174:177], v[194:197], v[26:29] cbsz:4 blgp:4
	v_mfma_f32_16x16x128_f8f6f4 v[30:33], v[170:173], v[186:189], v[30:33] cbsz:4 blgp:4
	v_mfma_f32_16x16x128_f8f6f4 v[30:33], v[178:181], v[194:197], v[30:33] cbsz:4 blgp:4
	v_mfma_f32_16x16x128_f8f6f4 v[58:61], v[214:217], v[186:189], v[58:61] cbsz:4 blgp:4
	v_mfma_f32_16x16x128_f8f6f4 v[58:61], v[222:225], v[194:197], v[58:61] cbsz:4 blgp:4
	v_mfma_f32_16x16x128_f8f6f4 v[62:65], v[218:221], v[186:189], v[62:65] cbsz:4 blgp:4
	v_mfma_f32_16x16x128_f8f6f4 v[62:65], v[226:229], v[194:197], v[62:65] cbsz:4 blgp:4
	v_mfma_f32_16x16x128_f8f6f4 v[34:37], v[166:169], v[198:201], v[34:37] cbsz:4 blgp:4
	v_mfma_f32_16x16x128_f8f6f4 v[34:37], v[174:177], v[206:209], v[34:37] cbsz:4 blgp:4
	v_mfma_f32_16x16x128_f8f6f4 v[38:41], v[170:173], v[198:201], v[38:41] cbsz:4 blgp:4
	v_mfma_f32_16x16x128_f8f6f4 v[38:41], v[178:181], v[206:209], v[38:41] cbsz:4 blgp:4
	v_mfma_f32_16x16x128_f8f6f4 v[66:69], v[214:217], v[198:201], v[66:69] cbsz:4 blgp:4
	v_mfma_f32_16x16x128_f8f6f4 v[66:69], v[222:225], v[206:209], v[66:69] cbsz:4 blgp:4
	v_mfma_f32_16x16x128_f8f6f4 v[70:73], v[218:221], v[198:201], v[70:73] cbsz:4 blgp:4
	v_mfma_f32_16x16x128_f8f6f4 v[70:73], v[226:229], v[206:209], v[70:73] cbsz:4 blgp:4
	v_mfma_f32_16x16x128_f8f6f4 v[42:45], v[166:169], v[202:205], v[42:45] cbsz:4 blgp:4
	v_mfma_f32_16x16x128_f8f6f4 v[42:45], v[174:177], v[210:213], v[42:45] cbsz:4 blgp:4
	v_mfma_f32_16x16x128_f8f6f4 v[46:49], v[170:173], v[202:205], v[46:49] cbsz:4 blgp:4
	v_mfma_f32_16x16x128_f8f6f4 v[46:49], v[178:181], v[210:213], v[46:49] cbsz:4 blgp:4
	v_mfma_f32_16x16x128_f8f6f4 v[74:77], v[214:217], v[202:205], v[74:77] cbsz:4 blgp:4
	v_mfma_f32_16x16x128_f8f6f4 v[74:77], v[222:225], v[210:213], v[74:77] cbsz:4 blgp:4
	v_mfma_f32_16x16x128_f8f6f4 v[78:81], v[218:221], v[202:205], v[78:81] cbsz:4 blgp:4
	v_mfma_f32_16x16x128_f8f6f4 v[78:81], v[226:229], v[210:213], v[78:81] cbsz:4 blgp:4
	s_setprio 0
	s_barrier
	s_mov_b32 m0, s55
	s_nop 0
	global_load_lds_dwordx4 v148, s[48:49]
	s_mov_b32 m0, s56
	s_nop 0
	global_load_lds_dwordx4 v152, s[48:49]
	ds_read_b128 v[182:185], v163 offset:16384
	ds_read_b128 v[186:189], v163 offset:18432
	ds_read_b128 v[190:193], v164 offset:16384
	ds_read_b128 v[194:197], v164 offset:18432
	ds_read_b128 v[198:201], v163 offset:20480
	ds_read_b128 v[202:205], v163 offset:22528
	ds_read_b128 v[206:209], v164 offset:20480
	ds_read_b128 v[210:213], v164 offset:22528
	s_mov_b32 m0, s54
	s_nop 0
	global_load_lds_dwordx4 v146, s[46:47]
	s_mov_b32 m0, s57
	s_nop 0
	global_load_lds_dwordx4 v150, s[46:47]
	s_add_u32 s48, s48, s24
	s_addc_u32 s49, s49, s25
	s_mov_b32 m0, s58
	s_nop 0
	global_load_lds_dwordx4 v148, s[48:49]
	s_mov_b32 m0, s59
	s_nop 0
	global_load_lds_dwordx4 v152, s[48:49]
	s_waitcnt vmcnt(8)
	s_waitcnt lgkmcnt(0)
	s_barrier
	s_setprio 1
	v_mfma_f32_16x16x128_f8f6f4 v[86:89], v[166:169], v[182:185], v[86:89] cbsz:4 blgp:4
	v_mfma_f32_16x16x128_f8f6f4 v[86:89], v[174:177], v[190:193], v[86:89] cbsz:4 blgp:4
	v_mfma_f32_16x16x128_f8f6f4 v[90:93], v[170:173], v[182:185], v[90:93] cbsz:4 blgp:4
	v_mfma_f32_16x16x128_f8f6f4 v[90:93], v[178:181], v[190:193], v[90:93] cbsz:4 blgp:4
	v_mfma_f32_16x16x128_f8f6f4 v[94:97], v[214:217], v[182:185], v[94:97] cbsz:4 blgp:4
	v_mfma_f32_16x16x128_f8f6f4 v[94:97], v[222:225], v[190:193], v[94:97] cbsz:4 blgp:4
	v_mfma_f32_16x16x128_f8f6f4 v[102:105], v[218:221], v[182:185], v[102:105] cbsz:4 blgp:4
	v_mfma_f32_16x16x128_f8f6f4 v[102:105], v[226:229], v[190:193], v[102:105] cbsz:4 blgp:4
	v_mfma_f32_16x16x128_f8f6f4 v[98:101], v[166:169], v[186:189], v[98:101] cbsz:4 blgp:4
	v_mfma_f32_16x16x128_f8f6f4 v[98:101], v[174:177], v[194:197], v[98:101] cbsz:4 blgp:4
	v_mfma_f32_16x16x128_f8f6f4 v[106:109], v[170:173], v[186:189], v[106:109] cbsz:4 blgp:4
	v_mfma_f32_16x16x128_f8f6f4 v[106:109], v[178:181], v[194:197], v[106:109] cbsz:4 blgp:4
	v_mfma_f32_16x16x128_f8f6f4 v[110:113], v[214:217], v[186:189], v[110:113] cbsz:4 blgp:4
	v_mfma_f32_16x16x128_f8f6f4 v[110:113], v[222:225], v[194:197], v[110:113] cbsz:4 blgp:4
	v_mfma_f32_16x16x128_f8f6f4 v[114:117], v[218:221], v[186:189], v[114:117] cbsz:4 blgp:4
	v_mfma_f32_16x16x128_f8f6f4 v[114:117], v[226:229], v[194:197], v[114:117] cbsz:4 blgp:4
	v_mfma_f32_16x16x128_f8f6f4 v[118:121], v[166:169], v[198:201], v[118:121] cbsz:4 blgp:4
	v_mfma_f32_16x16x128_f8f6f4 v[118:121], v[174:177], v[206:209], v[118:121] cbsz:4 blgp:4
	v_mfma_f32_16x16x128_f8f6f4 v[126:129], v[170:173], v[198:201], v[126:129] cbsz:4 blgp:4
	v_mfma_f32_16x16x128_f8f6f4 v[126:129], v[178:181], v[206:209], v[126:129] cbsz:4 blgp:4
	v_mfma_f32_16x16x128_f8f6f4 v[122:125], v[214:217], v[198:201], v[122:125] cbsz:4 blgp:4
	v_mfma_f32_16x16x128_f8f6f4 v[122:125], v[222:225], v[206:209], v[122:125] cbsz:4 blgp:4
	v_mfma_f32_16x16x128_f8f6f4 v[130:133], v[218:221], v[198:201], v[130:133] cbsz:4 blgp:4
	v_mfma_f32_16x16x128_f8f6f4 v[130:133], v[226:229], v[206:209], v[130:133] cbsz:4 blgp:4
	v_mfma_f32_16x16x128_f8f6f4 v[138:141], v[166:169], v[202:205], v[138:141] cbsz:4 blgp:4
	v_mfma_f32_16x16x128_f8f6f4 v[138:141], v[174:177], v[210:213], v[138:141] cbsz:4 blgp:4
	v_mfma_f32_16x16x128_f8f6f4 v[82:85], v[170:173], v[202:205], v[82:85] cbsz:4 blgp:4
	v_mfma_f32_16x16x128_f8f6f4 v[82:85], v[178:181], v[210:213], v[82:85] cbsz:4 blgp:4
	v_mfma_f32_16x16x128_f8f6f4 v[134:137], v[214:217], v[202:205], v[134:137] cbsz:4 blgp:4
	v_mfma_f32_16x16x128_f8f6f4 v[134:137], v[222:225], v[210:213], v[134:137] cbsz:4 blgp:4
	v_mfma_f32_16x16x128_f8f6f4 v[142:145], v[218:221], v[202:205], v[142:145] cbsz:4 blgp:4
	v_mfma_f32_16x16x128_f8f6f4 v[142:145], v[226:229], v[210:213], v[142:145] cbsz:4 blgp:4
	s_setprio 0
	s_barrier
	ds_read_b128 v[166:169], v161 offset:32768
	ds_read_b128 v[170:173], v161 offset:34816
	ds_read_b128 v[174:177], v162 offset:32768
	ds_read_b128 v[178:181], v162 offset:34816
	ds_read_b128 v[182:185], v163 offset:32768
	ds_read_b128 v[186:189], v163 offset:34816
	ds_read_b128 v[190:193], v164 offset:32768
	ds_read_b128 v[194:197], v164 offset:34816
	ds_read_b128 v[198:201], v163 offset:36864
	ds_read_b128 v[202:205], v163 offset:38912
	ds_read_b128 v[206:209], v164 offset:36864
	ds_read_b128 v[210:213], v164 offset:38912
	s_add_u32 s46, s46, s22
	s_addc_u32 s47, s47, s23
	s_mov_b32 m0, s60
	s_nop 0
	global_load_lds_dwordx4 v146, s[46:47]
	s_mov_b32 m0, s61
	s_nop 0
	global_load_lds_dwordx4 v150, s[46:47]
	s_waitcnt lgkmcnt(8)
	ds_read_b128 v[214:217], v161 offset:49152
	ds_read_b128 v[218:221], v161 offset:51200
	ds_read_b128 v[222:225], v162 offset:49152
	ds_read_b128 v[226:229], v162 offset:51200
	s_waitcnt vmcnt(8)
	s_waitcnt lgkmcnt(0)
	s_barrier
	s_waitcnt lgkmcnt(0)
	s_setprio 1
	v_mfma_f32_16x16x128_f8f6f4 v[18:21], v[166:169], v[182:185], v[18:21] cbsz:4 blgp:4
	v_mfma_f32_16x16x128_f8f6f4 v[18:21], v[174:177], v[190:193], v[18:21] cbsz:4 blgp:4
	v_mfma_f32_16x16x128_f8f6f4 v[22:25], v[170:173], v[182:185], v[22:25] cbsz:4 blgp:4
	v_mfma_f32_16x16x128_f8f6f4 v[22:25], v[178:181], v[190:193], v[22:25] cbsz:4 blgp:4
	v_mfma_f32_16x16x128_f8f6f4 v[50:53], v[214:217], v[182:185], v[50:53] cbsz:4 blgp:4
	v_mfma_f32_16x16x128_f8f6f4 v[50:53], v[222:225], v[190:193], v[50:53] cbsz:4 blgp:4
	v_mfma_f32_16x16x128_f8f6f4 v[54:57], v[218:221], v[182:185], v[54:57] cbsz:4 blgp:4
	v_mfma_f32_16x16x128_f8f6f4 v[54:57], v[226:229], v[190:193], v[54:57] cbsz:4 blgp:4
	v_mfma_f32_16x16x128_f8f6f4 v[26:29], v[166:169], v[186:189], v[26:29] cbsz:4 blgp:4
	v_mfma_f32_16x16x128_f8f6f4 v[26:29], v[174:177], v[194:197], v[26:29] cbsz:4 blgp:4
	v_mfma_f32_16x16x128_f8f6f4 v[30:33], v[170:173], v[186:189], v[30:33] cbsz:4 blgp:4
	v_mfma_f32_16x16x128_f8f6f4 v[30:33], v[178:181], v[194:197], v[30:33] cbsz:4 blgp:4
	v_mfma_f32_16x16x128_f8f6f4 v[58:61], v[214:217], v[186:189], v[58:61] cbsz:4 blgp:4
	v_mfma_f32_16x16x128_f8f6f4 v[58:61], v[222:225], v[194:197], v[58:61] cbsz:4 blgp:4
	v_mfma_f32_16x16x128_f8f6f4 v[62:65], v[218:221], v[186:189], v[62:65] cbsz:4 blgp:4
	v_mfma_f32_16x16x128_f8f6f4 v[62:65], v[226:229], v[194:197], v[62:65] cbsz:4 blgp:4
	v_mfma_f32_16x16x128_f8f6f4 v[34:37], v[166:169], v[198:201], v[34:37] cbsz:4 blgp:4
	v_mfma_f32_16x16x128_f8f6f4 v[34:37], v[174:177], v[206:209], v[34:37] cbsz:4 blgp:4
	v_mfma_f32_16x16x128_f8f6f4 v[38:41], v[170:173], v[198:201], v[38:41] cbsz:4 blgp:4
	v_mfma_f32_16x16x128_f8f6f4 v[38:41], v[178:181], v[206:209], v[38:41] cbsz:4 blgp:4
	v_mfma_f32_16x16x128_f8f6f4 v[66:69], v[214:217], v[198:201], v[66:69] cbsz:4 blgp:4
	v_mfma_f32_16x16x128_f8f6f4 v[66:69], v[222:225], v[206:209], v[66:69] cbsz:4 blgp:4
	v_mfma_f32_16x16x128_f8f6f4 v[70:73], v[218:221], v[198:201], v[70:73] cbsz:4 blgp:4
	v_mfma_f32_16x16x128_f8f6f4 v[70:73], v[226:229], v[206:209], v[70:73] cbsz:4 blgp:4
	v_mfma_f32_16x16x128_f8f6f4 v[42:45], v[166:169], v[202:205], v[42:45] cbsz:4 blgp:4
	v_mfma_f32_16x16x128_f8f6f4 v[42:45], v[174:177], v[210:213], v[42:45] cbsz:4 blgp:4
	v_mfma_f32_16x16x128_f8f6f4 v[46:49], v[170:173], v[202:205], v[46:49] cbsz:4 blgp:4
	v_mfma_f32_16x16x128_f8f6f4 v[46:49], v[178:181], v[210:213], v[46:49] cbsz:4 blgp:4
	v_mfma_f32_16x16x128_f8f6f4 v[74:77], v[214:217], v[202:205], v[74:77] cbsz:4 blgp:4
	v_mfma_f32_16x16x128_f8f6f4 v[74:77], v[222:225], v[210:213], v[74:77] cbsz:4 blgp:4
	v_mfma_f32_16x16x128_f8f6f4 v[78:81], v[218:221], v[202:205], v[78:81] cbsz:4 blgp:4
	v_mfma_f32_16x16x128_f8f6f4 v[78:81], v[226:229], v[210:213], v[78:81] cbsz:4 blgp:4
	s_setprio 0
	s_barrier
	s_mov_b32 m0, s64
	s_nop 0
	global_load_lds_dwordx4 v148, s[40:41]
	s_mov_b32 m0, s65
	s_nop 0
	global_load_lds_dwordx4 v152, s[40:41]
	ds_read_b128 v[182:185], v163 offset:49152
	ds_read_b128 v[186:189], v163 offset:51200
	ds_read_b128 v[190:193], v164 offset:49152
	ds_read_b128 v[194:197], v164 offset:51200
	ds_read_b128 v[198:201], v163 offset:53248
	ds_read_b128 v[202:205], v163 offset:55296
	ds_read_b128 v[206:209], v164 offset:53248
	ds_read_b128 v[210:213], v164 offset:55296
	s_mov_b32 m0, s66
	s_nop 0
	global_load_lds_dwordx4 v146, s[44:45]
	s_mov_b32 m0, s67
	s_nop 0
	global_load_lds_dwordx4 v150, s[44:45]
	s_add_u32 s40, s40, s24
	s_addc_u32 s41, s41, s25
	s_mov_b32 m0, s68
	s_nop 0
	global_load_lds_dwordx4 v148, s[40:41]
	s_mov_b32 m0, s69
	s_nop 0
	global_load_lds_dwordx4 v152, s[40:41]
	s_waitcnt vmcnt(8)
	s_waitcnt lgkmcnt(0)
	s_barrier
	s_setprio 1
	v_mfma_f32_16x16x128_f8f6f4 v[86:89], v[166:169], v[182:185], v[86:89] cbsz:4 blgp:4
	v_med3_f32 v232, v18, v160, 0
	v_med3_f32 v230, v19, v160, 0
	v_med3_f32 v233, v20, v160, 0
	v_mfma_f32_16x16x128_f8f6f4 v[86:89], v[174:177], v[190:193], v[86:89] cbsz:4 blgp:4
	v_med3_f32 v234, v21, v160, 0
	v_cvt_scalef32_pk_fp4_f32 v232, v232, v230, v159
	v_med3_f32 v235, v22, v160, 0
	v_med3_f32 v236, v23, v160, 0
	v_mfma_f32_16x16x128_f8f6f4 v[90:93], v[170:173], v[182:185], v[90:93] cbsz:4 blgp:4
	v_cvt_scalef32_pk_fp4_f32 v232, v233, v234, v159 op_sel:[0,0,1,0]
	v_med3_f32 v233, v50, v160, 0
	v_med3_f32 v230, v51, v160, 0
	v_mfma_f32_16x16x128_f8f6f4 v[90:93], v[178:181], v[190:193], v[90:93] cbsz:4 blgp:4
	v_med3_f32 v237, v24, v160, 0
	v_med3_f32 v238, v25, v160, 0
	v_cvt_scalef32_pk_fp4_f32 v232, v235, v236, v159 op_sel:[0,0,0,1]
	v_med3_f32 v234, v52, v160, 0
	v_mfma_f32_16x16x128_f8f6f4 v[94:97], v[214:217], v[182:185], v[94:97] cbsz:4 blgp:4
	v_med3_f32 v235, v53, v160, 0
	v_cvt_scalef32_pk_fp4_f32 v233, v233, v230, v159
	v_cvt_scalef32_pk_fp4_f32 v232, v237, v238, v159 op_sel:[0,0,1,1]
	v_mfma_f32_16x16x128_f8f6f4 v[94:97], v[222:225], v[190:193], v[94:97] cbsz:4 blgp:4
	v_med3_f32 v236, v54, v160, 0
	v_med3_f32 v237, v55, v160, 0
	v_cvt_scalef32_pk_fp4_f32 v233, v234, v235, v159 op_sel:[0,0,1,0]
	v_med3_f32 v234, v26, v160, 0
	v_mfma_f32_16x16x128_f8f6f4 v[102:105], v[218:221], v[182:185], v[102:105] cbsz:4 blgp:4
	v_med3_f32 v230, v27, v160, 0
	v_med3_f32 v238, v56, v160, 0
	v_med3_f32 v239, v57, v160, 0
	v_mfma_f32_16x16x128_f8f6f4 v[102:105], v[226:229], v[190:193], v[102:105] cbsz:4 blgp:4
	v_cvt_scalef32_pk_fp4_f32 v233, v236, v237, v159 op_sel:[0,0,0,1]
	v_med3_f32 v235, v28, v160, 0
	v_med3_f32 v236, v29, v160, 0
	v_cvt_scalef32_pk_fp4_f32 v234, v234, v230, v159
	v_mfma_f32_16x16x128_f8f6f4 v[98:101], v[166:169], v[186:189], v[98:101] cbsz:4 blgp:4
	v_cvt_scalef32_pk_fp4_f32 v233, v238, v239, v159 op_sel:[0,0,1,1]
	v_med3_f32 v237, v30, v160, 0
	v_med3_f32 v238, v31, v160, 0
	v_mfma_f32_16x16x128_f8f6f4 v[98:101], v[174:177], v[194:197], v[98:101] cbsz:4 blgp:4
	v_cvt_scalef32_pk_fp4_f32 v234, v235, v236, v159 op_sel:[0,0,1,0]
	v_med3_f32 v235, v58, v160, 0
	v_med3_f32 v230, v59, v160, 0
	v_med3_f32 v239, v32, v160, 0
	v_mfma_f32_16x16x128_f8f6f4 v[106:109], v[170:173], v[186:189], v[106:109] cbsz:4 blgp:4
	v_med3_f32 v240, v33, v160, 0
	v_cvt_scalef32_pk_fp4_f32 v234, v237, v238, v159 op_sel:[0,0,0,1]
	v_med3_f32 v236, v60, v160, 0
	v_mfma_f32_16x16x128_f8f6f4 v[106:109], v[178:181], v[194:197], v[106:109] cbsz:4 blgp:4
	v_med3_f32 v237, v61, v160, 0
	v_cvt_scalef32_pk_fp4_f32 v235, v235, v230, v159
	v_lshl_add_u32 v244, s77, 8, v149
	v_lshl_or_b32 v246, s76, 8, v151
	v_mfma_f32_16x16x128_f8f6f4 v[110:113], v[214:217], v[186:189], v[110:113] cbsz:4 blgp:4
	v_cvt_scalef32_pk_fp4_f32 v234, v239, v240, v159 op_sel:[0,0,1,1]
	v_med3_f32 v238, v62, v160, 0
	v_med3_f32 v239, v63, v160, 0
	v_mfma_f32_16x16x128_f8f6f4 v[110:113], v[222:225], v[194:197], v[110:113] cbsz:4 blgp:4
	v_cvt_scalef32_pk_fp4_f32 v235, v236, v237, v159 op_sel:[0,0,1,0]
	v_ashrrev_i32_e32 v246, 1, v246
	v_med3_f32 v240, v64, v160, 0
	v_med3_f32 v241, v65, v160, 0
	v_mfma_f32_16x16x128_f8f6f4 v[114:117], v[218:221], v[186:189], v[114:117] cbsz:4 blgp:4
	v_cvt_scalef32_pk_fp4_f32 v235, v238, v239, v159 op_sel:[0,0,0,1]
	v_or_b32_e32 v230, v244, v153
	v_mov_b64_e32 v[236:237], s[8:9]
	v_mfma_f32_16x16x128_f8f6f4 v[114:117], v[226:229], v[194:197], v[114:117] cbsz:4 blgp:4
	v_ashrrev_i32_e32 v247, 31, v246
	v_cvt_scalef32_pk_fp4_f32 v235, v240, v241, v159 op_sel:[0,0,1,1]
	v_mad_i64_i32 v[238:239], s[84:85], v230, s12, v[236:237]
	v_permlane16_swap_b32_e32 v232, v234
	v_mfma_f32_16x16x128_f8f6f4 v[118:121], v[166:169], v[198:201], v[118:121] cbsz:4 blgp:4
	v_permlane16_swap_b32_e32 v233, v235
	v_lshl_add_u64 v[238:239], v[238:239], 0, v[246:247]
	global_store_dwordx4 v[238:239], v[232:235], off
	v_med3_f32 v230, v35, v160, 0
	v_mfma_f32_16x16x128_f8f6f4 v[118:121], v[174:177], v[206:209], v[118:121] cbsz:4 blgp:4
	v_med3_f32 v238, v39, v160, 0
	v_med3_f32 v232, v34, v160, 0
	v_med3_f32 v233, v36, v160, 0
	v_mfma_f32_16x16x128_f8f6f4 v[126:129], v[170:173], v[198:201], v[126:129] cbsz:4 blgp:4
	v_med3_f32 v234, v37, v160, 0
	v_cvt_scalef32_pk_fp4_f32 v232, v232, v230, v159
	v_med3_f32 v235, v38, v160, 0
	v_cvt_scalef32_pk_fp4_f32 v232, v233, v234, v159 op_sel:[0,0,1,0]
	v_mfma_f32_16x16x128_f8f6f4 v[126:129], v[178:181], v[206:209], v[126:129] cbsz:4 blgp:4
	v_med3_f32 v233, v66, v160, 0
	v_med3_f32 v230, v67, v160, 0
	v_med3_f32 v239, v40, v160, 0
	v_mfma_f32_16x16x128_f8f6f4 v[122:125], v[214:217], v[198:201], v[122:125] cbsz:4 blgp:4
	v_med3_f32 v240, v41, v160, 0
	v_cvt_scalef32_pk_fp4_f32 v232, v235, v238, v159 op_sel:[0,0,0,1]
	v_med3_f32 v234, v68, v160, 0
	v_med3_f32 v235, v69, v160, 0
	v_mfma_f32_16x16x128_f8f6f4 v[122:125], v[222:225], v[206:209], v[122:125] cbsz:4 blgp:4
	v_cvt_scalef32_pk_fp4_f32 v233, v233, v230, v159
	v_cvt_scalef32_pk_fp4_f32 v232, v239, v240, v159 op_sel:[0,0,1,1]
	v_med3_f32 v238, v70, v160, 0
	v_mfma_f32_16x16x128_f8f6f4 v[130:133], v[218:221], v[198:201], v[130:133] cbsz:4 blgp:4
	v_med3_f32 v239, v71, v160, 0
	v_cvt_scalef32_pk_fp4_f32 v233, v234, v235, v159 op_sel:[0,0,1,0]
	v_med3_f32 v234, v42, v160, 0
	v_med3_f32 v230, v43, v160, 0
	v_mfma_f32_16x16x128_f8f6f4 v[130:133], v[226:229], v[206:209], v[130:133] cbsz:4 blgp:4
	v_med3_f32 v240, v72, v160, 0
	v_med3_f32 v241, v73, v160, 0
	v_cvt_scalef32_pk_fp4_f32 v233, v238, v239, v159 op_sel:[0,0,0,1]
	v_mfma_f32_16x16x128_f8f6f4 v[138:141], v[166:169], v[202:205], v[138:141] cbsz:4 blgp:4
	v_med3_f32 v235, v44, v160, 0
	v_med3_f32 v238, v45, v160, 0
	v_cvt_scalef32_pk_fp4_f32 v234, v234, v230, v159
	v_cvt_scalef32_pk_fp4_f32 v233, v240, v241, v159 op_sel:[0,0,1,1]
	v_mfma_f32_16x16x128_f8f6f4 v[138:141], v[174:177], v[210:213], v[138:141] cbsz:4 blgp:4
	v_med3_f32 v239, v46, v160, 0
	v_med3_f32 v240, v47, v160, 0
	v_cvt_scalef32_pk_fp4_f32 v234, v235, v238, v159 op_sel:[0,0,1,0]
	v_mfma_f32_16x16x128_f8f6f4 v[82:85], v[170:173], v[202:205], v[82:85] cbsz:4 blgp:4
	v_med3_f32 v235, v74, v160, 0
	v_med3_f32 v230, v75, v160, 0
	v_med3_f32 v241, v48, v160, 0
	v_med3_f32 v242, v49, v160, 0
	v_mfma_f32_16x16x128_f8f6f4 v[82:85], v[178:181], v[210:213], v[82:85] cbsz:4 blgp:4
	v_cvt_scalef32_pk_fp4_f32 v234, v239, v240, v159 op_sel:[0,0,0,1]
	v_med3_f32 v238, v76, v160, 0
	v_med3_f32 v239, v77, v160, 0
	v_mfma_f32_16x16x128_f8f6f4 v[134:137], v[214:217], v[202:205], v[134:137] cbsz:4 blgp:4
	v_cvt_scalef32_pk_fp4_f32 v235, v235, v230, v159
	v_cvt_scalef32_pk_fp4_f32 v234, v241, v242, v159 op_sel:[0,0,1,1]
	v_med3_f32 v240, v78, v160, 0
	v_med3_f32 v241, v79, v160, 0
	v_mfma_f32_16x16x128_f8f6f4 v[134:137], v[222:225], v[210:213], v[134:137] cbsz:4 blgp:4
	v_cvt_scalef32_pk_fp4_f32 v235, v238, v239, v159 op_sel:[0,0,1,0]
	v_med3_f32 v242, v80, v160, 0
	v_med3_f32 v243, v81, v160, 0
	v_mfma_f32_16x16x128_f8f6f4 v[142:145], v[218:221], v[202:205], v[142:145] cbsz:4 blgp:4
	v_cvt_scalef32_pk_fp4_f32 v235, v240, v241, v159 op_sel:[0,0,0,1]
	v_or_b32_e32 v230, v244, v158
	v_cvt_scalef32_pk_fp4_f32 v235, v242, v243, v159 op_sel:[0,0,1,1]
	v_mad_i64_i32 v[238:239], s[84:85], v230, s12, v[236:237]
	v_mfma_f32_16x16x128_f8f6f4 v[142:145], v[226:229], v[210:213], v[142:145] cbsz:4 blgp:4
	v_permlane16_swap_b32_e32 v232, v234
	v_permlane16_swap_b32_e32 v233, v235
	v_lshl_add_u64 v[238:239], v[238:239], 0, v[246:247]
	global_store_dwordx4 v[238:239], v[232:235], off
	s_setprio 0
	s_add_i32 s40, s81, 2
	s_add_u32 s29, s29, 0x100
	s_addc_u32 s78, s78, 0
	s_add_u32 s79, s79, 0x100
	s_addc_u32 s80, s80, 0
	s_add_u32 s38, s38, 0x100
	s_addc_u32 s39, s39, 0
	s_cmp_ge_i32 s81, s63
	s_barrier
	s_branch .Lep_half_4

	.amdhsa_kernel _Z6k_gemmI4Epi8ILi0ELb1ELb1EEEv4GemmT_iiii
		.amdhsa_group_segment_fixed_size 0
		.amdhsa_private_segment_fixed_size 0
		.amdhsa_kernarg_size 328
		.amdhsa_user_sgpr_count 2
		.amdhsa_user_sgpr_dispatch_ptr 0
		.amdhsa_user_sgpr_queue_ptr 0
		.amdhsa_user_sgpr_kernarg_segment_ptr 1
		.amdhsa_user_sgpr_dispatch_id 0
		.amdhsa_user_sgpr_kernarg_preload_length 0
		.amdhsa_user_sgpr_kernarg_preload_offset 0
		.amdhsa_user_sgpr_private_segment_size 0
		.amdhsa_uses_dynamic_stack 0
		.amdhsa_enable_private_segment 0
		.amdhsa_system_sgpr_workgroup_id_x 1
		.amdhsa_system_sgpr_workgroup_id_y 0
		.amdhsa_system_sgpr_workgroup_id_z 0
		.amdhsa_system_sgpr_workgroup_info 0
		.amdhsa_system_vgpr_workitem_id 0
		.amdhsa_next_free_vgpr 248
		.amdhsa_next_free_sgpr 86
		.amdhsa_accum_offset 248
		.amdhsa_reserve_vcc 1
		.amdhsa_float_round_mode_32 0
		.amdhsa_float_round_mode_16_64 0
		.amdhsa_float_denorm_mode_32 3
		.amdhsa_float_denorm_mode_16_64 3
		.amdhsa_dx10_clamp 1
		.amdhsa_ieee_mode 1
		.amdhsa_fp16_overflow 0
		.amdhsa_tg_split 0
		.amdhsa_exception_fp_ieee_invalid_op 0
		.amdhsa_exception_fp_denorm_src 0
		.amdhsa_exception_fp_ieee_div_zero 0
		.amdhsa_exception_fp_ieee_overflow 0
		.amdhsa_exception_fp_ieee_underflow 0
		.amdhsa_exception_fp_ieee_inexact 0
		.amdhsa_exception_int_div_zero 0
	.end_amdhsa_kernel

.Lfunc_end4:
	.size	_Z6k_gemmI4Epi8ILi0ELb1ELb1EEEv4GemmT_iiii, .Lfunc_end4-_Z6k_gemmI4Epi8ILi0ELb1ELb1EEEv4GemmT_iiii
	.set _Z6k_gemmI4Epi8ILi0ELb1ELb1EEEv4GemmT_iiii.num_vgpr, 248
	.set _Z6k_gemmI4Epi8ILi0ELb1ELb1EEEv4GemmT_iiii.num_agpr, 0
	.set _Z6k_gemmI4Epi8ILi0ELb1ELb1EEEv4GemmT_iiii.numbered_sgpr, 86
	.set _Z6k_gemmI4Epi8ILi0ELb1ELb1EEEv4GemmT_iiii.num_named_barrier, 0
	.set _Z6k_gemmI4Epi8ILi0ELb1ELb1EEEv4GemmT_iiii.private_seg_size, 0
	.set _Z6k_gemmI4Epi8ILi0ELb1ELb1EEEv4GemmT_iiii.uses_vcc, 1
	.set _Z6k_gemmI4Epi8ILi0ELb1ELb1EEEv4GemmT_iiii.uses_flat_scratch, 0
	.set _Z6k_gemmI4Epi8ILi0ELb1ELb1EEEv4GemmT_iiii.has_dyn_sized_stack, 0
	.set _Z6k_gemmI4Epi8ILi0ELb1ELb1EEEv4GemmT_iiii.has_recursion, 0
	.set _Z6k_gemmI4Epi8ILi0ELb1ELb1EEEv4GemmT_iiii.has_indirect_call, 0

.Lrs_a_5:
	s_add_u32 s82, s42, s22
	s_addc_u32 s83, s43, s23
	s_add_u32 s29, s42, 0x100
	s_addc_u32 s46, s43, 0
	s_and_b64 s[44:45], s[14:15], exec
	ds_read_b128 v[82:85], v163
	ds_read_b128 v[94:97], v163 offset:2048
	ds_read_b128 v[102:105], v164
	ds_read_b128 v[110:113], v164 offset:2048
	s_cselect_b32 s49, s39, s46
	s_cselect_b32 s48, s38, s29
	s_add_u32 s29, s40, 0x100
	s_addc_u32 s46, s41, 0
	s_and_b64 s[44:45], s[14:15], exec
	s_cselect_b32 s51, s5, s46
	s_cselect_b32 s50, s4, s29
	s_add_u32 s46, s48, 0x80
	s_addc_u32 s47, s49, 0
	s_add_u32 s44, s50, 0x80
	s_addc_u32 s45, s51, 0
	ds_read_b128 v[58:61], v165
	ds_read_b128 v[66:69], v165 offset:2048
	ds_read_b128 v[62:65], v166
	ds_read_b128 v[70:73], v166 offset:2048
	ds_read_b128 v[74:77], v165 offset:4096
	ds_read_b128 v[86:89], v165 offset:6144
	ds_read_b128 v[78:81], v166 offset:4096
	ds_read_b128 v[90:93], v166 offset:6144
	s_add_u32 s80, s82, 0x80
	s_addc_u32 s81, s83, 0
	s_mov_b32 m0, s71
	s_nop 0
	global_load_lds_dwordx4 v146, s[80:81]
	s_mov_b32 m0, s72
	s_nop 0
	global_load_lds_dwordx4 v150, s[80:81]
	s_waitcnt lgkmcnt(8)
	ds_read_b128 v[142:145], v163 offset:16384
	ds_read_b128 v[156:159], v163 offset:18432
	ds_read_b128 v[168:171], v164 offset:16384
	ds_read_b128 v[172:175], v164 offset:18432
	s_waitcnt vmcnt(8)
	s_waitcnt lgkmcnt(0)
	s_barrier
	s_waitcnt lgkmcnt(0)
	s_waitcnt vmcnt(16)
	v_mov_b32_e32 v1, v0
	v_pk_mul_f32 v[16:17], v[0:1], v[16:17]
	v_pk_mul_f32 v[14:15], v[154:155], v[14:15]
	v_pk_mul_f32 v[12:13], v[0:1], v[12:13]
	v_pk_mul_f32 v[10:11], v[154:155], v[10:11]
	v_pk_mul_f32 v[8:9], v[0:1], v[8:9]
	v_pk_mul_f32 v[6:7], v[154:155], v[6:7]
	v_pk_mul_f32 v[4:5], v[0:1], v[4:5]
	v_pk_mul_f32 v[2:3], v[154:155], v[2:3]
	s_setprio 1
	v_mfma_f32_16x16x128_f8f6f4 v[18:21], v[82:85], v[58:61], v[14:17] cbsz:4 blgp:4
	v_mfma_f32_16x16x128_f8f6f4 v[18:21], v[102:105], v[62:65], v[18:21] cbsz:4 blgp:4
	v_mfma_f32_16x16x128_f8f6f4 v[22:25], v[94:97], v[58:61], v[10:13] cbsz:4 blgp:4
	v_mfma_f32_16x16x128_f8f6f4 v[22:25], v[110:113], v[62:65], v[22:25] cbsz:4 blgp:4
	v_mfma_f32_16x16x128_f8f6f4 v[50:53], v[142:145], v[58:61], v[6:9] cbsz:4 blgp:4
	v_mfma_f32_16x16x128_f8f6f4 v[50:53], v[168:171], v[62:65], v[50:53] cbsz:4 blgp:4
	v_mfma_f32_16x16x128_f8f6f4 v[54:57], v[156:159], v[58:61], v[2:5] cbsz:4 blgp:4
	v_mfma_f32_16x16x128_f8f6f4 v[54:57], v[172:175], v[62:65], v[54:57] cbsz:4 blgp:4
	v_mfma_f32_16x16x128_f8f6f4 v[26:29], v[82:85], v[66:69], v[14:17] cbsz:4 blgp:4
	v_mfma_f32_16x16x128_f8f6f4 v[26:29], v[102:105], v[70:73], v[26:29] cbsz:4 blgp:4
	v_mfma_f32_16x16x128_f8f6f4 v[30:33], v[94:97], v[66:69], v[10:13] cbsz:4 blgp:4
	v_mfma_f32_16x16x128_f8f6f4 v[30:33], v[110:113], v[70:73], v[30:33] cbsz:4 blgp:4
	v_mfma_f32_16x16x128_f8f6f4 v[58:61], v[142:145], v[66:69], v[6:9] cbsz:4 blgp:4
	v_mfma_f32_16x16x128_f8f6f4 v[58:61], v[168:171], v[70:73], v[58:61] cbsz:4 blgp:4
	v_mfma_f32_16x16x128_f8f6f4 v[62:65], v[156:159], v[66:69], v[2:5] cbsz:4 blgp:4
	v_mfma_f32_16x16x128_f8f6f4 v[62:65], v[172:175], v[70:73], v[62:65] cbsz:4 blgp:4
	v_mfma_f32_16x16x128_f8f6f4 v[34:37], v[82:85], v[74:77], v[14:17] cbsz:4 blgp:4
	v_mfma_f32_16x16x128_f8f6f4 v[34:37], v[102:105], v[78:81], v[34:37] cbsz:4 blgp:4
	v_mfma_f32_16x16x128_f8f6f4 v[38:41], v[94:97], v[74:77], v[10:13] cbsz:4 blgp:4
	v_mfma_f32_16x16x128_f8f6f4 v[38:41], v[110:113], v[78:81], v[38:41] cbsz:4 blgp:4
	v_mfma_f32_16x16x128_f8f6f4 v[66:69], v[142:145], v[74:77], v[6:9] cbsz:4 blgp:4
	v_mfma_f32_16x16x128_f8f6f4 v[66:69], v[168:171], v[78:81], v[66:69] cbsz:4 blgp:4
	v_mfma_f32_16x16x128_f8f6f4 v[70:73], v[156:159], v[74:77], v[2:5] cbsz:4 blgp:4
	v_mfma_f32_16x16x128_f8f6f4 v[70:73], v[172:175], v[78:81], v[70:73] cbsz:4 blgp:4
	v_mfma_f32_16x16x128_f8f6f4 v[42:45], v[82:85], v[86:89], v[14:17] cbsz:4 blgp:4
	v_mfma_f32_16x16x128_f8f6f4 v[42:45], v[102:105], v[90:93], v[42:45] cbsz:4 blgp:4
	v_mfma_f32_16x16x128_f8f6f4 v[46:49], v[94:97], v[86:89], v[10:13] cbsz:4 blgp:4
	v_mfma_f32_16x16x128_f8f6f4 v[46:49], v[110:113], v[90:93], v[46:49] cbsz:4 blgp:4
	v_mfma_f32_16x16x128_f8f6f4 v[74:77], v[142:145], v[86:89], v[6:9] cbsz:4 blgp:4
	v_mfma_f32_16x16x128_f8f6f4 v[74:77], v[168:171], v[90:93], v[74:77] cbsz:4 blgp:4
	v_mfma_f32_16x16x128_f8f6f4 v[78:81], v[156:159], v[86:89], v[2:5] cbsz:4 blgp:4
	v_mfma_f32_16x16x128_f8f6f4 v[78:81], v[172:175], v[90:93], v[78:81] cbsz:4 blgp:4
	s_setprio 0
	s_barrier
	s_mov_b32 m0, s56
	s_nop 0
	global_load_lds_dwordx4 v148, s[50:51]
	s_mov_b32 m0, s57
	s_nop 0
	global_load_lds_dwordx4 v152, s[50:51]
	ds_read_b128 v[114:117], v165 offset:16384
	ds_read_b128 v[122:125], v165 offset:18432
	ds_read_b128 v[130:133], v166 offset:16384
	ds_read_b128 v[134:137], v166 offset:18432
	ds_read_b128 v[176:179], v165 offset:20480
	ds_read_b128 v[180:183], v165 offset:22528
	ds_read_b128 v[184:187], v166 offset:20480
	ds_read_b128 v[188:191], v166 offset:22528
	s_mov_b32 m0, s55
	s_nop 0
	global_load_lds_dwordx4 v146, s[48:49]
	s_mov_b32 m0, s58
	s_nop 0
	global_load_lds_dwordx4 v150, s[48:49]
	s_add_u32 s50, s50, s24
	s_addc_u32 s51, s51, s25
	s_mov_b32 m0, s59
	s_nop 0
	global_load_lds_dwordx4 v148, s[50:51]
	s_mov_b32 m0, s60
	s_nop 0
	global_load_lds_dwordx4 v152, s[50:51]
	s_waitcnt vmcnt(8)
	s_waitcnt lgkmcnt(0)
	s_barrier
	s_setprio 1
	v_mfma_f32_16x16x128_f8f6f4 v[86:89], v[82:85], v[114:117], v[14:17] cbsz:4 blgp:4
	v_mfma_f32_16x16x128_f8f6f4 v[86:89], v[102:105], v[130:133], v[86:89] cbsz:4 blgp:4
	v_mfma_f32_16x16x128_f8f6f4 v[90:93], v[94:97], v[114:117], v[10:13] cbsz:4 blgp:4
	v_mfma_f32_16x16x128_f8f6f4 v[90:93], v[110:113], v[130:133], v[90:93] cbsz:4 blgp:4
	v_mfma_f32_16x16x128_f8f6f4 v[98:101], v[82:85], v[122:125], v[14:17] cbsz:4 blgp:4
	v_mfma_f32_16x16x128_f8f6f4 v[98:101], v[102:105], v[134:137], v[98:101] cbsz:4 blgp:4
	v_mfma_f32_16x16x128_f8f6f4 v[106:109], v[94:97], v[122:125], v[10:13] cbsz:4 blgp:4
	v_mfma_f32_16x16x128_f8f6f4 v[106:109], v[110:113], v[134:137], v[106:109] cbsz:4 blgp:4
	v_mfma_f32_16x16x128_f8f6f4 v[118:121], v[82:85], v[176:179], v[14:17] cbsz:4 blgp:4
	v_mfma_f32_16x16x128_f8f6f4 v[118:121], v[102:105], v[184:187], v[118:121] cbsz:4 blgp:4
	v_mfma_f32_16x16x128_f8f6f4 v[126:129], v[94:97], v[176:179], v[10:13] cbsz:4 blgp:4
	v_mfma_f32_16x16x128_f8f6f4 v[126:129], v[110:113], v[184:187], v[126:129] cbsz:4 blgp:4
	v_mfma_f32_16x16x128_f8f6f4 v[138:141], v[82:85], v[180:183], v[14:17] cbsz:4 blgp:4
	v_mfma_f32_16x16x128_f8f6f4 v[138:141], v[102:105], v[188:191], v[138:141] cbsz:4 blgp:4
	v_mfma_f32_16x16x128_f8f6f4 v[82:85], v[94:97], v[180:183], v[10:13] cbsz:4 blgp:4
	v_mfma_f32_16x16x128_f8f6f4 v[82:85], v[110:113], v[188:191], v[82:85] cbsz:4 blgp:4
	v_mfma_f32_16x16x128_f8f6f4 v[94:97], v[142:145], v[114:117], v[6:9] cbsz:4 blgp:4
	v_mfma_f32_16x16x128_f8f6f4 v[94:97], v[168:171], v[130:133], v[94:97] cbsz:4 blgp:4
	v_mfma_f32_16x16x128_f8f6f4 v[102:105], v[156:159], v[114:117], v[2:5] cbsz:4 blgp:4
	v_mfma_f32_16x16x128_f8f6f4 v[102:105], v[172:175], v[130:133], v[102:105] cbsz:4 blgp:4
	v_mfma_f32_16x16x128_f8f6f4 v[110:113], v[142:145], v[122:125], v[6:9] cbsz:4 blgp:4
	v_mfma_f32_16x16x128_f8f6f4 v[110:113], v[168:171], v[134:137], v[110:113] cbsz:4 blgp:4
	v_mfma_f32_16x16x128_f8f6f4 v[114:117], v[156:159], v[122:125], v[2:5] cbsz:4 blgp:4
	v_mfma_f32_16x16x128_f8f6f4 v[114:117], v[172:175], v[134:137], v[114:117] cbsz:4 blgp:4
	v_mfma_f32_16x16x128_f8f6f4 v[122:125], v[142:145], v[176:179], v[6:9] cbsz:4 blgp:4
	v_mfma_f32_16x16x128_f8f6f4 v[122:125], v[168:171], v[184:187], v[122:125] cbsz:4 blgp:4
	v_mfma_f32_16x16x128_f8f6f4 v[130:133], v[156:159], v[176:179], v[2:5] cbsz:4 blgp:4
	v_mfma_f32_16x16x128_f8f6f4 v[130:133], v[172:175], v[184:187], v[130:133] cbsz:4 blgp:4
	v_mfma_f32_16x16x128_f8f6f4 v[134:137], v[142:145], v[180:183], v[6:9] cbsz:4 blgp:4
	v_mfma_f32_16x16x128_f8f6f4 v[134:137], v[168:171], v[188:191], v[134:137] cbsz:4 blgp:4
	v_mfma_f32_16x16x128_f8f6f4 v[142:145], v[156:159], v[180:183], v[2:5] cbsz:4 blgp:4
	v_mfma_f32_16x16x128_f8f6f4 v[142:145], v[172:175], v[188:191], v[142:145] cbsz:4 blgp:4
	s_setprio 0
	s_barrier
	ds_read_b128 v[156:159], v163 offset:32768
	ds_read_b128 v[168:171], v163 offset:34816
	ds_read_b128 v[172:175], v164 offset:32768
	ds_read_b128 v[176:179], v164 offset:34816
	ds_read_b128 v[180:183], v165 offset:32768
	ds_read_b128 v[184:187], v165 offset:34816
	ds_read_b128 v[188:191], v166 offset:32768
	ds_read_b128 v[192:195], v166 offset:34816
	ds_read_b128 v[196:199], v165 offset:36864
	ds_read_b128 v[200:203], v165 offset:38912
	ds_read_b128 v[204:207], v166 offset:36864
	ds_read_b128 v[208:211], v166 offset:38912
	s_add_u32 s48, s48, s22
	s_addc_u32 s49, s49, s23
	s_mov_b32 m0, s61
	s_nop 0
	global_load_lds_dwordx4 v146, s[48:49]
	s_mov_b32 m0, s62
	s_nop 0
	global_load_lds_dwordx4 v150, s[48:49]
	s_waitcnt lgkmcnt(8)
	ds_read_b128 v[212:215], v163 offset:49152
	ds_read_b128 v[216:219], v163 offset:51200
	ds_read_b128 v[220:223], v164 offset:49152
	ds_read_b128 v[224:227], v164 offset:51200
	s_waitcnt vmcnt(8)
	s_waitcnt lgkmcnt(0)
	s_barrier
	s_waitcnt lgkmcnt(0)
	s_setprio 1
	v_mfma_f32_16x16x128_f8f6f4 v[18:21], v[156:159], v[180:183], v[18:21] cbsz:4 blgp:4
	v_mfma_f32_16x16x128_f8f6f4 v[18:21], v[172:175], v[188:191], v[18:21] cbsz:4 blgp:4
	v_mfma_f32_16x16x128_f8f6f4 v[22:25], v[168:171], v[180:183], v[22:25] cbsz:4 blgp:4
	v_mfma_f32_16x16x128_f8f6f4 v[22:25], v[176:179], v[188:191], v[22:25] cbsz:4 blgp:4
	v_mfma_f32_16x16x128_f8f6f4 v[50:53], v[212:215], v[180:183], v[50:53] cbsz:4 blgp:4
	v_mfma_f32_16x16x128_f8f6f4 v[50:53], v[220:223], v[188:191], v[50:53] cbsz:4 blgp:4
	v_mfma_f32_16x16x128_f8f6f4 v[54:57], v[216:219], v[180:183], v[54:57] cbsz:4 blgp:4
	v_mfma_f32_16x16x128_f8f6f4 v[54:57], v[224:227], v[188:191], v[54:57] cbsz:4 blgp:4
	v_mfma_f32_16x16x128_f8f6f4 v[26:29], v[156:159], v[184:187], v[26:29] cbsz:4 blgp:4
	v_mfma_f32_16x16x128_f8f6f4 v[26:29], v[172:175], v[192:195], v[26:29] cbsz:4 blgp:4
	v_mfma_f32_16x16x128_f8f6f4 v[30:33], v[168:171], v[184:187], v[30:33] cbsz:4 blgp:4
	v_mfma_f32_16x16x128_f8f6f4 v[30:33], v[176:179], v[192:195], v[30:33] cbsz:4 blgp:4
	v_mfma_f32_16x16x128_f8f6f4 v[58:61], v[212:215], v[184:187], v[58:61] cbsz:4 blgp:4
	v_mfma_f32_16x16x128_f8f6f4 v[58:61], v[220:223], v[192:195], v[58:61] cbsz:4 blgp:4
	v_mfma_f32_16x16x128_f8f6f4 v[62:65], v[216:219], v[184:187], v[62:65] cbsz:4 blgp:4
	v_mfma_f32_16x16x128_f8f6f4 v[62:65], v[224:227], v[192:195], v[62:65] cbsz:4 blgp:4
	v_mfma_f32_16x16x128_f8f6f4 v[34:37], v[156:159], v[196:199], v[34:37] cbsz:4 blgp:4
	v_mfma_f32_16x16x128_f8f6f4 v[34:37], v[172:175], v[204:207], v[34:37] cbsz:4 blgp:4
	v_mfma_f32_16x16x128_f8f6f4 v[38:41], v[168:171], v[196:199], v[38:41] cbsz:4 blgp:4
	v_mfma_f32_16x16x128_f8f6f4 v[38:41], v[176:179], v[204:207], v[38:41] cbsz:4 blgp:4
	v_mfma_f32_16x16x128_f8f6f4 v[66:69], v[212:215], v[196:199], v[66:69] cbsz:4 blgp:4
	v_mfma_f32_16x16x128_f8f6f4 v[66:69], v[220:223], v[204:207], v[66:69] cbsz:4 blgp:4
	v_mfma_f32_16x16x128_f8f6f4 v[70:73], v[216:219], v[196:199], v[70:73] cbsz:4 blgp:4
	v_mfma_f32_16x16x128_f8f6f4 v[70:73], v[224:227], v[204:207], v[70:73] cbsz:4 blgp:4
	v_mfma_f32_16x16x128_f8f6f4 v[42:45], v[156:159], v[200:203], v[42:45] cbsz:4 blgp:4
	v_mfma_f32_16x16x128_f8f6f4 v[42:45], v[172:175], v[208:211], v[42:45] cbsz:4 blgp:4
	v_mfma_f32_16x16x128_f8f6f4 v[46:49], v[168:171], v[200:203], v[46:49] cbsz:4 blgp:4
	v_mfma_f32_16x16x128_f8f6f4 v[46:49], v[176:179], v[208:211], v[46:49] cbsz:4 blgp:4
	v_mfma_f32_16x16x128_f8f6f4 v[74:77], v[212:215], v[200:203], v[74:77] cbsz:4 blgp:4
	v_mfma_f32_16x16x128_f8f6f4 v[74:77], v[220:223], v[208:211], v[74:77] cbsz:4 blgp:4
	v_mfma_f32_16x16x128_f8f6f4 v[78:81], v[216:219], v[200:203], v[78:81] cbsz:4 blgp:4
	v_mfma_f32_16x16x128_f8f6f4 v[78:81], v[224:227], v[208:211], v[78:81] cbsz:4 blgp:4
	s_setprio 0
	s_barrier
	s_mov_b32 m0, s65
	s_nop 0
	global_load_lds_dwordx4 v148, s[44:45]
	s_mov_b32 m0, s66
	s_nop 0
	global_load_lds_dwordx4 v152, s[44:45]
	ds_read_b128 v[180:183], v165 offset:49152
	ds_read_b128 v[184:187], v165 offset:51200
	ds_read_b128 v[188:191], v166 offset:49152
	ds_read_b128 v[192:195], v166 offset:51200
	ds_read_b128 v[196:199], v165 offset:53248
	ds_read_b128 v[200:203], v165 offset:55296
	ds_read_b128 v[204:207], v166 offset:53248
	ds_read_b128 v[208:211], v166 offset:55296
	s_mov_b32 m0, s67
	s_nop 0
	global_load_lds_dwordx4 v146, s[46:47]
	s_mov_b32 m0, s68
	s_nop 0
	global_load_lds_dwordx4 v150, s[46:47]
	s_add_u32 s44, s44, s24
	s_addc_u32 s45, s45, s25
	s_mov_b32 m0, s69
	s_nop 0
	global_load_lds_dwordx4 v148, s[44:45]
	s_mov_b32 m0, s70
	s_nop 0
	global_load_lds_dwordx4 v152, s[44:45]
	s_waitcnt vmcnt(8)
	s_waitcnt lgkmcnt(0)
	s_barrier
	s_setprio 1
	v_mfma_f32_16x16x128_f8f6f4 v[86:89], v[156:159], v[180:183], v[86:89] cbsz:4 blgp:4
	v_mfma_f32_16x16x128_f8f6f4 v[86:89], v[172:175], v[188:191], v[86:89] cbsz:4 blgp:4
	v_mfma_f32_16x16x128_f8f6f4 v[90:93], v[168:171], v[180:183], v[90:93] cbsz:4 blgp:4
	v_mfma_f32_16x16x128_f8f6f4 v[90:93], v[176:179], v[188:191], v[90:93] cbsz:4 blgp:4
	v_mfma_f32_16x16x128_f8f6f4 v[94:97], v[212:215], v[180:183], v[94:97] cbsz:4 blgp:4
	v_mfma_f32_16x16x128_f8f6f4 v[94:97], v[220:223], v[188:191], v[94:97] cbsz:4 blgp:4
	v_mfma_f32_16x16x128_f8f6f4 v[102:105], v[216:219], v[180:183], v[102:105] cbsz:4 blgp:4
	v_mfma_f32_16x16x128_f8f6f4 v[102:105], v[224:227], v[188:191], v[102:105] cbsz:4 blgp:4
	v_mfma_f32_16x16x128_f8f6f4 v[98:101], v[156:159], v[184:187], v[98:101] cbsz:4 blgp:4
	v_mfma_f32_16x16x128_f8f6f4 v[98:101], v[172:175], v[192:195], v[98:101] cbsz:4 blgp:4
	v_mfma_f32_16x16x128_f8f6f4 v[106:109], v[168:171], v[184:187], v[106:109] cbsz:4 blgp:4
	v_mfma_f32_16x16x128_f8f6f4 v[106:109], v[176:179], v[192:195], v[106:109] cbsz:4 blgp:4
	v_mfma_f32_16x16x128_f8f6f4 v[110:113], v[212:215], v[184:187], v[110:113] cbsz:4 blgp:4
	v_mfma_f32_16x16x128_f8f6f4 v[110:113], v[220:223], v[192:195], v[110:113] cbsz:4 blgp:4
	v_mfma_f32_16x16x128_f8f6f4 v[114:117], v[216:219], v[184:187], v[114:117] cbsz:4 blgp:4
	v_mfma_f32_16x16x128_f8f6f4 v[114:117], v[224:227], v[192:195], v[114:117] cbsz:4 blgp:4
	v_mfma_f32_16x16x128_f8f6f4 v[118:121], v[156:159], v[196:199], v[118:121] cbsz:4 blgp:4
	v_mfma_f32_16x16x128_f8f6f4 v[118:121], v[172:175], v[204:207], v[118:121] cbsz:4 blgp:4
	v_mfma_f32_16x16x128_f8f6f4 v[126:129], v[168:171], v[196:199], v[126:129] cbsz:4 blgp:4
	v_mfma_f32_16x16x128_f8f6f4 v[126:129], v[176:179], v[204:207], v[126:129] cbsz:4 blgp:4
	v_mfma_f32_16x16x128_f8f6f4 v[122:125], v[212:215], v[196:199], v[122:125] cbsz:4 blgp:4
	v_mfma_f32_16x16x128_f8f6f4 v[122:125], v[220:223], v[204:207], v[122:125] cbsz:4 blgp:4
	v_mfma_f32_16x16x128_f8f6f4 v[130:133], v[216:219], v[196:199], v[130:133] cbsz:4 blgp:4
	v_mfma_f32_16x16x128_f8f6f4 v[130:133], v[224:227], v[204:207], v[130:133] cbsz:4 blgp:4
	v_mfma_f32_16x16x128_f8f6f4 v[138:141], v[156:159], v[200:203], v[138:141] cbsz:4 blgp:4
	v_mfma_f32_16x16x128_f8f6f4 v[138:141], v[172:175], v[208:211], v[138:141] cbsz:4 blgp:4
	v_mfma_f32_16x16x128_f8f6f4 v[82:85], v[168:171], v[200:203], v[82:85] cbsz:4 blgp:4
	v_mfma_f32_16x16x128_f8f6f4 v[82:85], v[176:179], v[208:211], v[82:85] cbsz:4 blgp:4
	v_mfma_f32_16x16x128_f8f6f4 v[134:137], v[212:215], v[200:203], v[134:137] cbsz:4 blgp:4
	v_mfma_f32_16x16x128_f8f6f4 v[134:137], v[220:223], v[208:211], v[134:137] cbsz:4 blgp:4
	v_mfma_f32_16x16x128_f8f6f4 v[142:145], v[216:219], v[200:203], v[142:145] cbsz:4 blgp:4
	v_mfma_f32_16x16x128_f8f6f4 v[142:145], v[224:227], v[208:211], v[142:145] cbsz:4 blgp:4
	s_setprio 0
	s_andn2_b64 vcc, exec, s[34:35]
	s_barrier
	s_cbranch_vccnz .LBB5_4
	s_ashr_i32 s29, s28, 31
	s_lshl_b64 s[44:45], s[28:29], 10
	s_add_u32 s44, s10, s44
	s_addc_u32 s45, s11, s45
	s_add_u32 s29, s42, 0x200
	s_addc_u32 s79, s43, 0
	s_add_u32 s80, s40, 0x200
	s_addc_u32 s81, s41, 0
	s_add_u32 s40, s82, 0x180
	s_addc_u32 s41, s83, 0
	s_mov_b32 s82, 4
	s_cmp_eq_u32 s64, s82
	s_cselect_b64 s[42:43], -1, 0
	s_cmp_lg_u32 s64, s82
	s_cbranch_scc1 .LBB5_15

.LBB5_15:
	ds_read_b128 v[156:159], v163
	ds_read_b128 v[168:171], v163 offset:2048
	ds_read_b128 v[172:175], v164
	ds_read_b128 v[176:179], v164 offset:2048
	s_and_b64 s[42:43], s[42:43], exec
	s_cselect_b32 s48, s38, s29
	s_cselect_b32 s49, s39, s79
	s_cselect_b32 s51, s5, s81
	s_cselect_b32 s50, s4, s80
	s_add_u32 s46, s48, 0x80
	s_addc_u32 s47, s49, 0
	s_add_u32 s42, s50, 0x80
	s_addc_u32 s43, s51, 0
	ds_read_b128 v[180:183], v165
	ds_read_b128 v[184:187], v165 offset:2048
	ds_read_b128 v[188:191], v166
	ds_read_b128 v[192:195], v166 offset:2048
	ds_read_b128 v[196:199], v165 offset:4096
	ds_read_b128 v[200:203], v165 offset:6144
	ds_read_b128 v[204:207], v166 offset:4096
	ds_read_b128 v[208:211], v166 offset:6144
	s_mov_b32 m0, s71
	s_nop 0
	global_load_lds_dwordx4 v146, s[40:41]
	s_mov_b32 m0, s72
	s_nop 0
	global_load_lds_dwordx4 v150, s[40:41]
	s_waitcnt lgkmcnt(8)
	ds_read_b128 v[212:215], v163 offset:16384
	ds_read_b128 v[216:219], v163 offset:18432
	ds_read_b128 v[220:223], v164 offset:16384
	ds_read_b128 v[224:227], v164 offset:18432
	s_waitcnt vmcnt(8)
	s_waitcnt lgkmcnt(0)
	s_barrier
	s_waitcnt lgkmcnt(0)
	s_setprio 1
	v_mfma_f32_16x16x128_f8f6f4 v[18:21], v[156:159], v[180:183], v[18:21] cbsz:4 blgp:4
	v_mfma_f32_16x16x128_f8f6f4 v[18:21], v[172:175], v[188:191], v[18:21] cbsz:4 blgp:4
	v_mfma_f32_16x16x128_f8f6f4 v[22:25], v[168:171], v[180:183], v[22:25] cbsz:4 blgp:4
	v_mfma_f32_16x16x128_f8f6f4 v[22:25], v[176:179], v[188:191], v[22:25] cbsz:4 blgp:4
	v_mfma_f32_16x16x128_f8f6f4 v[50:53], v[212:215], v[180:183], v[50:53] cbsz:4 blgp:4
	v_mfma_f32_16x16x128_f8f6f4 v[50:53], v[220:223], v[188:191], v[50:53] cbsz:4 blgp:4
	v_mfma_f32_16x16x128_f8f6f4 v[54:57], v[216:219], v[180:183], v[54:57] cbsz:4 blgp:4
	v_mfma_f32_16x16x128_f8f6f4 v[54:57], v[224:227], v[188:191], v[54:57] cbsz:4 blgp:4
	v_mfma_f32_16x16x128_f8f6f4 v[26:29], v[156:159], v[184:187], v[26:29] cbsz:4 blgp:4
	v_mfma_f32_16x16x128_f8f6f4 v[26:29], v[172:175], v[192:195], v[26:29] cbsz:4 blgp:4
	v_mfma_f32_16x16x128_f8f6f4 v[30:33], v[168:171], v[184:187], v[30:33] cbsz:4 blgp:4
	v_mfma_f32_16x16x128_f8f6f4 v[30:33], v[176:179], v[192:195], v[30:33] cbsz:4 blgp:4
	v_mfma_f32_16x16x128_f8f6f4 v[58:61], v[212:215], v[184:187], v[58:61] cbsz:4 blgp:4
	v_mfma_f32_16x16x128_f8f6f4 v[58:61], v[220:223], v[192:195], v[58:61] cbsz:4 blgp:4
	v_mfma_f32_16x16x128_f8f6f4 v[62:65], v[216:219], v[184:187], v[62:65] cbsz:4 blgp:4
	v_mfma_f32_16x16x128_f8f6f4 v[62:65], v[224:227], v[192:195], v[62:65] cbsz:4 blgp:4
	v_mfma_f32_16x16x128_f8f6f4 v[34:37], v[156:159], v[196:199], v[34:37] cbsz:4 blgp:4
	v_mfma_f32_16x16x128_f8f6f4 v[34:37], v[172:175], v[204:207], v[34:37] cbsz:4 blgp:4
	v_mfma_f32_16x16x128_f8f6f4 v[38:41], v[168:171], v[196:199], v[38:41] cbsz:4 blgp:4
	v_mfma_f32_16x16x128_f8f6f4 v[38:41], v[176:179], v[204:207], v[38:41] cbsz:4 blgp:4
	v_mfma_f32_16x16x128_f8f6f4 v[66:69], v[212:215], v[196:199], v[66:69] cbsz:4 blgp:4
	v_mfma_f32_16x16x128_f8f6f4 v[66:69], v[220:223], v[204:207], v[66:69] cbsz:4 blgp:4
	v_mfma_f32_16x16x128_f8f6f4 v[70:73], v[216:219], v[196:199], v[70:73] cbsz:4 blgp:4
	v_mfma_f32_16x16x128_f8f6f4 v[70:73], v[224:227], v[204:207], v[70:73] cbsz:4 blgp:4
	v_mfma_f32_16x16x128_f8f6f4 v[42:45], v[156:159], v[200:203], v[42:45] cbsz:4 blgp:4
	v_mfma_f32_16x16x128_f8f6f4 v[42:45], v[172:175], v[208:211], v[42:45] cbsz:4 blgp:4
	v_mfma_f32_16x16x128_f8f6f4 v[46:49], v[168:171], v[200:203], v[46:49] cbsz:4 blgp:4
	v_mfma_f32_16x16x128_f8f6f4 v[46:49], v[176:179], v[208:211], v[46:49] cbsz:4 blgp:4
	v_mfma_f32_16x16x128_f8f6f4 v[74:77], v[212:215], v[200:203], v[74:77] cbsz:4 blgp:4
	v_mfma_f32_16x16x128_f8f6f4 v[74:77], v[220:223], v[208:211], v[74:77] cbsz:4 blgp:4
	v_mfma_f32_16x16x128_f8f6f4 v[78:81], v[216:219], v[200:203], v[78:81] cbsz:4 blgp:4
	v_mfma_f32_16x16x128_f8f6f4 v[78:81], v[224:227], v[208:211], v[78:81] cbsz:4 blgp:4
	s_setprio 0
	s_barrier
	s_mov_b32 m0, s56
	s_nop 0
	global_load_lds_dwordx4 v148, s[50:51]
	s_mov_b32 m0, s57
	s_nop 0
	global_load_lds_dwordx4 v152, s[50:51]
	ds_read_b128 v[180:183], v165 offset:16384
	ds_read_b128 v[184:187], v165 offset:18432
	ds_read_b128 v[188:191], v166 offset:16384
	ds_read_b128 v[192:195], v166 offset:18432
	ds_read_b128 v[196:199], v165 offset:20480
	ds_read_b128 v[200:203], v165 offset:22528
	ds_read_b128 v[204:207], v166 offset:20480
	ds_read_b128 v[208:211], v166 offset:22528
	s_mov_b32 m0, s55
	s_nop 0
	global_load_lds_dwordx4 v146, s[48:49]
	s_mov_b32 m0, s58
	s_nop 0
	global_load_lds_dwordx4 v150, s[48:49]
	s_add_u32 s50, s50, s24
	s_addc_u32 s51, s51, s25
	s_mov_b32 m0, s59
	s_nop 0
	global_load_lds_dwordx4 v148, s[50:51]
	s_mov_b32 m0, s60
	s_nop 0
	global_load_lds_dwordx4 v152, s[50:51]
	s_waitcnt vmcnt(8)
	s_waitcnt lgkmcnt(0)
	s_barrier
	s_setprio 1
	v_mfma_f32_16x16x128_f8f6f4 v[86:89], v[156:159], v[180:183], v[86:89] cbsz:4 blgp:4
	v_mfma_f32_16x16x128_f8f6f4 v[86:89], v[172:175], v[188:191], v[86:89] cbsz:4 blgp:4
	v_mfma_f32_16x16x128_f8f6f4 v[90:93], v[168:171], v[180:183], v[90:93] cbsz:4 blgp:4
	v_mfma_f32_16x16x128_f8f6f4 v[90:93], v[176:179], v[188:191], v[90:93] cbsz:4 blgp:4
	v_mfma_f32_16x16x128_f8f6f4 v[94:97], v[212:215], v[180:183], v[94:97] cbsz:4 blgp:4
	v_mfma_f32_16x16x128_f8f6f4 v[94:97], v[220:223], v[188:191], v[94:97] cbsz:4 blgp:4
	v_mfma_f32_16x16x128_f8f6f4 v[102:105], v[216:219], v[180:183], v[102:105] cbsz:4 blgp:4
	v_mfma_f32_16x16x128_f8f6f4 v[102:105], v[224:227], v[188:191], v[102:105] cbsz:4 blgp:4
	v_mfma_f32_16x16x128_f8f6f4 v[98:101], v[156:159], v[184:187], v[98:101] cbsz:4 blgp:4
	v_mfma_f32_16x16x128_f8f6f4 v[98:101], v[172:175], v[192:195], v[98:101] cbsz:4 blgp:4
	v_mfma_f32_16x16x128_f8f6f4 v[106:109], v[168:171], v[184:187], v[106:109] cbsz:4 blgp:4
	v_mfma_f32_16x16x128_f8f6f4 v[106:109], v[176:179], v[192:195], v[106:109] cbsz:4 blgp:4
	v_mfma_f32_16x16x128_f8f6f4 v[110:113], v[212:215], v[184:187], v[110:113] cbsz:4 blgp:4
	v_mfma_f32_16x16x128_f8f6f4 v[110:113], v[220:223], v[192:195], v[110:113] cbsz:4 blgp:4
	v_mfma_f32_16x16x128_f8f6f4 v[114:117], v[216:219], v[184:187], v[114:117] cbsz:4 blgp:4
	v_mfma_f32_16x16x128_f8f6f4 v[114:117], v[224:227], v[192:195], v[114:117] cbsz:4 blgp:4
	v_mfma_f32_16x16x128_f8f6f4 v[118:121], v[156:159], v[196:199], v[118:121] cbsz:4 blgp:4
	v_mfma_f32_16x16x128_f8f6f4 v[118:121], v[172:175], v[204:207], v[118:121] cbsz:4 blgp:4
	v_mfma_f32_16x16x128_f8f6f4 v[126:129], v[168:171], v[196:199], v[126:129] cbsz:4 blgp:4
	v_mfma_f32_16x16x128_f8f6f4 v[126:129], v[176:179], v[204:207], v[126:129] cbsz:4 blgp:4
	v_mfma_f32_16x16x128_f8f6f4 v[122:125], v[212:215], v[196:199], v[122:125] cbsz:4 blgp:4
	v_mfma_f32_16x16x128_f8f6f4 v[122:125], v[220:223], v[204:207], v[122:125] cbsz:4 blgp:4
	v_mfma_f32_16x16x128_f8f6f4 v[130:133], v[216:219], v[196:199], v[130:133] cbsz:4 blgp:4
	v_mfma_f32_16x16x128_f8f6f4 v[130:133], v[224:227], v[204:207], v[130:133] cbsz:4 blgp:4
	v_mfma_f32_16x16x128_f8f6f4 v[138:141], v[156:159], v[200:203], v[138:141] cbsz:4 blgp:4
	v_mfma_f32_16x16x128_f8f6f4 v[138:141], v[172:175], v[208:211], v[138:141] cbsz:4 blgp:4
	v_mfma_f32_16x16x128_f8f6f4 v[82:85], v[168:171], v[200:203], v[82:85] cbsz:4 blgp:4
	v_mfma_f32_16x16x128_f8f6f4 v[82:85], v[176:179], v[208:211], v[82:85] cbsz:4 blgp:4
	v_mfma_f32_16x16x128_f8f6f4 v[134:137], v[212:215], v[200:203], v[134:137] cbsz:4 blgp:4
	v_mfma_f32_16x16x128_f8f6f4 v[134:137], v[220:223], v[208:211], v[134:137] cbsz:4 blgp:4
	v_mfma_f32_16x16x128_f8f6f4 v[142:145], v[216:219], v[200:203], v[142:145] cbsz:4 blgp:4
	v_mfma_f32_16x16x128_f8f6f4 v[142:145], v[224:227], v[208:211], v[142:145] cbsz:4 blgp:4
	s_setprio 0
	s_barrier
	ds_read_b128 v[156:159], v163 offset:32768
	ds_read_b128 v[168:171], v163 offset:34816
	ds_read_b128 v[172:175], v164 offset:32768
	ds_read_b128 v[176:179], v164 offset:34816
	ds_read_b128 v[180:183], v165 offset:32768
	ds_read_b128 v[184:187], v165 offset:34816
	ds_read_b128 v[188:191], v166 offset:32768
	ds_read_b128 v[192:195], v166 offset:34816
	ds_read_b128 v[196:199], v165 offset:36864
	ds_read_b128 v[200:203], v165 offset:38912
	ds_read_b128 v[204:207], v166 offset:36864
	ds_read_b128 v[208:211], v166 offset:38912
	s_add_u32 s48, s48, s22
	s_addc_u32 s49, s49, s23
	s_mov_b32 m0, s61
	s_nop 0
	global_load_lds_dwordx4 v146, s[48:49]
	s_mov_b32 m0, s62
	s_nop 0
	global_load_lds_dwordx4 v150, s[48:49]
	s_waitcnt lgkmcnt(8)
	ds_read_b128 v[212:215], v163 offset:49152
	ds_read_b128 v[216:219], v163 offset:51200
	ds_read_b128 v[220:223], v164 offset:49152
	ds_read_b128 v[224:227], v164 offset:51200
	s_waitcnt vmcnt(8)
	s_waitcnt lgkmcnt(0)
	s_barrier
	s_waitcnt lgkmcnt(0)
	s_setprio 1
	v_mfma_f32_16x16x128_f8f6f4 v[18:21], v[156:159], v[180:183], v[18:21] cbsz:4 blgp:4
	v_mfma_f32_16x16x128_f8f6f4 v[18:21], v[172:175], v[188:191], v[18:21] cbsz:4 blgp:4
	v_mfma_f32_16x16x128_f8f6f4 v[22:25], v[168:171], v[180:183], v[22:25] cbsz:4 blgp:4
	v_mfma_f32_16x16x128_f8f6f4 v[22:25], v[176:179], v[188:191], v[22:25] cbsz:4 blgp:4
	v_mfma_f32_16x16x128_f8f6f4 v[50:53], v[212:215], v[180:183], v[50:53] cbsz:4 blgp:4
	v_mfma_f32_16x16x128_f8f6f4 v[50:53], v[220:223], v[188:191], v[50:53] cbsz:4 blgp:4
	v_mfma_f32_16x16x128_f8f6f4 v[54:57], v[216:219], v[180:183], v[54:57] cbsz:4 blgp:4
	v_mfma_f32_16x16x128_f8f6f4 v[54:57], v[224:227], v[188:191], v[54:57] cbsz:4 blgp:4
	v_mfma_f32_16x16x128_f8f6f4 v[26:29], v[156:159], v[184:187], v[26:29] cbsz:4 blgp:4
	v_mfma_f32_16x16x128_f8f6f4 v[26:29], v[172:175], v[192:195], v[26:29] cbsz:4 blgp:4
	v_mfma_f32_16x16x128_f8f6f4 v[30:33], v[168:171], v[184:187], v[30:33] cbsz:4 blgp:4
	v_mfma_f32_16x16x128_f8f6f4 v[30:33], v[176:179], v[192:195], v[30:33] cbsz:4 blgp:4
	v_mfma_f32_16x16x128_f8f6f4 v[58:61], v[212:215], v[184:187], v[58:61] cbsz:4 blgp:4
	v_mfma_f32_16x16x128_f8f6f4 v[58:61], v[220:223], v[192:195], v[58:61] cbsz:4 blgp:4
	v_mfma_f32_16x16x128_f8f6f4 v[62:65], v[216:219], v[184:187], v[62:65] cbsz:4 blgp:4
	v_mfma_f32_16x16x128_f8f6f4 v[62:65], v[224:227], v[192:195], v[62:65] cbsz:4 blgp:4
	v_mfma_f32_16x16x128_f8f6f4 v[34:37], v[156:159], v[196:199], v[34:37] cbsz:4 blgp:4
	v_mfma_f32_16x16x128_f8f6f4 v[34:37], v[172:175], v[204:207], v[34:37] cbsz:4 blgp:4
	v_mfma_f32_16x16x128_f8f6f4 v[38:41], v[168:171], v[196:199], v[38:41] cbsz:4 blgp:4
	v_mfma_f32_16x16x128_f8f6f4 v[38:41], v[176:179], v[204:207], v[38:41] cbsz:4 blgp:4
	v_mfma_f32_16x16x128_f8f6f4 v[66:69], v[212:215], v[196:199], v[66:69] cbsz:4 blgp:4
	v_mfma_f32_16x16x128_f8f6f4 v[66:69], v[220:223], v[204:207], v[66:69] cbsz:4 blgp:4
	v_mfma_f32_16x16x128_f8f6f4 v[70:73], v[216:219], v[196:199], v[70:73] cbsz:4 blgp:4
	v_mfma_f32_16x16x128_f8f6f4 v[70:73], v[224:227], v[204:207], v[70:73] cbsz:4 blgp:4
	v_mfma_f32_16x16x128_f8f6f4 v[42:45], v[156:159], v[200:203], v[42:45] cbsz:4 blgp:4
	v_mfma_f32_16x16x128_f8f6f4 v[42:45], v[172:175], v[208:211], v[42:45] cbsz:4 blgp:4
	v_mfma_f32_16x16x128_f8f6f4 v[46:49], v[168:171], v[200:203], v[46:49] cbsz:4 blgp:4
	v_mfma_f32_16x16x128_f8f6f4 v[46:49], v[176:179], v[208:211], v[46:49] cbsz:4 blgp:4
	v_mfma_f32_16x16x128_f8f6f4 v[74:77], v[212:215], v[200:203], v[74:77] cbsz:4 blgp:4
	v_mfma_f32_16x16x128_f8f6f4 v[74:77], v[220:223], v[208:211], v[74:77] cbsz:4 blgp:4
	v_mfma_f32_16x16x128_f8f6f4 v[78:81], v[216:219], v[200:203], v[78:81] cbsz:4 blgp:4
	v_mfma_f32_16x16x128_f8f6f4 v[78:81], v[224:227], v[208:211], v[78:81] cbsz:4 blgp:4
	s_setprio 0
	s_barrier
	s_mov_b32 m0, s65
	s_nop 0
	global_load_lds_dwordx4 v148, s[42:43]
	s_mov_b32 m0, s66
	s_nop 0
	global_load_lds_dwordx4 v152, s[42:43]
	ds_read_b128 v[180:183], v165 offset:49152
	ds_read_b128 v[184:187], v165 offset:51200
	ds_read_b128 v[188:191], v166 offset:49152
	ds_read_b128 v[192:195], v166 offset:51200
	ds_read_b128 v[196:199], v165 offset:53248
	ds_read_b128 v[200:203], v165 offset:55296
	ds_read_b128 v[204:207], v166 offset:53248
	ds_read_b128 v[208:211], v166 offset:55296
	s_mov_b32 m0, s67
	s_nop 0
	global_load_lds_dwordx4 v146, s[46:47]
	s_mov_b32 m0, s68
	s_nop 0
	global_load_lds_dwordx4 v150, s[46:47]
	s_add_u32 s42, s42, s24
	s_addc_u32 s43, s43, s25
	s_mov_b32 m0, s69
	s_nop 0
	global_load_lds_dwordx4 v148, s[42:43]
	s_mov_b32 m0, s70
	s_nop 0
	global_load_lds_dwordx4 v152, s[42:43]
	s_waitcnt vmcnt(8)
	s_waitcnt lgkmcnt(0)
	s_barrier
	s_setprio 1
	v_mfma_f32_16x16x128_f8f6f4 v[86:89], v[156:159], v[180:183], v[86:89] cbsz:4 blgp:4
	v_mfma_f32_16x16x128_f8f6f4 v[86:89], v[172:175], v[188:191], v[86:89] cbsz:4 blgp:4
	v_mfma_f32_16x16x128_f8f6f4 v[90:93], v[168:171], v[180:183], v[90:93] cbsz:4 blgp:4
	v_mfma_f32_16x16x128_f8f6f4 v[90:93], v[176:179], v[188:191], v[90:93] cbsz:4 blgp:4
	v_mfma_f32_16x16x128_f8f6f4 v[94:97], v[212:215], v[180:183], v[94:97] cbsz:4 blgp:4
	v_mfma_f32_16x16x128_f8f6f4 v[94:97], v[220:223], v[188:191], v[94:97] cbsz:4 blgp:4
	v_mfma_f32_16x16x128_f8f6f4 v[102:105], v[216:219], v[180:183], v[102:105] cbsz:4 blgp:4
	v_mfma_f32_16x16x128_f8f6f4 v[102:105], v[224:227], v[188:191], v[102:105] cbsz:4 blgp:4
	v_mfma_f32_16x16x128_f8f6f4 v[98:101], v[156:159], v[184:187], v[98:101] cbsz:4 blgp:4
	v_mfma_f32_16x16x128_f8f6f4 v[98:101], v[172:175], v[192:195], v[98:101] cbsz:4 blgp:4
	v_mfma_f32_16x16x128_f8f6f4 v[106:109], v[168:171], v[184:187], v[106:109] cbsz:4 blgp:4
	v_mfma_f32_16x16x128_f8f6f4 v[106:109], v[176:179], v[192:195], v[106:109] cbsz:4 blgp:4
	v_mfma_f32_16x16x128_f8f6f4 v[110:113], v[212:215], v[184:187], v[110:113] cbsz:4 blgp:4
	v_mfma_f32_16x16x128_f8f6f4 v[110:113], v[220:223], v[192:195], v[110:113] cbsz:4 blgp:4
	v_mfma_f32_16x16x128_f8f6f4 v[114:117], v[216:219], v[184:187], v[114:117] cbsz:4 blgp:4
	v_mfma_f32_16x16x128_f8f6f4 v[114:117], v[224:227], v[192:195], v[114:117] cbsz:4 blgp:4
	v_mfma_f32_16x16x128_f8f6f4 v[118:121], v[156:159], v[196:199], v[118:121] cbsz:4 blgp:4
	v_mfma_f32_16x16x128_f8f6f4 v[118:121], v[172:175], v[204:207], v[118:121] cbsz:4 blgp:4
	v_mfma_f32_16x16x128_f8f6f4 v[126:129], v[168:171], v[196:199], v[126:129] cbsz:4 blgp:4
	v_mfma_f32_16x16x128_f8f6f4 v[126:129], v[176:179], v[204:207], v[126:129] cbsz:4 blgp:4
	v_mfma_f32_16x16x128_f8f6f4 v[122:125], v[212:215], v[196:199], v[122:125] cbsz:4 blgp:4
	v_mfma_f32_16x16x128_f8f6f4 v[122:125], v[220:223], v[204:207], v[122:125] cbsz:4 blgp:4
	v_mfma_f32_16x16x128_f8f6f4 v[130:133], v[216:219], v[196:199], v[130:133] cbsz:4 blgp:4
	v_mfma_f32_16x16x128_f8f6f4 v[130:133], v[224:227], v[204:207], v[130:133] cbsz:4 blgp:4
	v_mfma_f32_16x16x128_f8f6f4 v[138:141], v[156:159], v[200:203], v[138:141] cbsz:4 blgp:4
	v_mfma_f32_16x16x128_f8f6f4 v[138:141], v[172:175], v[208:211], v[138:141] cbsz:4 blgp:4
	v_mfma_f32_16x16x128_f8f6f4 v[82:85], v[168:171], v[200:203], v[82:85] cbsz:4 blgp:4
	v_mfma_f32_16x16x128_f8f6f4 v[82:85], v[176:179], v[208:211], v[82:85] cbsz:4 blgp:4
	v_mfma_f32_16x16x128_f8f6f4 v[134:137], v[212:215], v[200:203], v[134:137] cbsz:4 blgp:4
	v_mfma_f32_16x16x128_f8f6f4 v[134:137], v[220:223], v[208:211], v[134:137] cbsz:4 blgp:4
	v_mfma_f32_16x16x128_f8f6f4 v[142:145], v[216:219], v[200:203], v[142:145] cbsz:4 blgp:4
	v_mfma_f32_16x16x128_f8f6f4 v[142:145], v[224:227], v[208:211], v[142:145] cbsz:4 blgp:4
	s_setprio 0
	s_add_i32 s42, s82, 2
	s_add_u32 s29, s29, 0x100
	s_addc_u32 s79, s79, 0
	s_add_u32 s80, s80, 0x100
	s_addc_u32 s81, s81, 0
	s_add_u32 s40, s40, 0x100
	s_addc_u32 s41, s41, 0
	s_cmp_ge_i32 s82, s64
	s_barrier
	s_cbranch_scc1 .LBB5_4
	s_mov_b32 s82, s42
	s_cmp_eq_u32 s64, s82
	s_cselect_b64 s[42:43], -1, 0
	s_cmp_lg_u32 s64, s82
	s_cbranch_scc0 .LBB5_14
	s_branch .LBB5_15

.LBB6_15:
	s_add_u32 s82, s36, s20
	s_addc_u32 s83, s37, s21
	s_add_u32 s31, s36, 0x100
	s_addc_u32 s39, s37, 0
	s_and_b64 s[40:41], s[12:13], exec
	ds_read_b128 v[82:85], v169
	ds_read_b128 v[94:97], v169 offset:2048
	ds_read_b128 v[102:105], v178
	ds_read_b128 v[110:113], v178 offset:2048
	s_cselect_b32 s45, s5, s39
	s_cselect_b32 s44, s4, s31
	s_add_u32 s31, s34, 0x100
	s_addc_u32 s39, s35, 0
	s_and_b64 s[40:41], s[12:13], exec
	s_cselect_b32 s47, s7, s39
	s_cselect_b32 s46, s6, s31
	s_add_u32 s42, s44, 0x80
	s_addc_u32 s43, s45, 0
	s_add_u32 s40, s46, 0x80
	s_addc_u32 s41, s47, 0
	ds_read_b128 v[58:61], v179
	ds_read_b128 v[66:69], v179 offset:2048
	ds_read_b128 v[62:65], v180
	ds_read_b128 v[70:73], v180 offset:2048
	ds_read_b128 v[74:77], v179 offset:4096
	ds_read_b128 v[86:89], v179 offset:6144
	ds_read_b128 v[78:81], v180 offset:4096
	ds_read_b128 v[90:93], v180 offset:6144
	s_add_u32 s84, s82, 0x80
	s_addc_u32 s85, s83, 0
	s_mov_b32 m0, s68
	s_nop 0
	global_load_lds_dwordx4 v162, s[84:85]
	s_mov_b32 m0, s69
	s_nop 0
	global_load_lds_dwordx4 v166, s[84:85]
	s_waitcnt lgkmcnt(8)
	ds_read_b128 v[142:145], v169 offset:16384
	ds_read_b128 v[146:149], v169 offset:18432
	ds_read_b128 v[150:153], v178 offset:16384
	ds_read_b128 v[154:157], v178 offset:18432
	s_waitcnt vmcnt(8)
	s_waitcnt lgkmcnt(0)
	s_barrier
	s_waitcnt lgkmcnt(0)
	s_waitcnt vmcnt(16)
	v_mov_b32_e32 v171, v170
	v_pk_mul_f32 v[16:17], v[170:171], v[16:17]
	v_pk_mul_f32 v[14:15], v[172:173], v[14:15]
	v_pk_mul_f32 v[12:13], v[170:171], v[12:13]
	v_pk_mul_f32 v[10:11], v[172:173], v[10:11]
	v_pk_mul_f32 v[8:9], v[170:171], v[8:9]
	v_pk_mul_f32 v[6:7], v[172:173], v[6:7]
	v_pk_mul_f32 v[4:5], v[170:171], v[4:5]
	v_pk_mul_f32 v[2:3], v[172:173], v[2:3]
	s_setprio 1
	v_mfma_f32_16x16x128_f8f6f4 v[18:21], v[82:85], v[58:61], v[14:17] cbsz:4 blgp:4
	v_mfma_f32_16x16x128_f8f6f4 v[18:21], v[102:105], v[62:65], v[18:21] cbsz:4 blgp:4
	v_mfma_f32_16x16x128_f8f6f4 v[22:25], v[94:97], v[58:61], v[10:13] cbsz:4 blgp:4
	v_mfma_f32_16x16x128_f8f6f4 v[22:25], v[110:113], v[62:65], v[22:25] cbsz:4 blgp:4
	v_mfma_f32_16x16x128_f8f6f4 v[50:53], v[142:145], v[58:61], v[6:9] cbsz:4 blgp:4
	v_mfma_f32_16x16x128_f8f6f4 v[50:53], v[150:153], v[62:65], v[50:53] cbsz:4 blgp:4
	v_mfma_f32_16x16x128_f8f6f4 v[54:57], v[146:149], v[58:61], v[2:5] cbsz:4 blgp:4
	v_mfma_f32_16x16x128_f8f6f4 v[54:57], v[154:157], v[62:65], v[54:57] cbsz:4 blgp:4
	v_mfma_f32_16x16x128_f8f6f4 v[26:29], v[82:85], v[66:69], v[14:17] cbsz:4 blgp:4
	v_mfma_f32_16x16x128_f8f6f4 v[26:29], v[102:105], v[70:73], v[26:29] cbsz:4 blgp:4
	v_mfma_f32_16x16x128_f8f6f4 v[30:33], v[94:97], v[66:69], v[10:13] cbsz:4 blgp:4
	v_mfma_f32_16x16x128_f8f6f4 v[30:33], v[110:113], v[70:73], v[30:33] cbsz:4 blgp:4
	v_mfma_f32_16x16x128_f8f6f4 v[58:61], v[142:145], v[66:69], v[6:9] cbsz:4 blgp:4
	v_mfma_f32_16x16x128_f8f6f4 v[58:61], v[150:153], v[70:73], v[58:61] cbsz:4 blgp:4
	v_mfma_f32_16x16x128_f8f6f4 v[62:65], v[146:149], v[66:69], v[2:5] cbsz:4 blgp:4
	v_mfma_f32_16x16x128_f8f6f4 v[62:65], v[154:157], v[70:73], v[62:65] cbsz:4 blgp:4
	v_mfma_f32_16x16x128_f8f6f4 v[34:37], v[82:85], v[74:77], v[14:17] cbsz:4 blgp:4
	v_mfma_f32_16x16x128_f8f6f4 v[34:37], v[102:105], v[78:81], v[34:37] cbsz:4 blgp:4
	v_mfma_f32_16x16x128_f8f6f4 v[38:41], v[94:97], v[74:77], v[10:13] cbsz:4 blgp:4
	v_mfma_f32_16x16x128_f8f6f4 v[38:41], v[110:113], v[78:81], v[38:41] cbsz:4 blgp:4
	v_mfma_f32_16x16x128_f8f6f4 v[66:69], v[142:145], v[74:77], v[6:9] cbsz:4 blgp:4
	v_mfma_f32_16x16x128_f8f6f4 v[66:69], v[150:153], v[78:81], v[66:69] cbsz:4 blgp:4
	v_mfma_f32_16x16x128_f8f6f4 v[70:73], v[146:149], v[74:77], v[2:5] cbsz:4 blgp:4
	v_mfma_f32_16x16x128_f8f6f4 v[70:73], v[154:157], v[78:81], v[70:73] cbsz:4 blgp:4
	v_mfma_f32_16x16x128_f8f6f4 v[42:45], v[82:85], v[86:89], v[14:17] cbsz:4 blgp:4
	v_mfma_f32_16x16x128_f8f6f4 v[42:45], v[102:105], v[90:93], v[42:45] cbsz:4 blgp:4
	v_mfma_f32_16x16x128_f8f6f4 v[46:49], v[94:97], v[86:89], v[10:13] cbsz:4 blgp:4
	v_mfma_f32_16x16x128_f8f6f4 v[46:49], v[110:113], v[90:93], v[46:49] cbsz:4 blgp:4
	v_mfma_f32_16x16x128_f8f6f4 v[74:77], v[142:145], v[86:89], v[6:9] cbsz:4 blgp:4
	v_mfma_f32_16x16x128_f8f6f4 v[74:77], v[150:153], v[90:93], v[74:77] cbsz:4 blgp:4
	v_mfma_f32_16x16x128_f8f6f4 v[78:81], v[146:149], v[86:89], v[2:5] cbsz:4 blgp:4
	v_mfma_f32_16x16x128_f8f6f4 v[78:81], v[154:157], v[90:93], v[78:81] cbsz:4 blgp:4
	s_setprio 0
	s_barrier
	s_mov_b32 m0, s54
	s_nop 0
	global_load_lds_dwordx4 v164, s[46:47]
	s_mov_b32 m0, s55
	s_nop 0
	global_load_lds_dwordx4 v168, s[46:47]
	ds_read_b128 v[114:117], v179 offset:16384
	ds_read_b128 v[122:125], v179 offset:18432
	ds_read_b128 v[130:133], v180 offset:16384
	ds_read_b128 v[134:137], v180 offset:18432
	ds_read_b128 v[158:161], v179 offset:20480
	ds_read_b128 v[182:185], v179 offset:22528
	ds_read_b128 v[186:189], v180 offset:20480
	ds_read_b128 v[190:193], v180 offset:22528
	s_mov_b32 m0, s53
	s_nop 0
	global_load_lds_dwordx4 v162, s[44:45]
	s_mov_b32 m0, s56
	s_nop 0
	global_load_lds_dwordx4 v166, s[44:45]
	s_add_u32 s46, s46, s22
	s_addc_u32 s47, s47, s23
	s_mov_b32 m0, s57
	s_nop 0
	global_load_lds_dwordx4 v164, s[46:47]
	s_mov_b32 m0, s58
	s_nop 0
	global_load_lds_dwordx4 v168, s[46:47]
	s_waitcnt vmcnt(8)
	s_waitcnt lgkmcnt(0)
	s_barrier
	s_setprio 1
	v_mfma_f32_16x16x128_f8f6f4 v[86:89], v[82:85], v[114:117], v[14:17] cbsz:4 blgp:4
	v_mfma_f32_16x16x128_f8f6f4 v[86:89], v[102:105], v[130:133], v[86:89] cbsz:4 blgp:4
	v_mfma_f32_16x16x128_f8f6f4 v[90:93], v[94:97], v[114:117], v[10:13] cbsz:4 blgp:4
	v_mfma_f32_16x16x128_f8f6f4 v[90:93], v[110:113], v[130:133], v[90:93] cbsz:4 blgp:4
	v_mfma_f32_16x16x128_f8f6f4 v[98:101], v[82:85], v[122:125], v[14:17] cbsz:4 blgp:4
	v_mfma_f32_16x16x128_f8f6f4 v[98:101], v[102:105], v[134:137], v[98:101] cbsz:4 blgp:4
	v_mfma_f32_16x16x128_f8f6f4 v[106:109], v[94:97], v[122:125], v[10:13] cbsz:4 blgp:4
	v_mfma_f32_16x16x128_f8f6f4 v[106:109], v[110:113], v[134:137], v[106:109] cbsz:4 blgp:4
	v_mfma_f32_16x16x128_f8f6f4 v[118:121], v[82:85], v[158:161], v[14:17] cbsz:4 blgp:4
	v_mfma_f32_16x16x128_f8f6f4 v[118:121], v[102:105], v[186:189], v[118:121] cbsz:4 blgp:4
	v_mfma_f32_16x16x128_f8f6f4 v[126:129], v[94:97], v[158:161], v[10:13] cbsz:4 blgp:4
	v_mfma_f32_16x16x128_f8f6f4 v[126:129], v[110:113], v[186:189], v[126:129] cbsz:4 blgp:4
	v_mfma_f32_16x16x128_f8f6f4 v[138:141], v[82:85], v[182:185], v[14:17] cbsz:4 blgp:4
	v_mfma_f32_16x16x128_f8f6f4 v[138:141], v[102:105], v[190:193], v[138:141] cbsz:4 blgp:4
	v_mfma_f32_16x16x128_f8f6f4 v[82:85], v[94:97], v[182:185], v[10:13] cbsz:4 blgp:4
	v_mfma_f32_16x16x128_f8f6f4 v[82:85], v[110:113], v[190:193], v[82:85] cbsz:4 blgp:4
	v_mfma_f32_16x16x128_f8f6f4 v[94:97], v[142:145], v[114:117], v[6:9] cbsz:4 blgp:4
	v_mfma_f32_16x16x128_f8f6f4 v[94:97], v[150:153], v[130:133], v[94:97] cbsz:4 blgp:4
	v_mfma_f32_16x16x128_f8f6f4 v[102:105], v[146:149], v[114:117], v[2:5] cbsz:4 blgp:4
	v_mfma_f32_16x16x128_f8f6f4 v[102:105], v[154:157], v[130:133], v[102:105] cbsz:4 blgp:4
	v_mfma_f32_16x16x128_f8f6f4 v[110:113], v[142:145], v[122:125], v[6:9] cbsz:4 blgp:4
	v_mfma_f32_16x16x128_f8f6f4 v[110:113], v[150:153], v[134:137], v[110:113] cbsz:4 blgp:4
	v_mfma_f32_16x16x128_f8f6f4 v[114:117], v[146:149], v[122:125], v[2:5] cbsz:4 blgp:4
	v_mfma_f32_16x16x128_f8f6f4 v[114:117], v[154:157], v[134:137], v[114:117] cbsz:4 blgp:4
	v_mfma_f32_16x16x128_f8f6f4 v[122:125], v[142:145], v[158:161], v[6:9] cbsz:4 blgp:4
	v_mfma_f32_16x16x128_f8f6f4 v[122:125], v[150:153], v[186:189], v[122:125] cbsz:4 blgp:4
	v_mfma_f32_16x16x128_f8f6f4 v[130:133], v[146:149], v[158:161], v[2:5] cbsz:4 blgp:4
	v_mfma_f32_16x16x128_f8f6f4 v[130:133], v[154:157], v[186:189], v[130:133] cbsz:4 blgp:4
	v_mfma_f32_16x16x128_f8f6f4 v[134:137], v[142:145], v[182:185], v[6:9] cbsz:4 blgp:4
	v_mfma_f32_16x16x128_f8f6f4 v[134:137], v[150:153], v[190:193], v[134:137] cbsz:4 blgp:4
	v_mfma_f32_16x16x128_f8f6f4 v[142:145], v[146:149], v[182:185], v[2:5] cbsz:4 blgp:4
	v_mfma_f32_16x16x128_f8f6f4 v[142:145], v[154:157], v[190:193], v[142:145] cbsz:4 blgp:4
	s_setprio 0
	s_barrier
	ds_read_b128 v[146:149], v169 offset:32768
	ds_read_b128 v[150:153], v169 offset:34816
	ds_read_b128 v[154:157], v178 offset:32768
	ds_read_b128 v[158:161], v178 offset:34816
	ds_read_b128 v[182:185], v179 offset:32768
	ds_read_b128 v[186:189], v179 offset:34816
	ds_read_b128 v[190:193], v180 offset:32768
	ds_read_b128 v[194:197], v180 offset:34816
	ds_read_b128 v[198:201], v179 offset:36864
	ds_read_b128 v[202:205], v179 offset:38912
	ds_read_b128 v[206:209], v180 offset:36864
	ds_read_b128 v[210:213], v180 offset:38912
	s_add_u32 s44, s44, s20
	s_addc_u32 s45, s45, s21
	s_mov_b32 m0, s59
	s_nop 0
	global_load_lds_dwordx4 v162, s[44:45]
	s_mov_b32 m0, s60
	s_nop 0
	global_load_lds_dwordx4 v166, s[44:45]
	s_waitcnt lgkmcnt(8)
	ds_read_b128 v[214:217], v169 offset:49152
	ds_read_b128 v[218:221], v169 offset:51200
	ds_read_b128 v[222:225], v178 offset:49152
	ds_read_b128 v[226:229], v178 offset:51200
	s_waitcnt vmcnt(8)
	s_waitcnt lgkmcnt(0)
	s_barrier
	s_waitcnt lgkmcnt(0)
	s_setprio 1
	v_mfma_f32_16x16x128_f8f6f4 v[18:21], v[146:149], v[182:185], v[18:21] cbsz:4 blgp:4
	v_mfma_f32_16x16x128_f8f6f4 v[18:21], v[154:157], v[190:193], v[18:21] cbsz:4 blgp:4
	v_mfma_f32_16x16x128_f8f6f4 v[22:25], v[150:153], v[182:185], v[22:25] cbsz:4 blgp:4
	v_mfma_f32_16x16x128_f8f6f4 v[22:25], v[158:161], v[190:193], v[22:25] cbsz:4 blgp:4
	v_mfma_f32_16x16x128_f8f6f4 v[50:53], v[214:217], v[182:185], v[50:53] cbsz:4 blgp:4
	v_mfma_f32_16x16x128_f8f6f4 v[50:53], v[222:225], v[190:193], v[50:53] cbsz:4 blgp:4
	v_mfma_f32_16x16x128_f8f6f4 v[54:57], v[218:221], v[182:185], v[54:57] cbsz:4 blgp:4
	v_mfma_f32_16x16x128_f8f6f4 v[54:57], v[226:229], v[190:193], v[54:57] cbsz:4 blgp:4
	v_mfma_f32_16x16x128_f8f6f4 v[26:29], v[146:149], v[186:189], v[26:29] cbsz:4 blgp:4
	v_mfma_f32_16x16x128_f8f6f4 v[26:29], v[154:157], v[194:197], v[26:29] cbsz:4 blgp:4
	v_mfma_f32_16x16x128_f8f6f4 v[30:33], v[150:153], v[186:189], v[30:33] cbsz:4 blgp:4
	v_mfma_f32_16x16x128_f8f6f4 v[30:33], v[158:161], v[194:197], v[30:33] cbsz:4 blgp:4
	v_mfma_f32_16x16x128_f8f6f4 v[58:61], v[214:217], v[186:189], v[58:61] cbsz:4 blgp:4
	v_mfma_f32_16x16x128_f8f6f4 v[58:61], v[222:225], v[194:197], v[58:61] cbsz:4 blgp:4
	v_mfma_f32_16x16x128_f8f6f4 v[62:65], v[218:221], v[186:189], v[62:65] cbsz:4 blgp:4
	v_mfma_f32_16x16x128_f8f6f4 v[62:65], v[226:229], v[194:197], v[62:65] cbsz:4 blgp:4
	v_mfma_f32_16x16x128_f8f6f4 v[34:37], v[146:149], v[198:201], v[34:37] cbsz:4 blgp:4
	v_mfma_f32_16x16x128_f8f6f4 v[34:37], v[154:157], v[206:209], v[34:37] cbsz:4 blgp:4
	v_mfma_f32_16x16x128_f8f6f4 v[38:41], v[150:153], v[198:201], v[38:41] cbsz:4 blgp:4
	v_mfma_f32_16x16x128_f8f6f4 v[38:41], v[158:161], v[206:209], v[38:41] cbsz:4 blgp:4
	v_mfma_f32_16x16x128_f8f6f4 v[66:69], v[214:217], v[198:201], v[66:69] cbsz:4 blgp:4
	v_mfma_f32_16x16x128_f8f6f4 v[66:69], v[222:225], v[206:209], v[66:69] cbsz:4 blgp:4
	v_mfma_f32_16x16x128_f8f6f4 v[70:73], v[218:221], v[198:201], v[70:73] cbsz:4 blgp:4
	v_mfma_f32_16x16x128_f8f6f4 v[70:73], v[226:229], v[206:209], v[70:73] cbsz:4 blgp:4
	v_mfma_f32_16x16x128_f8f6f4 v[42:45], v[146:149], v[202:205], v[42:45] cbsz:4 blgp:4
	v_mfma_f32_16x16x128_f8f6f4 v[42:45], v[154:157], v[210:213], v[42:45] cbsz:4 blgp:4
	v_mfma_f32_16x16x128_f8f6f4 v[46:49], v[150:153], v[202:205], v[46:49] cbsz:4 blgp:4
	v_mfma_f32_16x16x128_f8f6f4 v[46:49], v[158:161], v[210:213], v[46:49] cbsz:4 blgp:4
	v_mfma_f32_16x16x128_f8f6f4 v[74:77], v[214:217], v[202:205], v[74:77] cbsz:4 blgp:4
	v_mfma_f32_16x16x128_f8f6f4 v[74:77], v[222:225], v[210:213], v[74:77] cbsz:4 blgp:4
	v_mfma_f32_16x16x128_f8f6f4 v[78:81], v[218:221], v[202:205], v[78:81] cbsz:4 blgp:4
	v_mfma_f32_16x16x128_f8f6f4 v[78:81], v[226:229], v[210:213], v[78:81] cbsz:4 blgp:4
	s_setprio 0
	s_barrier
	s_mov_b32 m0, s62
	s_nop 0
	global_load_lds_dwordx4 v164, s[40:41]
	s_mov_b32 m0, s63
	s_nop 0
	global_load_lds_dwordx4 v168, s[40:41]
	ds_read_b128 v[182:185], v179 offset:49152
	ds_read_b128 v[186:189], v179 offset:51200
	ds_read_b128 v[190:193], v180 offset:49152
	ds_read_b128 v[194:197], v180 offset:51200
	ds_read_b128 v[198:201], v179 offset:53248
	ds_read_b128 v[202:205], v179 offset:55296
	ds_read_b128 v[206:209], v180 offset:53248
	ds_read_b128 v[210:213], v180 offset:55296
	s_mov_b32 m0, s64
	s_nop 0
	global_load_lds_dwordx4 v162, s[42:43]
	s_mov_b32 m0, s65
	s_nop 0
	global_load_lds_dwordx4 v166, s[42:43]
	s_add_u32 s40, s40, s22
	s_addc_u32 s41, s41, s23
	s_mov_b32 m0, s66
	s_nop 0
	global_load_lds_dwordx4 v164, s[40:41]
	s_mov_b32 m0, s67
	s_nop 0
	global_load_lds_dwordx4 v168, s[40:41]
	s_waitcnt vmcnt(8)
	s_waitcnt lgkmcnt(0)
	s_barrier
	s_setprio 1
	v_mfma_f32_16x16x128_f8f6f4 v[86:89], v[146:149], v[182:185], v[86:89] cbsz:4 blgp:4
	v_mfma_f32_16x16x128_f8f6f4 v[86:89], v[154:157], v[190:193], v[86:89] cbsz:4 blgp:4
	v_mfma_f32_16x16x128_f8f6f4 v[90:93], v[150:153], v[182:185], v[90:93] cbsz:4 blgp:4
	v_mfma_f32_16x16x128_f8f6f4 v[90:93], v[158:161], v[190:193], v[90:93] cbsz:4 blgp:4
	v_mfma_f32_16x16x128_f8f6f4 v[94:97], v[214:217], v[182:185], v[94:97] cbsz:4 blgp:4
	v_mfma_f32_16x16x128_f8f6f4 v[94:97], v[222:225], v[190:193], v[94:97] cbsz:4 blgp:4
	v_mfma_f32_16x16x128_f8f6f4 v[102:105], v[218:221], v[182:185], v[102:105] cbsz:4 blgp:4
	v_mfma_f32_16x16x128_f8f6f4 v[102:105], v[226:229], v[190:193], v[102:105] cbsz:4 blgp:4
	v_mfma_f32_16x16x128_f8f6f4 v[98:101], v[146:149], v[186:189], v[98:101] cbsz:4 blgp:4
	v_mfma_f32_16x16x128_f8f6f4 v[98:101], v[154:157], v[194:197], v[98:101] cbsz:4 blgp:4
	v_mfma_f32_16x16x128_f8f6f4 v[106:109], v[150:153], v[186:189], v[106:109] cbsz:4 blgp:4
	v_mfma_f32_16x16x128_f8f6f4 v[106:109], v[158:161], v[194:197], v[106:109] cbsz:4 blgp:4
	v_mfma_f32_16x16x128_f8f6f4 v[110:113], v[214:217], v[186:189], v[110:113] cbsz:4 blgp:4
	v_mfma_f32_16x16x128_f8f6f4 v[110:113], v[222:225], v[194:197], v[110:113] cbsz:4 blgp:4
	v_mfma_f32_16x16x128_f8f6f4 v[114:117], v[218:221], v[186:189], v[114:117] cbsz:4 blgp:4
	v_mfma_f32_16x16x128_f8f6f4 v[114:117], v[226:229], v[194:197], v[114:117] cbsz:4 blgp:4
	v_mfma_f32_16x16x128_f8f6f4 v[118:121], v[146:149], v[198:201], v[118:121] cbsz:4 blgp:4
	v_mfma_f32_16x16x128_f8f6f4 v[118:121], v[154:157], v[206:209], v[118:121] cbsz:4 blgp:4
	v_mfma_f32_16x16x128_f8f6f4 v[126:129], v[150:153], v[198:201], v[126:129] cbsz:4 blgp:4
	v_mfma_f32_16x16x128_f8f6f4 v[126:129], v[158:161], v[206:209], v[126:129] cbsz:4 blgp:4
	v_mfma_f32_16x16x128_f8f6f4 v[122:125], v[214:217], v[198:201], v[122:125] cbsz:4 blgp:4
	v_mfma_f32_16x16x128_f8f6f4 v[122:125], v[222:225], v[206:209], v[122:125] cbsz:4 blgp:4
	v_mfma_f32_16x16x128_f8f6f4 v[130:133], v[218:221], v[198:201], v[130:133] cbsz:4 blgp:4
	v_mfma_f32_16x16x128_f8f6f4 v[130:133], v[226:229], v[206:209], v[130:133] cbsz:4 blgp:4
	v_mfma_f32_16x16x128_f8f6f4 v[138:141], v[146:149], v[202:205], v[138:141] cbsz:4 blgp:4
	v_mfma_f32_16x16x128_f8f6f4 v[138:141], v[154:157], v[210:213], v[138:141] cbsz:4 blgp:4
	v_mfma_f32_16x16x128_f8f6f4 v[82:85], v[150:153], v[202:205], v[82:85] cbsz:4 blgp:4
	v_mfma_f32_16x16x128_f8f6f4 v[82:85], v[158:161], v[210:213], v[82:85] cbsz:4 blgp:4
	v_mfma_f32_16x16x128_f8f6f4 v[134:137], v[214:217], v[202:205], v[134:137] cbsz:4 blgp:4
	v_mfma_f32_16x16x128_f8f6f4 v[134:137], v[222:225], v[210:213], v[134:137] cbsz:4 blgp:4
	v_mfma_f32_16x16x128_f8f6f4 v[142:145], v[218:221], v[202:205], v[142:145] cbsz:4 blgp:4
	v_mfma_f32_16x16x128_f8f6f4 v[142:145], v[226:229], v[210:213], v[142:145] cbsz:4 blgp:4
	s_setprio 0
	s_andn2_b64 vcc, exec, s[28:29]
	s_barrier
	s_cbranch_vccnz .LBB6_20
	s_ashr_i32 s39, s38, 31
	s_lshl_b64 s[38:39], s[38:39], 10
	s_add_u32 s38, s14, s38
	s_addc_u32 s39, s15, s39
	s_add_u32 s31, s36, 0x200
	s_addc_u32 s46, s37, 0
	s_add_u32 s47, s34, 0x200
	s_addc_u32 s81, s35, 0
	s_add_u32 s34, s82, 0x180
	s_addc_u32 s35, s83, 0
	s_mov_b32 s82, 4
	s_cmp_eq_u32 s61, s82
	s_cselect_b64 s[36:37], -1, 0
	s_cmp_lg_u32 s61, s82
	s_cbranch_scc1 .LBB6_18

.LBB6_18:
	ds_read_b128 v[146:149], v169
	ds_read_b128 v[150:153], v169 offset:2048
	ds_read_b128 v[154:157], v178
	ds_read_b128 v[158:161], v178 offset:2048
	s_and_b64 s[36:37], s[36:37], exec
	s_cselect_b32 s42, s4, s31
	s_cselect_b32 s43, s5, s46
	s_cselect_b32 s45, s7, s81
	s_cselect_b32 s44, s6, s47
	s_add_u32 s40, s42, 0x80
	s_addc_u32 s41, s43, 0
	s_add_u32 s36, s44, 0x80
	s_addc_u32 s37, s45, 0
	ds_read_b128 v[182:185], v179
	ds_read_b128 v[186:189], v179 offset:2048
	ds_read_b128 v[190:193], v180
	ds_read_b128 v[194:197], v180 offset:2048
	ds_read_b128 v[198:201], v179 offset:4096
	ds_read_b128 v[202:205], v179 offset:6144
	ds_read_b128 v[206:209], v180 offset:4096
	ds_read_b128 v[210:213], v180 offset:6144
	s_mov_b32 m0, s68
	s_nop 0
	global_load_lds_dwordx4 v162, s[34:35]
	s_mov_b32 m0, s69
	s_nop 0
	global_load_lds_dwordx4 v166, s[34:35]
	s_waitcnt lgkmcnt(8)
	ds_read_b128 v[214:217], v169 offset:16384
	ds_read_b128 v[218:221], v169 offset:18432
	ds_read_b128 v[222:225], v178 offset:16384
	ds_read_b128 v[226:229], v178 offset:18432
	s_waitcnt vmcnt(8)
	s_waitcnt lgkmcnt(0)
	s_barrier
	s_waitcnt lgkmcnt(0)
	s_setprio 1
	v_mfma_f32_16x16x128_f8f6f4 v[18:21], v[146:149], v[182:185], v[18:21] cbsz:4 blgp:4
	v_mfma_f32_16x16x128_f8f6f4 v[18:21], v[154:157], v[190:193], v[18:21] cbsz:4 blgp:4
	v_mfma_f32_16x16x128_f8f6f4 v[22:25], v[150:153], v[182:185], v[22:25] cbsz:4 blgp:4
	v_mfma_f32_16x16x128_f8f6f4 v[22:25], v[158:161], v[190:193], v[22:25] cbsz:4 blgp:4
	v_mfma_f32_16x16x128_f8f6f4 v[50:53], v[214:217], v[182:185], v[50:53] cbsz:4 blgp:4
	v_mfma_f32_16x16x128_f8f6f4 v[50:53], v[222:225], v[190:193], v[50:53] cbsz:4 blgp:4
	v_mfma_f32_16x16x128_f8f6f4 v[54:57], v[218:221], v[182:185], v[54:57] cbsz:4 blgp:4
	v_mfma_f32_16x16x128_f8f6f4 v[54:57], v[226:229], v[190:193], v[54:57] cbsz:4 blgp:4
	v_mfma_f32_16x16x128_f8f6f4 v[26:29], v[146:149], v[186:189], v[26:29] cbsz:4 blgp:4
	v_mfma_f32_16x16x128_f8f6f4 v[26:29], v[154:157], v[194:197], v[26:29] cbsz:4 blgp:4
	v_mfma_f32_16x16x128_f8f6f4 v[30:33], v[150:153], v[186:189], v[30:33] cbsz:4 blgp:4
	v_mfma_f32_16x16x128_f8f6f4 v[30:33], v[158:161], v[194:197], v[30:33] cbsz:4 blgp:4
	v_mfma_f32_16x16x128_f8f6f4 v[58:61], v[214:217], v[186:189], v[58:61] cbsz:4 blgp:4
	v_mfma_f32_16x16x128_f8f6f4 v[58:61], v[222:225], v[194:197], v[58:61] cbsz:4 blgp:4
	v_mfma_f32_16x16x128_f8f6f4 v[62:65], v[218:221], v[186:189], v[62:65] cbsz:4 blgp:4
	v_mfma_f32_16x16x128_f8f6f4 v[62:65], v[226:229], v[194:197], v[62:65] cbsz:4 blgp:4
	v_mfma_f32_16x16x128_f8f6f4 v[34:37], v[146:149], v[198:201], v[34:37] cbsz:4 blgp:4
	v_mfma_f32_16x16x128_f8f6f4 v[34:37], v[154:157], v[206:209], v[34:37] cbsz:4 blgp:4
	v_mfma_f32_16x16x128_f8f6f4 v[38:41], v[150:153], v[198:201], v[38:41] cbsz:4 blgp:4
	v_mfma_f32_16x16x128_f8f6f4 v[38:41], v[158:161], v[206:209], v[38:41] cbsz:4 blgp:4
	v_mfma_f32_16x16x128_f8f6f4 v[66:69], v[214:217], v[198:201], v[66:69] cbsz:4 blgp:4
	v_mfma_f32_16x16x128_f8f6f4 v[66:69], v[222:225], v[206:209], v[66:69] cbsz:4 blgp:4
	v_mfma_f32_16x16x128_f8f6f4 v[70:73], v[218:221], v[198:201], v[70:73] cbsz:4 blgp:4
	v_mfma_f32_16x16x128_f8f6f4 v[70:73], v[226:229], v[206:209], v[70:73] cbsz:4 blgp:4
	v_mfma_f32_16x16x128_f8f6f4 v[42:45], v[146:149], v[202:205], v[42:45] cbsz:4 blgp:4
	v_mfma_f32_16x16x128_f8f6f4 v[42:45], v[154:157], v[210:213], v[42:45] cbsz:4 blgp:4
	v_mfma_f32_16x16x128_f8f6f4 v[46:49], v[150:153], v[202:205], v[46:49] cbsz:4 blgp:4
	v_mfma_f32_16x16x128_f8f6f4 v[46:49], v[158:161], v[210:213], v[46:49] cbsz:4 blgp:4
	v_mfma_f32_16x16x128_f8f6f4 v[74:77], v[214:217], v[202:205], v[74:77] cbsz:4 blgp:4
	v_mfma_f32_16x16x128_f8f6f4 v[74:77], v[222:225], v[210:213], v[74:77] cbsz:4 blgp:4
	v_mfma_f32_16x16x128_f8f6f4 v[78:81], v[218:221], v[202:205], v[78:81] cbsz:4 blgp:4
	v_mfma_f32_16x16x128_f8f6f4 v[78:81], v[226:229], v[210:213], v[78:81] cbsz:4 blgp:4
	s_setprio 0
	s_barrier
	s_mov_b32 m0, s54
	s_nop 0
	global_load_lds_dwordx4 v164, s[44:45]
	s_mov_b32 m0, s55
	s_nop 0
	global_load_lds_dwordx4 v168, s[44:45]
	ds_read_b128 v[182:185], v179 offset:16384
	ds_read_b128 v[186:189], v179 offset:18432
	ds_read_b128 v[190:193], v180 offset:16384
	ds_read_b128 v[194:197], v180 offset:18432
	ds_read_b128 v[198:201], v179 offset:20480
	ds_read_b128 v[202:205], v179 offset:22528
	ds_read_b128 v[206:209], v180 offset:20480
	ds_read_b128 v[210:213], v180 offset:22528
	s_mov_b32 m0, s53
	s_nop 0
	global_load_lds_dwordx4 v162, s[42:43]
	s_mov_b32 m0, s56
	s_nop 0
	global_load_lds_dwordx4 v166, s[42:43]
	s_add_u32 s44, s44, s22
	s_addc_u32 s45, s45, s23
	s_mov_b32 m0, s57
	s_nop 0
	global_load_lds_dwordx4 v164, s[44:45]
	s_mov_b32 m0, s58
	s_nop 0
	global_load_lds_dwordx4 v168, s[44:45]
	s_waitcnt vmcnt(8)
	s_waitcnt lgkmcnt(0)
	s_barrier
	s_setprio 1
	v_mfma_f32_16x16x128_f8f6f4 v[86:89], v[146:149], v[182:185], v[86:89] cbsz:4 blgp:4
	v_mfma_f32_16x16x128_f8f6f4 v[86:89], v[154:157], v[190:193], v[86:89] cbsz:4 blgp:4
	v_mfma_f32_16x16x128_f8f6f4 v[90:93], v[150:153], v[182:185], v[90:93] cbsz:4 blgp:4
	v_mfma_f32_16x16x128_f8f6f4 v[90:93], v[158:161], v[190:193], v[90:93] cbsz:4 blgp:4
	v_mfma_f32_16x16x128_f8f6f4 v[94:97], v[214:217], v[182:185], v[94:97] cbsz:4 blgp:4
	v_mfma_f32_16x16x128_f8f6f4 v[94:97], v[222:225], v[190:193], v[94:97] cbsz:4 blgp:4
	v_mfma_f32_16x16x128_f8f6f4 v[102:105], v[218:221], v[182:185], v[102:105] cbsz:4 blgp:4
	v_mfma_f32_16x16x128_f8f6f4 v[102:105], v[226:229], v[190:193], v[102:105] cbsz:4 blgp:4
	v_mfma_f32_16x16x128_f8f6f4 v[98:101], v[146:149], v[186:189], v[98:101] cbsz:4 blgp:4
	v_mfma_f32_16x16x128_f8f6f4 v[98:101], v[154:157], v[194:197], v[98:101] cbsz:4 blgp:4
	v_mfma_f32_16x16x128_f8f6f4 v[106:109], v[150:153], v[186:189], v[106:109] cbsz:4 blgp:4
	v_mfma_f32_16x16x128_f8f6f4 v[106:109], v[158:161], v[194:197], v[106:109] cbsz:4 blgp:4
	v_mfma_f32_16x16x128_f8f6f4 v[110:113], v[214:217], v[186:189], v[110:113] cbsz:4 blgp:4
	v_mfma_f32_16x16x128_f8f6f4 v[110:113], v[222:225], v[194:197], v[110:113] cbsz:4 blgp:4
	v_mfma_f32_16x16x128_f8f6f4 v[114:117], v[218:221], v[186:189], v[114:117] cbsz:4 blgp:4
	v_mfma_f32_16x16x128_f8f6f4 v[114:117], v[226:229], v[194:197], v[114:117] cbsz:4 blgp:4
	v_mfma_f32_16x16x128_f8f6f4 v[118:121], v[146:149], v[198:201], v[118:121] cbsz:4 blgp:4
	v_mfma_f32_16x16x128_f8f6f4 v[118:121], v[154:157], v[206:209], v[118:121] cbsz:4 blgp:4
	v_mfma_f32_16x16x128_f8f6f4 v[126:129], v[150:153], v[198:201], v[126:129] cbsz:4 blgp:4
	v_mfma_f32_16x16x128_f8f6f4 v[126:129], v[158:161], v[206:209], v[126:129] cbsz:4 blgp:4
	v_mfma_f32_16x16x128_f8f6f4 v[122:125], v[214:217], v[198:201], v[122:125] cbsz:4 blgp:4
	v_mfma_f32_16x16x128_f8f6f4 v[122:125], v[222:225], v[206:209], v[122:125] cbsz:4 blgp:4
	v_mfma_f32_16x16x128_f8f6f4 v[130:133], v[218:221], v[198:201], v[130:133] cbsz:4 blgp:4
	v_mfma_f32_16x16x128_f8f6f4 v[130:133], v[226:229], v[206:209], v[130:133] cbsz:4 blgp:4
	v_mfma_f32_16x16x128_f8f6f4 v[138:141], v[146:149], v[202:205], v[138:141] cbsz:4 blgp:4
	v_mfma_f32_16x16x128_f8f6f4 v[138:141], v[154:157], v[210:213], v[138:141] cbsz:4 blgp:4
	v_mfma_f32_16x16x128_f8f6f4 v[82:85], v[150:153], v[202:205], v[82:85] cbsz:4 blgp:4
	v_mfma_f32_16x16x128_f8f6f4 v[82:85], v[158:161], v[210:213], v[82:85] cbsz:4 blgp:4
	v_mfma_f32_16x16x128_f8f6f4 v[134:137], v[214:217], v[202:205], v[134:137] cbsz:4 blgp:4
	v_mfma_f32_16x16x128_f8f6f4 v[134:137], v[222:225], v[210:213], v[134:137] cbsz:4 blgp:4
	v_mfma_f32_16x16x128_f8f6f4 v[142:145], v[218:221], v[202:205], v[142:145] cbsz:4 blgp:4
	v_mfma_f32_16x16x128_f8f6f4 v[142:145], v[226:229], v[210:213], v[142:145] cbsz:4 blgp:4
	s_setprio 0
	s_barrier
	ds_read_b128 v[146:149], v169 offset:32768
	ds_read_b128 v[150:153], v169 offset:34816
	ds_read_b128 v[154:157], v178 offset:32768
	ds_read_b128 v[158:161], v178 offset:34816
	ds_read_b128 v[182:185], v179 offset:32768
	ds_read_b128 v[186:189], v179 offset:34816
	ds_read_b128 v[190:193], v180 offset:32768
	ds_read_b128 v[194:197], v180 offset:34816
	ds_read_b128 v[198:201], v179 offset:36864
	ds_read_b128 v[202:205], v179 offset:38912
	ds_read_b128 v[206:209], v180 offset:36864
	ds_read_b128 v[210:213], v180 offset:38912
	s_add_u32 s42, s42, s20
	s_addc_u32 s43, s43, s21
	s_mov_b32 m0, s59
	s_nop 0
	global_load_lds_dwordx4 v162, s[42:43]
	s_mov_b32 m0, s60
	s_nop 0
	global_load_lds_dwordx4 v166, s[42:43]
	s_waitcnt lgkmcnt(8)
	ds_read_b128 v[214:217], v169 offset:49152
	ds_read_b128 v[218:221], v169 offset:51200
	ds_read_b128 v[222:225], v178 offset:49152
	ds_read_b128 v[226:229], v178 offset:51200
	s_waitcnt vmcnt(8)
	s_waitcnt lgkmcnt(0)
	s_barrier
	s_waitcnt lgkmcnt(0)
	s_setprio 1
	v_mfma_f32_16x16x128_f8f6f4 v[18:21], v[146:149], v[182:185], v[18:21] cbsz:4 blgp:4
	v_mfma_f32_16x16x128_f8f6f4 v[18:21], v[154:157], v[190:193], v[18:21] cbsz:4 blgp:4
	v_mfma_f32_16x16x128_f8f6f4 v[22:25], v[150:153], v[182:185], v[22:25] cbsz:4 blgp:4
	v_mfma_f32_16x16x128_f8f6f4 v[22:25], v[158:161], v[190:193], v[22:25] cbsz:4 blgp:4
	v_mfma_f32_16x16x128_f8f6f4 v[50:53], v[214:217], v[182:185], v[50:53] cbsz:4 blgp:4
	v_mfma_f32_16x16x128_f8f6f4 v[50:53], v[222:225], v[190:193], v[50:53] cbsz:4 blgp:4
	v_mfma_f32_16x16x128_f8f6f4 v[54:57], v[218:221], v[182:185], v[54:57] cbsz:4 blgp:4
	v_mfma_f32_16x16x128_f8f6f4 v[54:57], v[226:229], v[190:193], v[54:57] cbsz:4 blgp:4
	v_mfma_f32_16x16x128_f8f6f4 v[26:29], v[146:149], v[186:189], v[26:29] cbsz:4 blgp:4
	v_mfma_f32_16x16x128_f8f6f4 v[26:29], v[154:157], v[194:197], v[26:29] cbsz:4 blgp:4
	v_mfma_f32_16x16x128_f8f6f4 v[30:33], v[150:153], v[186:189], v[30:33] cbsz:4 blgp:4
	v_mfma_f32_16x16x128_f8f6f4 v[30:33], v[158:161], v[194:197], v[30:33] cbsz:4 blgp:4
	v_mfma_f32_16x16x128_f8f6f4 v[58:61], v[214:217], v[186:189], v[58:61] cbsz:4 blgp:4
	v_mfma_f32_16x16x128_f8f6f4 v[58:61], v[222:225], v[194:197], v[58:61] cbsz:4 blgp:4
	v_mfma_f32_16x16x128_f8f6f4 v[62:65], v[218:221], v[186:189], v[62:65] cbsz:4 blgp:4
	v_mfma_f32_16x16x128_f8f6f4 v[62:65], v[226:229], v[194:197], v[62:65] cbsz:4 blgp:4
	v_mfma_f32_16x16x128_f8f6f4 v[34:37], v[146:149], v[198:201], v[34:37] cbsz:4 blgp:4
	v_mfma_f32_16x16x128_f8f6f4 v[34:37], v[154:157], v[206:209], v[34:37] cbsz:4 blgp:4
	v_mfma_f32_16x16x128_f8f6f4 v[38:41], v[150:153], v[198:201], v[38:41] cbsz:4 blgp:4
	v_mfma_f32_16x16x128_f8f6f4 v[38:41], v[158:161], v[206:209], v[38:41] cbsz:4 blgp:4
	v_mfma_f32_16x16x128_f8f6f4 v[66:69], v[214:217], v[198:201], v[66:69] cbsz:4 blgp:4
	v_mfma_f32_16x16x128_f8f6f4 v[66:69], v[222:225], v[206:209], v[66:69] cbsz:4 blgp:4
	v_mfma_f32_16x16x128_f8f6f4 v[70:73], v[218:221], v[198:201], v[70:73] cbsz:4 blgp:4
	v_mfma_f32_16x16x128_f8f6f4 v[70:73], v[226:229], v[206:209], v[70:73] cbsz:4 blgp:4
	v_mfma_f32_16x16x128_f8f6f4 v[42:45], v[146:149], v[202:205], v[42:45] cbsz:4 blgp:4
	v_mfma_f32_16x16x128_f8f6f4 v[42:45], v[154:157], v[210:213], v[42:45] cbsz:4 blgp:4
	v_mfma_f32_16x16x128_f8f6f4 v[46:49], v[150:153], v[202:205], v[46:49] cbsz:4 blgp:4
	v_mfma_f32_16x16x128_f8f6f4 v[46:49], v[158:161], v[210:213], v[46:49] cbsz:4 blgp:4
	v_mfma_f32_16x16x128_f8f6f4 v[74:77], v[214:217], v[202:205], v[74:77] cbsz:4 blgp:4
	v_mfma_f32_16x16x128_f8f6f4 v[74:77], v[222:225], v[210:213], v[74:77] cbsz:4 blgp:4
	v_mfma_f32_16x16x128_f8f6f4 v[78:81], v[218:221], v[202:205], v[78:81] cbsz:4 blgp:4
	v_mfma_f32_16x16x128_f8f6f4 v[78:81], v[226:229], v[210:213], v[78:81] cbsz:4 blgp:4
	s_setprio 0
	s_barrier
	s_mov_b32 m0, s62
	s_nop 0
	global_load_lds_dwordx4 v164, s[36:37]
	s_mov_b32 m0, s63
	s_nop 0
	global_load_lds_dwordx4 v168, s[36:37]
	ds_read_b128 v[182:185], v179 offset:49152
	ds_read_b128 v[186:189], v179 offset:51200
	ds_read_b128 v[190:193], v180 offset:49152
	ds_read_b128 v[194:197], v180 offset:51200
	ds_read_b128 v[198:201], v179 offset:53248
	ds_read_b128 v[202:205], v179 offset:55296
	ds_read_b128 v[206:209], v180 offset:53248
	ds_read_b128 v[210:213], v180 offset:55296
	s_mov_b32 m0, s64
	s_nop 0
	global_load_lds_dwordx4 v162, s[40:41]
	s_mov_b32 m0, s65
	s_nop 0
	global_load_lds_dwordx4 v166, s[40:41]
	s_add_u32 s36, s36, s22
	s_addc_u32 s37, s37, s23
	s_mov_b32 m0, s66
	s_nop 0
	global_load_lds_dwordx4 v164, s[36:37]
	s_mov_b32 m0, s67
	s_nop 0
	global_load_lds_dwordx4 v168, s[36:37]
	s_waitcnt vmcnt(8)
	s_waitcnt lgkmcnt(0)
	s_barrier
	s_setprio 1
	v_mfma_f32_16x16x128_f8f6f4 v[86:89], v[146:149], v[182:185], v[86:89] cbsz:4 blgp:4
	v_mfma_f32_16x16x128_f8f6f4 v[86:89], v[154:157], v[190:193], v[86:89] cbsz:4 blgp:4
	v_mfma_f32_16x16x128_f8f6f4 v[90:93], v[150:153], v[182:185], v[90:93] cbsz:4 blgp:4
	v_mfma_f32_16x16x128_f8f6f4 v[90:93], v[158:161], v[190:193], v[90:93] cbsz:4 blgp:4
	v_mfma_f32_16x16x128_f8f6f4 v[94:97], v[214:217], v[182:185], v[94:97] cbsz:4 blgp:4
	v_mfma_f32_16x16x128_f8f6f4 v[94:97], v[222:225], v[190:193], v[94:97] cbsz:4 blgp:4
	v_mfma_f32_16x16x128_f8f6f4 v[102:105], v[218:221], v[182:185], v[102:105] cbsz:4 blgp:4
	v_mfma_f32_16x16x128_f8f6f4 v[102:105], v[226:229], v[190:193], v[102:105] cbsz:4 blgp:4
	v_mfma_f32_16x16x128_f8f6f4 v[98:101], v[146:149], v[186:189], v[98:101] cbsz:4 blgp:4
	v_mfma_f32_16x16x128_f8f6f4 v[98:101], v[154:157], v[194:197], v[98:101] cbsz:4 blgp:4
	v_mfma_f32_16x16x128_f8f6f4 v[106:109], v[150:153], v[186:189], v[106:109] cbsz:4 blgp:4
	v_mfma_f32_16x16x128_f8f6f4 v[106:109], v[158:161], v[194:197], v[106:109] cbsz:4 blgp:4
	v_mfma_f32_16x16x128_f8f6f4 v[110:113], v[214:217], v[186:189], v[110:113] cbsz:4 blgp:4
	v_mfma_f32_16x16x128_f8f6f4 v[110:113], v[222:225], v[194:197], v[110:113] cbsz:4 blgp:4
	v_mfma_f32_16x16x128_f8f6f4 v[114:117], v[218:221], v[186:189], v[114:117] cbsz:4 blgp:4
	v_mfma_f32_16x16x128_f8f6f4 v[114:117], v[226:229], v[194:197], v[114:117] cbsz:4 blgp:4
	v_mfma_f32_16x16x128_f8f6f4 v[118:121], v[146:149], v[198:201], v[118:121] cbsz:4 blgp:4
	v_mfma_f32_16x16x128_f8f6f4 v[118:121], v[154:157], v[206:209], v[118:121] cbsz:4 blgp:4
	v_mfma_f32_16x16x128_f8f6f4 v[126:129], v[150:153], v[198:201], v[126:129] cbsz:4 blgp:4
	v_mfma_f32_16x16x128_f8f6f4 v[126:129], v[158:161], v[206:209], v[126:129] cbsz:4 blgp:4
	v_mfma_f32_16x16x128_f8f6f4 v[122:125], v[214:217], v[198:201], v[122:125] cbsz:4 blgp:4
	v_mfma_f32_16x16x128_f8f6f4 v[122:125], v[222:225], v[206:209], v[122:125] cbsz:4 blgp:4
	v_mfma_f32_16x16x128_f8f6f4 v[130:133], v[218:221], v[198:201], v[130:133] cbsz:4 blgp:4
	v_mfma_f32_16x16x128_f8f6f4 v[130:133], v[226:229], v[206:209], v[130:133] cbsz:4 blgp:4
	v_mfma_f32_16x16x128_f8f6f4 v[138:141], v[146:149], v[202:205], v[138:141] cbsz:4 blgp:4
	v_mfma_f32_16x16x128_f8f6f4 v[138:141], v[154:157], v[210:213], v[138:141] cbsz:4 blgp:4
	v_mfma_f32_16x16x128_f8f6f4 v[82:85], v[150:153], v[202:205], v[82:85] cbsz:4 blgp:4
	v_mfma_f32_16x16x128_f8f6f4 v[82:85], v[158:161], v[210:213], v[82:85] cbsz:4 blgp:4
	v_mfma_f32_16x16x128_f8f6f4 v[134:137], v[214:217], v[202:205], v[134:137] cbsz:4 blgp:4
	v_mfma_f32_16x16x128_f8f6f4 v[134:137], v[222:225], v[210:213], v[134:137] cbsz:4 blgp:4
	v_mfma_f32_16x16x128_f8f6f4 v[142:145], v[218:221], v[202:205], v[142:145] cbsz:4 blgp:4
	v_mfma_f32_16x16x128_f8f6f4 v[142:145], v[226:229], v[210:213], v[142:145] cbsz:4 blgp:4
	s_setprio 0
	s_add_i32 s36, s82, 2
	s_add_u32 s31, s31, 0x100
	s_addc_u32 s46, s46, 0
	s_add_u32 s47, s47, 0x100
	s_addc_u32 s81, s81, 0
	s_add_u32 s34, s34, 0x100
	s_addc_u32 s35, s35, 0
	s_cmp_ge_i32 s82, s61
	s_barrier
	s_cbranch_scc1 .LBB6_20
	s_mov_b32 s82, s36
	s_cmp_eq_u32 s61, s82
	s_cselect_b64 s[36:37], -1, 0
	s_cmp_lg_u32 s61, s82
	s_cbranch_scc0 .LBB6_17
	s_branch .LBB6_18

amdhsa.kernels:
  - .agpr_count:     0
    .args:
      - .offset:         0
        .size:           80
        .value_kind:     by_value
    .group_segment_fixed_size: 8192
    .kernarg_segment_align: 8
    .kernarg_segment_size: 80
    .language:       OpenCL C
    .language_version:
      - 2
      - 0
    .max_flat_workgroup_size: 256
    .name:           _Z6k_prep8PrepArgs
    .private_segment_fixed_size: 0
    .sgpr_count:     35
    .sgpr_spill_count: 0
    .symbol:         _Z6k_prep8PrepArgs.kd
    .uniform_work_group_size: 1
    .uses_dynamic_stack: false
    .vgpr_count:     45
    .vgpr_spill_count: 0
    .wavefront_size: 64
  - .agpr_count:     4
    .args:
      - .actual_access:  read_only
        .address_space:  global
        .offset:         0
        .size:           8
        .value_kind:     global_buffer
      - .actual_access:  read_only
        .address_space:  global
        .offset:         8
        .size:           8
        .value_kind:     global_buffer
      - .actual_access:  read_only
        .address_space:  global
        .offset:         16
        .size:           8
        .value_kind:     global_buffer
      - .actual_access:  write_only
        .address_space:  global
        .offset:         24
        .size:           8
        .value_kind:     global_buffer
      - .actual_access:  write_only
        .address_space:  global
        .offset:         32
        .size:           8
        .value_kind:     global_buffer
    .group_segment_fixed_size: 36096
    .kernarg_segment_align: 8
    .kernarg_segment_size: 40
    .language:       OpenCL C
    .language_version:
      - 2
      - 0
    .max_flat_workgroup_size: 256
    .name:           _Z7k_gatesPKfPKtS0_PhPf
    .private_segment_fixed_size: 0
    .sgpr_count:     18
    .sgpr_spill_count: 0
    .symbol:         _Z7k_gatesPKfPKtS0_PhPf.kd
    .uniform_work_group_size: 1
    .uses_dynamic_stack: false
    .vgpr_count:     88
    .vgpr_spill_count: 0
    .wavefront_size: 64
  - .agpr_count:     0
    .args:
      - .actual_access:  read_only
        .address_space:  global
        .offset:         0
        .size:           8
        .value_kind:     global_buffer
      - .actual_access:  read_only
        .address_space:  global
        .offset:         8
        .size:           8
        .value_kind:     global_buffer
      - .actual_access:  write_only
        .address_space:  global
        .offset:         16
        .size:           8
        .value_kind:     global_buffer
      - .offset:         24
        .size:           4
        .value_kind:     by_value
    .group_segment_fixed_size: 0
    .kernarg_segment_align: 8
    .kernarg_segment_size: 28
    .language:       OpenCL C
    .language_version:
      - 2
      - 0
    .max_flat_workgroup_size: 256
    .name:           _Z5k_mixPKhPKfPhi
    .private_segment_fixed_size: 0
    .sgpr_count:     14
    .sgpr_spill_count: 0
    .symbol:         _Z5k_mixPKhPKfPhi.kd
    .uniform_work_group_size: 1
    .uses_dynamic_stack: false
    .vgpr_count:     126
    .vgpr_spill_count: 0
    .wavefront_size: 64
  - .agpr_count:     0
    .args:
      - .actual_access:  read_only
        .address_space:  global
        .offset:         0
        .size:           8
        .value_kind:     global_buffer
      - .actual_access:  read_only
        .address_space:  global
        .offset:         8
        .size:           8
        .value_kind:     global_buffer
      - .actual_access:  write_only
        .address_space:  global
        .offset:         16
        .size:           8
        .value_kind:     global_buffer
    .group_segment_fixed_size: 0
    .kernarg_segment_align: 8
    .kernarg_segment_size: 24
    .language:       OpenCL C
    .language_version:
      - 2
      - 0
    .max_flat_workgroup_size: 256
    .name:           _Z7k_finalPKfS0_Pf
    .private_segment_fixed_size: 0
    .sgpr_count:     16
    .sgpr_spill_count: 0
    .symbol:         _Z7k_finalPKfS0_Pf.kd
    .uniform_work_group_size: 1
    .uses_dynamic_stack: false
    .vgpr_count:     16
    .vgpr_spill_count: 0
    .wavefront_size: 64
  - .agpr_count:     0
    .args:
      - .offset:         0
        .size:           24
        .value_kind:     by_value
      - .offset:         24
        .size:           32
        .value_kind:     by_value
      - .offset:         56
        .size:           4
        .value_kind:     by_value
      - .offset:         60
        .size:           4
        .value_kind:     by_value
      - .offset:         64
        .size:           4
        .value_kind:     by_value
      - .offset:         68
        .size:           4
        .value_kind:     by_value
      - .offset:         72
        .size:           4
        .value_kind:     hidden_block_count_x
      - .offset:         76
        .size:           4
        .value_kind:     hidden_block_count_y
      - .offset:         80
        .size:           4
        .value_kind:     hidden_block_count_z
      - .offset:         84
        .size:           2
        .value_kind:     hidden_group_size_x
      - .offset:         86
        .size:           2
        .value_kind:     hidden_group_size_y
      - .offset:         88
        .size:           2
        .value_kind:     hidden_group_size_z
      - .offset:         90
        .size:           2
        .value_kind:     hidden_remainder_x
      - .offset:         92
        .size:           2
        .value_kind:     hidden_remainder_y
      - .offset:         94
        .size:           2
        .value_kind:     hidden_remainder_z
      - .offset:         112
        .size:           8
        .value_kind:     hidden_global_offset_x
      - .offset:         120
        .size:           8
        .value_kind:     hidden_global_offset_y
      - .offset:         128
        .size:           8
        .value_kind:     hidden_global_offset_z
      - .offset:         136
        .size:           2
        .value_kind:     hidden_grid_dims
      - .offset:         192
        .size:           4
        .value_kind:     hidden_dynamic_lds_size
    .group_segment_fixed_size: 0
    .kernarg_segment_align: 8
    .kernarg_segment_size: 328
    .language:       OpenCL C
    .language_version:
      - 2
      - 0
    .max_flat_workgroup_size: 512
    .name:           _Z6k_gemmI4Epi8ILi0ELb1ELb1EEEv4GemmT_iiii
    .private_segment_fixed_size: 0
    .sgpr_count:     92
    .sgpr_spill_count: 0
    .symbol:         _Z6k_gemmI4Epi8ILi0ELb1ELb1EEEv4GemmT_iiii.kd
    .uniform_work_group_size: 1
    .uses_dynamic_stack: false
    .vgpr_count:     248
    .vgpr_spill_count: 0
    .wavefront_size: 64
  - .agpr_count:     0
    .args:
      - .offset:         0
        .size:           24
        .value_kind:     by_value
      - .offset:         24
        .size:           32
        .value_kind:     by_value
      - .offset:         56
        .size:           4
        .value_kind:     by_value
      - .offset:         60
        .size:           4
        .value_kind:     by_value
      - .offset:         64
        .size:           4
        .value_kind:     by_value
      - .offset:         68
        .size:           4
        .value_kind:     by_value
      - .offset:         72
        .size:           4
        .value_kind:     hidden_block_count_x
      - .offset:         76
        .size:           4
        .value_kind:     hidden_block_count_y
      - .offset:         80
        .size:           4
        .value_kind:     hidden_block_count_z
      - .offset:         84
        .size:           2
        .value_kind:     hidden_group_size_x
      - .offset:         86
        .size:           2
        .value_kind:     hidden_group_size_y
      - .offset:         88
        .size:           2
        .value_kind:     hidden_group_size_z
      - .offset:         90
        .size:           2
        .value_kind:     hidden_remainder_x
      - .offset:         92
        .size:           2
        .value_kind:     hidden_remainder_y
      - .offset:         94
        .size:           2
        .value_kind:     hidden_remainder_z
      - .offset:         112
        .size:           8
        .value_kind:     hidden_global_offset_x
      - .offset:         120
        .size:           8
        .value_kind:     hidden_global_offset_y
      - .offset:         128
        .size:           8
        .value_kind:     hidden_global_offset_z
      - .offset:         136
        .size:           2
        .value_kind:     hidden_grid_dims
      - .offset:         192
        .size:           4
        .value_kind:     hidden_dynamic_lds_size
    .group_segment_fixed_size: 0
    .kernarg_segment_align: 8
    .kernarg_segment_size: 328
    .language:       OpenCL C
    .language_version:
      - 2
      - 0
    .max_flat_workgroup_size: 512
    .name:           _Z6k_gemmI4Epi8ILi1ELb1ELb1EEEv4GemmT_iiii
    .private_segment_fixed_size: 0
    .sgpr_count:     90
    .sgpr_spill_count: 0
    .symbol:         _Z6k_gemmI4Epi8ILi1ELb1ELb1EEEv4GemmT_iiii.kd
    .uniform_work_group_size: 1
    .uses_dynamic_stack: false
    .vgpr_count:     228
    .vgpr_spill_count: 0
    .wavefront_size: 64
  - .agpr_count:     0
    .args:
      - .offset:         0
        .size:           24
        .value_kind:     by_value
      - .offset:         24
        .size:           32
        .value_kind:     by_value
      - .offset:         56
        .size:           4
        .value_kind:     by_value
      - .offset:         60
        .size:           4
        .value_kind:     by_value
      - .offset:         64
        .size:           4
        .value_kind:     by_value
      - .offset:         68
        .size:           4
        .value_kind:     by_value
      - .offset:         72
        .size:           4
        .value_kind:     hidden_block_count_x
      - .offset:         76
        .size:           4
        .value_kind:     hidden_block_count_y
      - .offset:         80
        .size:           4
        .value_kind:     hidden_block_count_z
      - .offset:         84
        .size:           2
        .value_kind:     hidden_group_size_x
      - .offset:         86
        .size:           2
        .value_kind:     hidden_group_size_y
      - .offset:         88
        .size:           2
        .value_kind:     hidden_group_size_z
      - .offset:         90
        .size:           2
        .value_kind:     hidden_remainder_x
      - .offset:         92
        .size:           2
        .value_kind:     hidden_remainder_y
      - .offset:         94
        .size:           2
        .value_kind:     hidden_remainder_z
      - .offset:         112
        .size:           8
        .value_kind:     hidden_global_offset_x
      - .offset:         120
        .size:           8
        .value_kind:     hidden_global_offset_y
      - .offset:         128
        .size:           8
        .value_kind:     hidden_global_offset_z
      - .offset:         136
        .size:           2
        .value_kind:     hidden_grid_dims
      - .offset:         192
        .size:           4
        .value_kind:     hidden_dynamic_lds_size
    .group_segment_fixed_size: 0
    .kernarg_segment_align: 8
    .kernarg_segment_size: 328
    .language:       OpenCL C
    .language_version:
      - 2
      - 0
    .max_flat_workgroup_size: 512
    .name:           _Z6k_gemmI8EpiTowerEv4GemmT_iiii
    .private_segment_fixed_size: 0
    .sgpr_count:     92
    .sgpr_spill_count: 0
    .symbol:         _Z6k_gemmI8EpiTowerEv4GemmT_iiii.kd
    .uniform_work_group_size: 1
    .uses_dynamic_stack: false
    .vgpr_count:     230
    .vgpr_spill_count: 0
    .wavefront_size: 64
